# hand-written k-loops (LDS double buffer, interleaved ops, conflict-free layouts) ported to MoE gate/up, MoE down (whole tile) and out-proj GEMMs; second WG per CU staggered 896 cycles in in-proj and o
# speedup vs baseline: 1.0422x; 1.0251x over previous
; #define PR_BEGIN(id) do { if (PROBE_SP == (id)) c.prt = __builtin_amdgcn_s_memrealtime(); } while (0)
; __global__ void __launch_bounds__(NTHR, 2) mk_fwd(Params prm) {
;     ...
;     for (int ph = prm.ph_lo; ph < prm.ph_hi; ++ph) {
;         if (PROBE_SP >= 0) pr_t0 = __builtin_amdgcn_s_memrealtime();
;         asm volatile("" : "+s"(c.p));
;         { int t_ = threadIdx.x; asm volatile("" : "+v"(t_)); c.tid = t_; }
;         if (ph == 0) {
;             const bool split = G >= 384;
;             const int g2 = split ? (bid >= 256 ? gtid - 65536 : 0x3fffffff) : gtid, gth2 = split ? gthreads - 65536 : gthreads;
;             ph_prep(c, g2, gth2, bid, G, (float*)smem_raw); PR_BEGIN(124); cvt_small(c, g2, gth2); PR_END(124); }
;         else if (ph == 1) ph_norm1(c, 0, gw, nwaves, smem_raw);
;         else {
;             const int layer = (ph - 2) / PH_PER_LAYER, sp = (ph - 2) % PH_PER_LAYER;
;             switch (sp) {
;             case 0: for (int t = bid; t < 136 * 18 + (layer == 0 ? 5120 : 0); t += G) { asm volatile("" : "+v"(c.tid)); if (t < 136 * 18) ph_inproj_mfma(c, layer, t, smem_raw); else ph_prepB(c, t - 136 * 18); } break;
;             case 1: for (int t = bid; t < (NT / 32) * 3; t += G) { asm volatile("" : "+v"(c.tid)); asm volatile("" : "+s"(c.p)); MpRegs mpr; mp_load(c, t, mpr); ph_minipost(c, layer, t, -1, mpr, smem_raw); } break;
;             case 2: ph_mix1(c, layer, bid, G, smem_raw, (const volatile unsigned*)smem + 100); break;
;             case 3: for (int t = bid; t < 1088 + 320; t += G) { asm volatile("" : "+v"(c.tid)); asm volatile("" : "+s"(c.p)); if (t < 1088) ssd_s3(c, layer, t, smem_raw); else s5_gemm_y(c, layer, t - 1088, smem_raw); } break;
;             case 4: if (G > 272 + 64) {
;                         if (bid < 272) ph_glu_mfma(c, layer, bid, smem_raw);
;                         else for (int t = bid - 272; t < NT / 32; t += G - 272) { asm volatile("" : "+v"(c.tid)); ph_gates(c, layer, t); }
;                     } else for (int t = bid; t < 136 * 2 + NT / 32; t += G) { asm volatile("" : "+v"(c.tid)); if (t < 136 * 2) ph_glu_mfma(c, layer, t, smem_raw); else ph_gates(c, layer, t - 136 * 2); }
;                     break;
;             case 5: for (int t = bid; t < 136 * 8; t += G) ph_outproj_mfma(c, layer, t, smem_raw); break;
.LBB0_13:
	s_lshr_b32 s6, 0x10884, s66
	s_bitcmp1_b32 s6, 0
	s_cbranch_scc0 .Lstag_done
	ds_read_b32 v2, v146
	s_waitcnt lgkmcnt(0)
	v_readfirstlane_b32 s6, v2
	s_cmp_eq_u32 s6, 0
	s_cbranch_scc1 .Lstag_done
	s_sleep 14

;     const int lane = tid & 63, wid = tid >> 6, wr = wid >> 1, wc = wid & 1, fr = lane & 15, fq = lane >> 4;
; #pragma unroll
;     for (int m = 0; m < 4; ++m)
; #pragma unroll
;         for (int n = 0; n < 4; ++n) acc[m][n] = (f32x4){0.f, 0.f, 0.f, 0.f};
;     unsigned ao[4];
; #pragma unroll
;     for (int i = 0; i < 4; ++i) ao[i] = arow((tid >> 3) + 32 * i) + (tid & 7) * 8;
;     const int bk = tid >> 4, bnc = tid & 15;
;     constexpr int NRB = B_F32 ? 8 : 4;
;     u32x4 ra0[4], ra1[4]; u32x4 rb0[NRB], rb1[NRB];
;     auto gloadA = [&](int kt, u32x4 (&ra)[4]) __attribute__((always_inline)) {
; #pragma unroll
;         for (int i = 0; i < 4; ++i) ra[i] = *(const u32x4*)(Abase + (ao[i] + kt * 64));
;     };
;     auto gloadB = [&](int kt, u32x4 (&rb)[NRB]) __attribute__((always_inline)) {
;         if (B_F32) {
;             const float* bp = (const float*)Bbase + (boff + (unsigned)((kt * 64 + bk) * ldb));
; #pragma unroll
;             for (int i = 0; i < 4; ++i) {
;                 if (bval) { rb[2 * i] = *(const u32x4*)(bp + (unsigned)(16 * i * ldb)); rb[2 * i + 1] = *(const u32x4*)(bp + (unsigned)(16 * i * ldb) + 4); }
;                 else { rb[2 * i] = (u32x4){0u, 0u, 0u, 0u}; rb[2 * i + 1] = rb[2 * i]; }
;             }
;         } else {
; __device__ __forceinline__ void ph_moe2_mfma(const Ctx& c, int layer, int tile, const int* sm, unsigned char* lds) {
;     const int st = tile >> 3, nt = tile & 7;
;     const int s0 = st * 128;
;     if (s0 >= sm[32]) return;
;     const int e = slot_expert(sm, s0), base = s0 - sm[e], ce = sm[33 + e];
;     if (base >= ce) return;
;     {
;         unsigned* flag = c.w<unsigned>(WS_CTL) + CW_MOEF + (layer * 512 + st) * 16;
;         if (c.tid == 0) {
;             unsigned sp = 0u;
;             while (__hip_atomic_load(flag, __ATOMIC_RELAXED, __HIP_MEMORY_SCOPE_AGENT) < 8u) { __builtin_amdgcn_s_sleep(1); if (++sp > (1u << 22)) break; }
;             __builtin_amdgcn_fence(__ATOMIC_ACQUIRE, "agent");
;         }
;         __syncthreads();
;     }
;     const bf16* ACT = c.w<bf16>(WS_ACT) + (size_t)s0 * DE;
;     f32x4 acc[4][4];
;     const int bc = nt * 128 + (c.tid & 15) * 8;
;     gemm_tile<false>(c.tid, lds, ACT, [&](int r) __attribute__((always_inline)) { return (unsigned)(r * DE); }, c.w<bf16>(WS_BDN) + (size_t)e * DE * D, (unsigned)bc, D, true, DE, acc);
.LBB0_152:
	s_or_b64 exec, exec, s[28:29]
	s_waitcnt lgkmcnt(0)
	s_lshl_b64 s[16:17], s[72:73], 10
	s_add_u32 s28, s42, s16
	s_addc_u32 s29, s43, s17
	s_add_u32 s28, s28, 0xb3c6000
	s_addc_u32 s29, s29, 0
	s_lshl_b32 s7, s7, 20
	s_lshl_b32 s6, s59, 8
	s_and_b32 s6, s6, 0x700
	s_add_u32 s44, s42, s7
	s_addc_u32 s45, s43, 0
	s_add_u32 s44, s44, s6
	s_addc_u32 s45, s45, 0
	s_add_u32 s44, s44, 0x1cdd5100
	s_addc_u32 s45, s45, 0
	v_lshrrev_b32_e32 v202, 3, v118
	v_lshlrev_b32_e32 v202, 10, v202
	v_and_b32_e32 v215, 7, v118
	v_lshlrev_b32_e32 v215, 4, v215
	v_or_b32_e32 v202, v202, v215
	v_add_u32_e32 v203, 0x8000, v202
	v_add_u32_e32 v204, 0x10000, v202
	v_add_u32_e32 v205, 0x18000, v202
	v_lshrrev_b32_e32 v206, 4, v118
	v_lshlrev_b32_e32 v206, 11, v206
	v_and_b32_e32 v215, 15, v118
	v_lshlrev_b32_e32 v215, 4, v215
	v_or_b32_e32 v206, v206, v215
	v_add_u32_e32 v207, 0x8000, v206
	v_add_u32_e32 v208, 0x10000, v206
	v_add_u32_e32 v209, 0x18000, v206
	v_bfe_u32 v210, v118, 2, 1
	v_mul_u32_u24_e32 v210, 0x2040, v210
	v_lshrrev_b32_e32 v215, 3, v118
	v_lshlrev_b32_e32 v215, 6, v215
	v_add_u32_e32 v210, v210, v215
	v_and_b32_e32 v215, 3, v118
	v_lshlrev_b32_e32 v215, 4, v215
	v_add_u32_e32 v210, v210, v215
	v_lshrrev_b32_e32 v211, 7, v118
	v_lshlrev_b32_e32 v211, 6, v211
	v_and_b32_e32 v215, 15, v118
	v_or_b32_e32 v211, v211, v215
	v_lshlrev_b32_e32 v211, 6, v211
	v_bfe_u32 v215, v118, 4, 2
	v_lshlrev_b32_e32 v215, 4, v215
	v_or_b32_e32 v211, v211, v215
	v_bfe_u32 v215, v118, 5, 2
	v_sub_u32_e32 v215, 0, v215
	v_and_b32_e32 v215, 3, v215
	v_lshlrev_b32_e32 v215, 4, v215
	v_xor_b32_e32 v210, v210, v215
	v_bfe_u32 v215, v118, 2, 2
	v_sub_u32_e32 v215, 0, v215
	v_and_b32_e32 v215, 3, v215
	v_lshlrev_b32_e32 v215, 4, v215
	v_xor_b32_e32 v211, v211, v215
	v_and_b32_e32 v212, 15, v118
	v_lshlrev_b32_e32 v212, 4, v212
	v_bfe_u32 v215, v118, 7, 1
	v_lshlrev_b32_e32 v215, 7, v215
	v_xor_b32_e32 v212, v212, v215
	v_lshrrev_b32_e32 v215, 4, v118
	v_mul_u32_u24_e32 v215, 0x120, v215
	v_add_u32_e32 v212, v212, v215
	v_add_u32_e32 v213, 0x9000, v212
	v_bfe_u32 v214, v118, 4, 2
	v_lshlrev_b32_e32 v214, 3, v214
	v_bfe_u32 v215, v118, 2, 2
	v_add_u32_e32 v214, v214, v215
	v_mul_u32_u24_e32 v214, 0x120, v214
	v_lshrrev_b32_e32 v215, 6, v118
	v_lshrrev_b32_e32 v216, 4, v118
	v_xor_b32_e32 v215, v215, v216
	v_and_b32_e32 v215, 1, v215
	v_lshlrev_b32_e32 v215, 7, v215
	v_and_b32_e32 v216, 3, v118
	v_lshlrev_b32_e32 v216, 3, v216
	v_or3_b32 v214, v214, v215, v216
	s_barrier
	global_load_dwordx4 v[68:71], v202, s[28:29]
	global_load_dwordx4 v[72:75], v203, s[28:29]
	global_load_dwordx4 v[76:79], v204, s[28:29]
	global_load_dwordx4 v[80:83], v205, s[28:29]
	global_load_dwordx4 v[100:103], v206, s[44:45]
	global_load_dwordx4 v[104:107], v207, s[44:45]
	global_load_dwordx4 v[108:111], v208, s[44:45]
	global_load_dwordx4 v[112:115], v209, s[44:45]
	s_add_u32 s44, s44, 0x20000
	s_addc_u32 s45, s45, 0
	global_load_dwordx4 v[84:87], v202, s[28:29] offset:128
	global_load_dwordx4 v[88:91], v203, s[28:29] offset:128
	global_load_dwordx4 v[92:95], v204, s[28:29] offset:128
	global_load_dwordx4 v[96:99], v205, s[28:29] offset:128
	global_load_dwordx4 v[120:123], v206, s[44:45]
	global_load_dwordx4 v[124:127], v207, s[44:45]
	global_load_dwordx4 v[128:131], v208, s[44:45]
	global_load_dwordx4 v[132:135], v209, s[44:45]
	s_add_u32 s44, s44, 0x20000
	s_addc_u32 s45, s45, 0
	v_mov_b32_e32 v4, 0
	v_mov_b32_e32 v5, 0
	v_mov_b32_e32 v6, 0
	v_mov_b32_e32 v7, 0
	v_mov_b32_e32 v8, 0
	v_mov_b32_e32 v9, 0
	v_mov_b32_e32 v10, 0
	v_mov_b32_e32 v11, 0
	v_mov_b32_e32 v12, 0
	v_mov_b32_e32 v13, 0
	v_mov_b32_e32 v14, 0
	v_mov_b32_e32 v15, 0
	v_mov_b32_e32 v16, 0
	v_mov_b32_e32 v17, 0
	v_mov_b32_e32 v18, 0
	v_mov_b32_e32 v19, 0
	v_mov_b32_e32 v20, 0
	v_mov_b32_e32 v21, 0
	v_mov_b32_e32 v22, 0
	v_mov_b32_e32 v23, 0
	v_mov_b32_e32 v24, 0
	v_mov_b32_e32 v25, 0
	v_mov_b32_e32 v26, 0
	v_mov_b32_e32 v27, 0
	v_mov_b32_e32 v28, 0
	v_mov_b32_e32 v29, 0
	v_mov_b32_e32 v30, 0
	v_mov_b32_e32 v31, 0
	v_mov_b32_e32 v32, 0
	v_mov_b32_e32 v33, 0
	v_mov_b32_e32 v34, 0
	v_mov_b32_e32 v35, 0
	v_mov_b32_e32 v36, 0
	v_mov_b32_e32 v37, 0
	v_mov_b32_e32 v38, 0
	v_mov_b32_e32 v39, 0
	v_mov_b32_e32 v40, 0
	v_mov_b32_e32 v41, 0
	v_mov_b32_e32 v42, 0
	v_mov_b32_e32 v43, 0
	v_mov_b32_e32 v44, 0
	v_mov_b32_e32 v45, 0
	v_mov_b32_e32 v46, 0
	v_mov_b32_e32 v47, 0
	v_mov_b32_e32 v48, 0
	v_mov_b32_e32 v49, 0
	v_mov_b32_e32 v50, 0
	v_mov_b32_e32 v51, 0
	v_mov_b32_e32 v52, 0
	v_mov_b32_e32 v53, 0
	v_mov_b32_e32 v54, 0
	v_mov_b32_e32 v55, 0
	v_mov_b32_e32 v56, 0
	v_mov_b32_e32 v57, 0
	v_mov_b32_e32 v58, 0
	v_mov_b32_e32 v59, 0
	v_mov_b32_e32 v60, 0
	v_mov_b32_e32 v61, 0
	v_mov_b32_e32 v62, 0
	v_mov_b32_e32 v63, 0
	v_mov_b32_e32 v64, 0
	v_mov_b32_e32 v65, 0
	v_mov_b32_e32 v66, 0
	v_mov_b32_e32 v67, 0
	s_mov_b32 s6, 0
	s_waitcnt vmcnt(8)
	s_barrier
	ds_write_b128 v210, v[68:71]
	ds_write_b128 v210, v[72:75] offset:2048
	ds_write_b128 v210, v[76:79] offset:4096
	ds_write_b128 v210, v[80:83] offset:6144
	ds_write_b128 v212, v[100:103] offset:16512
	ds_write_b128 v212, v[104:107] offset:21120
	ds_write_b128 v212, v[108:111] offset:25728
	ds_write_b128 v212, v[112:115] offset:30336
	global_load_dwordx4 v[68:71], v202, s[28:29] offset:256
	global_load_dwordx4 v[72:75], v203, s[28:29] offset:256
	global_load_dwordx4 v[76:79], v204, s[28:29] offset:256
	global_load_dwordx4 v[80:83], v205, s[28:29] offset:256
	global_load_dwordx4 v[100:103], v206, s[44:45]
	global_load_dwordx4 v[104:107], v207, s[44:45]
	global_load_dwordx4 v[108:111], v208, s[44:45]
	global_load_dwordx4 v[112:115], v209, s[44:45]
	s_add_u32 s44, s44, 0x20000
	s_addc_u32 s45, s45, 0
	s_add_u32 s100, s44, 0x20000
	s_addc_u32 s101, s45, 0
	s_waitcnt lgkmcnt(0)
	s_barrier
;     ...
;     auto lstore = [&](const u32x4 (&ra)[4], const u32x4 (&rb)[NRB]) __attribute__((always_inline)) {
; #pragma unroll
;         for (int i = 0; i < 4; ++i) { const int row = (tid >> 3) + 32 * i, kc = tid & 7;
;             const u32x4 v = (kc & 1) ? (u32x4){ra[i][2], ra[i][3], ra[i][0], ra[i][1]} : ra[i];
;             *(u32x4*)(lds + (kc >> 2) * GA_KH + row * 64 + (kc & 3) * 16) = v; }
; #pragma unroll
;         for (int i = 0; i < 4; ++i) { const int k = bk + 16 * i;
;             u32x4 v;
;             if (B_F32) { const f32x4 x = __builtin_bit_cast(f32x4, rb[2 * i]), y = __builtin_bit_cast(f32x4, rb[2 * i + 1]);
;                 v[0] = pk2bf(x[0], x[1]); v[1] = pk2bf(x[2], x[3]); v[2] = pk2bf(y[0], y[1]); v[3] = pk2bf(y[2], y[3]); }
;             else v = rb[i];
;             *(u32x4*)(lds + GB_OFF + k * GB_ST + bnc * 16) = v; }
;     };
;     const lds_cptr la = (lds_cptr)lds + (wr * 64 + fr) * 64 + fq * 16;
;     const lds_cptr lb = (lds_cptr)lds + GB_OFF + (8 * fq + (fr >> 2) + (fq & 1) * 4) * GB_ST + wc * 128 + (fr & 3) * 8;
;     const int bsw = (fq & 1) ? -4 * GB_ST : 4 * GB_ST;
;     auto compute = [&]() __attribute__((always_inline)) {
; #pragma unroll
;         for (int kh = 0; kh < 2; ++kh) {
;             bf16x8 af[4], bfr[4];
; #pragma unroll
;             for (int m = 0; m < 4; ++m) af[m] = *(const LAS bf16x8*)(la + kh * GA_KH + m * 1024);
; #pragma unroll
;             for (int n = 0; n < 4; ++n) {
;                 const s16x4 r0 = lds_tr(lb + kh * 32 * GB_ST + n * 32), r1 = lds_tr(lb + kh * 32 * GB_ST + n * 32 + bsw);
;                 bfr[n] = (bf16x8){r0[0], r0[1], r0[2], r0[3], r1[0], r1[1], r1[2], r1[3]};
;             }
; #pragma unroll
;             for (int m = 0; m < 4; ++m)
; #pragma unroll
;                 for (int n = 0; n < 4; ++n) acc[m][n] = __builtin_amdgcn_mfma_f32_16x16x32_bf16(bfr[n], af[m], acc[m][n], 0, 0, 0);
;         }
;     };
;     ...
;     gloadB(0, rb0); gloadA(0, ra0); gloadB(1, rb1);
;     for (int kt = 0; kt < nk; kt += 2) {
;         __syncthreads();
;         lstore(ra0, rb0);
;         __syncthreads();
;         gloadA(kt + 1, ra0);
;         if (kt + 2 < nk) gloadB(kt + 2, rb0);
;         compute();
;         __syncthreads();
;         lstore(ra0, rb1);
;         __syncthreads();
;         if (kt + 2 < nk) gloadA(kt + 2, ra0);
;         if (kt + 3 < nk) gloadB(kt + 3, rb1);
;         compute();
;     }
.Lm2_loop:
	ds_read_b64_tr_b16 v[166:167], v214 offset:16512
	ds_read_b64_tr_b16 v[168:169], v214 offset:17664
	ds_read_b128 v[136:139], v211
	ds_read_b64_tr_b16 v[170:171], v214 offset:16544
	ds_read_b64_tr_b16 v[172:173], v214 offset:17696
	s_waitcnt lgkmcnt(2)
	v_mfma_f32_16x16x32_bf16 v[4:7], v[166:169], v[136:139], v[4:7]
	ds_read_b64_tr_b16 v[174:175], v214 offset:16576
	ds_read_b64_tr_b16 v[176:177], v214 offset:17728
	s_waitcnt lgkmcnt(2)
	v_mfma_f32_16x16x32_bf16 v[8:11], v[170:173], v[136:139], v[8:11]
	ds_read_b64_tr_b16 v[178:179], v214 offset:16608
	ds_read_b64_tr_b16 v[180:181], v214 offset:17760
	s_waitcnt lgkmcnt(2)
	v_mfma_f32_16x16x32_bf16 v[12:15], v[174:177], v[136:139], v[12:15]
	ds_read_b128 v[140:143], v211 offset:1024
	s_waitcnt lgkmcnt(1)
	v_mfma_f32_16x16x32_bf16 v[16:19], v[178:181], v[136:139], v[16:19]
	ds_read_b128 v[158:161], v211 offset:2048
	s_waitcnt lgkmcnt(1)
	v_mfma_f32_16x16x32_bf16 v[20:23], v[166:169], v[140:143], v[20:23]
	ds_read_b128 v[162:165], v211 offset:3072
	v_mfma_f32_16x16x32_bf16 v[24:27], v[170:173], v[140:143], v[24:27]
	ds_read_b64_tr_b16 v[182:183], v214 offset:25728
	ds_read_b64_tr_b16 v[184:185], v214 offset:26880
	v_mfma_f32_16x16x32_bf16 v[28:31], v[174:177], v[140:143], v[28:31]
	ds_read_b64_tr_b16 v[186:187], v214 offset:25760
	ds_read_b64_tr_b16 v[188:189], v214 offset:26912
	v_mfma_f32_16x16x32_bf16 v[32:35], v[178:181], v[140:143], v[32:35]
	ds_read_b128 v[136:139], v211 offset:8256
	s_waitcnt lgkmcnt(6)
	v_mfma_f32_16x16x32_bf16 v[36:39], v[166:169], v[158:161], v[36:39]
	ds_read_b64_tr_b16 v[190:191], v214 offset:25792
	ds_read_b64_tr_b16 v[192:193], v214 offset:26944
	v_mfma_f32_16x16x32_bf16 v[40:43], v[170:173], v[158:161], v[40:43]
	ds_read_b64_tr_b16 v[198:199], v214 offset:25824
	ds_read_b64_tr_b16 v[200:201], v214 offset:26976
	v_mfma_f32_16x16x32_bf16 v[44:47], v[174:177], v[158:161], v[44:47]
	s_waitcnt vmcnt(8)
	ds_write_b128 v210, v[84:87] offset:36864
	v_mfma_f32_16x16x32_bf16 v[48:51], v[178:181], v[158:161], v[48:51]
	ds_read_b128 v[140:143], v211 offset:9280
	s_waitcnt lgkmcnt(11)
	v_mfma_f32_16x16x32_bf16 v[52:55], v[166:169], v[162:165], v[52:55]
	ds_write_b128 v210, v[88:91] offset:38912
	v_mfma_f32_16x16x32_bf16 v[56:59], v[170:173], v[162:165], v[56:59]
	ds_write_b128 v210, v[92:95] offset:40960
	v_mfma_f32_16x16x32_bf16 v[60:63], v[174:177], v[162:165], v[60:63]
	ds_write_b128 v210, v[96:99] offset:43008
	v_mfma_f32_16x16x32_bf16 v[64:67], v[178:181], v[162:165], v[64:67]
	s_waitcnt lgkmcnt(10)
	ds_read_b128 v[158:161], v211 offset:10304
	s_waitcnt lgkmcnt(10)
	v_mfma_f32_16x16x32_bf16 v[4:7], v[182:185], v[136:139], v[4:7]
	ds_write_b128 v213, v[120:123] offset:16512
	v_mfma_f32_16x16x32_bf16 v[8:11], v[186:189], v[136:139], v[8:11]
	ds_write_b128 v213, v[124:127] offset:21120
	s_waitcnt lgkmcnt(10)
	v_mfma_f32_16x16x32_bf16 v[12:15], v[190:193], v[136:139], v[12:15]
	ds_write_b128 v213, v[128:131] offset:25728
	s_waitcnt lgkmcnt(9)
	v_mfma_f32_16x16x32_bf16 v[16:19], v[198:201], v[136:139], v[16:19]
	ds_read_b128 v[162:165], v211 offset:11328
	s_waitcnt lgkmcnt(8)
	v_mfma_f32_16x16x32_bf16 v[20:23], v[182:185], v[140:143], v[20:23]
	ds_write_b128 v213, v[132:135] offset:30336
	v_mfma_f32_16x16x32_bf16 v[24:27], v[186:189], v[140:143], v[24:27]
	global_load_dwordx4 v[84:87], v202, s[28:29] offset:384
	v_mfma_f32_16x16x32_bf16 v[28:31], v[190:193], v[140:143], v[28:31]
	global_load_dwordx4 v[88:91], v203, s[28:29] offset:384
	v_mfma_f32_16x16x32_bf16 v[32:35], v[198:201], v[140:143], v[32:35]
	global_load_dwordx4 v[92:95], v204, s[28:29] offset:384
	s_waitcnt lgkmcnt(5)
	v_mfma_f32_16x16x32_bf16 v[36:39], v[182:185], v[158:161], v[36:39]
	global_load_dwordx4 v[96:99], v205, s[28:29] offset:384
	v_mfma_f32_16x16x32_bf16 v[40:43], v[186:189], v[158:161], v[40:43]
	global_load_dwordx4 v[120:123], v206, s[44:45]
	v_mfma_f32_16x16x32_bf16 v[44:47], v[190:193], v[158:161], v[44:47]
	global_load_dwordx4 v[124:127], v207, s[44:45]
	v_mfma_f32_16x16x32_bf16 v[48:51], v[198:201], v[158:161], v[48:51]
	global_load_dwordx4 v[128:131], v208, s[44:45]
	s_waitcnt lgkmcnt(1)
	v_mfma_f32_16x16x32_bf16 v[52:55], v[182:185], v[162:165], v[52:55]
	global_load_dwordx4 v[132:135], v209, s[44:45]
	v_mfma_f32_16x16x32_bf16 v[56:59], v[186:189], v[162:165], v[56:59]
	v_mfma_f32_16x16x32_bf16 v[60:63], v[190:193], v[162:165], v[60:63]
	v_mfma_f32_16x16x32_bf16 v[64:67], v[198:201], v[162:165], v[64:67]
	s_waitcnt lgkmcnt(0)
	s_barrier
	s_cmp_lt_u32 s6, 4
	s_cbranch_scc0 .Lm2_h1_last
;     ...
;     auto lstore = [&](const u32x4 (&ra)[4], const u32x4 (&rb)[NRB]) __attribute__((always_inline)) {
; #pragma unroll
;         for (int i = 0; i < 4; ++i) { const int row = (tid >> 3) + 32 * i, kc = tid & 7;
;             const u32x4 v = (kc & 1) ? (u32x4){ra[i][2], ra[i][3], ra[i][0], ra[i][1]} : ra[i];
;             *(u32x4*)(lds + (kc >> 2) * GA_KH + row * 64 + (kc & 3) * 16) = v; }
; #pragma unroll
;         for (int i = 0; i < 4; ++i) { const int k = bk + 16 * i;
;             u32x4 v;
;             if (B_F32) { const f32x4 x = __builtin_bit_cast(f32x4, rb[2 * i]), y = __builtin_bit_cast(f32x4, rb[2 * i + 1]);
;                 v[0] = pk2bf(x[0], x[1]); v[1] = pk2bf(x[2], x[3]); v[2] = pk2bf(y[0], y[1]); v[3] = pk2bf(y[2], y[3]); }
;             else v = rb[i];
;             *(u32x4*)(lds + GB_OFF + k * GB_ST + bnc * 16) = v; }
;     };
;     const lds_cptr la = (lds_cptr)lds + (wr * 64 + fr) * 64 + fq * 16;
;     const lds_cptr lb = (lds_cptr)lds + GB_OFF + (8 * fq + (fr >> 2) + (fq & 1) * 4) * GB_ST + wc * 128 + (fr & 3) * 8;
;     const int bsw = (fq & 1) ? -4 * GB_ST : 4 * GB_ST;
;     auto compute = [&]() __attribute__((always_inline)) {
; #pragma unroll
;         for (int kh = 0; kh < 2; ++kh) {
;             bf16x8 af[4], bfr[4];
; #pragma unroll
;             for (int m = 0; m < 4; ++m) af[m] = *(const LAS bf16x8*)(la + kh * GA_KH + m * 1024);
; #pragma unroll
;             for (int n = 0; n < 4; ++n) {
;                 const s16x4 r0 = lds_tr(lb + kh * 32 * GB_ST + n * 32), r1 = lds_tr(lb + kh * 32 * GB_ST + n * 32 + bsw);
;                 bfr[n] = (bf16x8){r0[0], r0[1], r0[2], r0[3], r1[0], r1[1], r1[2], r1[3]};
;             }
; #pragma unroll
;             for (int m = 0; m < 4; ++m)
; #pragma unroll
;                 for (int n = 0; n < 4; ++n) acc[m][n] = __builtin_amdgcn_mfma_f32_16x16x32_bf16(bfr[n], af[m], acc[m][n], 0, 0, 0);
;         }
;     };
;     ...
;     gloadB(0, rb0); gloadA(0, ra0); gloadB(1, rb1);
;     for (int kt = 0; kt < nk; kt += 2) {
;         __syncthreads();
;         lstore(ra0, rb0);
;         __syncthreads();
;         gloadA(kt + 1, ra0);
;         if (kt + 2 < nk) gloadB(kt + 2, rb0);
;         compute();
;         __syncthreads();
;         lstore(ra0, rb1);
;         __syncthreads();
;         if (kt + 2 < nk) gloadA(kt + 2, ra0);
;         if (kt + 3 < nk) gloadB(kt + 3, rb1);
;         compute();
;     }
	ds_read_b64_tr_b16 v[166:167], v214 offset:53376
	ds_read_b64_tr_b16 v[168:169], v214 offset:54528
	ds_read_b128 v[136:139], v211 offset:36864
	ds_read_b64_tr_b16 v[170:171], v214 offset:53408
	ds_read_b64_tr_b16 v[172:173], v214 offset:54560
	s_waitcnt lgkmcnt(2)
	v_mfma_f32_16x16x32_bf16 v[4:7], v[166:169], v[136:139], v[4:7]
	ds_read_b64_tr_b16 v[174:175], v214 offset:53440
	ds_read_b64_tr_b16 v[176:177], v214 offset:54592
	s_waitcnt lgkmcnt(2)
	v_mfma_f32_16x16x32_bf16 v[8:11], v[170:173], v[136:139], v[8:11]
	ds_read_b64_tr_b16 v[178:179], v214 offset:53472
	ds_read_b64_tr_b16 v[180:181], v214 offset:54624
	s_waitcnt lgkmcnt(2)
	v_mfma_f32_16x16x32_bf16 v[12:15], v[174:177], v[136:139], v[12:15]
	ds_read_b128 v[140:143], v211 offset:37888
	s_waitcnt lgkmcnt(1)
	v_mfma_f32_16x16x32_bf16 v[16:19], v[178:181], v[136:139], v[16:19]
	ds_read_b128 v[158:161], v211 offset:38912
	s_waitcnt lgkmcnt(1)
	v_mfma_f32_16x16x32_bf16 v[20:23], v[166:169], v[140:143], v[20:23]
	ds_read_b128 v[162:165], v211 offset:39936
	v_mfma_f32_16x16x32_bf16 v[24:27], v[170:173], v[140:143], v[24:27]
	ds_read_b64_tr_b16 v[182:183], v214 offset:62592
	ds_read_b64_tr_b16 v[184:185], v214 offset:63744
	v_mfma_f32_16x16x32_bf16 v[28:31], v[174:177], v[140:143], v[28:31]
	ds_read_b64_tr_b16 v[186:187], v214 offset:62624
	ds_read_b64_tr_b16 v[188:189], v214 offset:63776
	v_mfma_f32_16x16x32_bf16 v[32:35], v[178:181], v[140:143], v[32:35]
	ds_read_b128 v[136:139], v211 offset:45120
	s_waitcnt lgkmcnt(6)
	v_mfma_f32_16x16x32_bf16 v[36:39], v[166:169], v[158:161], v[36:39]
	ds_read_b64_tr_b16 v[190:191], v214 offset:62656
	ds_read_b64_tr_b16 v[192:193], v214 offset:63808
	v_mfma_f32_16x16x32_bf16 v[40:43], v[170:173], v[158:161], v[40:43]
	ds_read_b64_tr_b16 v[198:199], v214 offset:62688
	ds_read_b64_tr_b16 v[200:201], v214 offset:63840
	v_mfma_f32_16x16x32_bf16 v[44:47], v[174:177], v[158:161], v[44:47]
	s_waitcnt vmcnt(8)
	ds_write_b128 v210, v[68:71]
	v_mfma_f32_16x16x32_bf16 v[48:51], v[178:181], v[158:161], v[48:51]
	ds_read_b128 v[140:143], v211 offset:46144
	s_waitcnt lgkmcnt(11)
	v_mfma_f32_16x16x32_bf16 v[52:55], v[166:169], v[162:165], v[52:55]
	ds_write_b128 v210, v[72:75] offset:2048
	v_mfma_f32_16x16x32_bf16 v[56:59], v[170:173], v[162:165], v[56:59]
	ds_write_b128 v210, v[76:79] offset:4096
	v_mfma_f32_16x16x32_bf16 v[60:63], v[174:177], v[162:165], v[60:63]
	ds_write_b128 v210, v[80:83] offset:6144
	v_mfma_f32_16x16x32_bf16 v[64:67], v[178:181], v[162:165], v[64:67]
	s_waitcnt lgkmcnt(10)
	ds_read_b128 v[158:161], v211 offset:47168
	s_waitcnt lgkmcnt(10)
	v_mfma_f32_16x16x32_bf16 v[4:7], v[182:185], v[136:139], v[4:7]
	ds_write_b128 v212, v[100:103] offset:16512
	v_mfma_f32_16x16x32_bf16 v[8:11], v[186:189], v[136:139], v[8:11]
	ds_write_b128 v212, v[104:107] offset:21120
	s_waitcnt lgkmcnt(10)
	v_mfma_f32_16x16x32_bf16 v[12:15], v[190:193], v[136:139], v[12:15]
	ds_write_b128 v212, v[108:111] offset:25728
	s_waitcnt lgkmcnt(9)
	v_mfma_f32_16x16x32_bf16 v[16:19], v[198:201], v[136:139], v[16:19]
	ds_read_b128 v[162:165], v211 offset:48192
	s_waitcnt lgkmcnt(8)
	v_mfma_f32_16x16x32_bf16 v[20:23], v[182:185], v[140:143], v[20:23]
	ds_write_b128 v212, v[112:115] offset:30336
	v_mfma_f32_16x16x32_bf16 v[24:27], v[186:189], v[140:143], v[24:27]
	global_load_dwordx4 v[68:71], v202, s[28:29] offset:512
	v_mfma_f32_16x16x32_bf16 v[28:31], v[190:193], v[140:143], v[28:31]
	global_load_dwordx4 v[72:75], v203, s[28:29] offset:512
	v_mfma_f32_16x16x32_bf16 v[32:35], v[198:201], v[140:143], v[32:35]
	global_load_dwordx4 v[76:79], v204, s[28:29] offset:512
	s_waitcnt lgkmcnt(5)
	v_mfma_f32_16x16x32_bf16 v[36:39], v[182:185], v[158:161], v[36:39]
	global_load_dwordx4 v[80:83], v205, s[28:29] offset:512
	v_mfma_f32_16x16x32_bf16 v[40:43], v[186:189], v[158:161], v[40:43]
	global_load_dwordx4 v[100:103], v206, s[100:101]
	v_mfma_f32_16x16x32_bf16 v[44:47], v[190:193], v[158:161], v[44:47]
	global_load_dwordx4 v[104:107], v207, s[100:101]
	v_mfma_f32_16x16x32_bf16 v[48:51], v[198:201], v[158:161], v[48:51]
	global_load_dwordx4 v[108:111], v208, s[100:101]
	s_waitcnt lgkmcnt(1)
	v_mfma_f32_16x16x32_bf16 v[52:55], v[182:185], v[162:165], v[52:55]
	global_load_dwordx4 v[112:115], v209, s[100:101]
	v_mfma_f32_16x16x32_bf16 v[56:59], v[186:189], v[162:165], v[56:59]
	v_mfma_f32_16x16x32_bf16 v[60:63], v[190:193], v[162:165], v[60:63]
	v_mfma_f32_16x16x32_bf16 v[64:67], v[198:201], v[162:165], v[64:67]
	s_waitcnt lgkmcnt(0)
	s_barrier
	s_add_u32 s28, s28, 0x100
	s_addc_u32 s29, s29, 0
	s_add_u32 s44, s44, 0x40000
	s_addc_u32 s45, s45, 0
	s_add_u32 s100, s100, 0x40000
	s_addc_u32 s101, s101, 0
	s_add_i32 s6, s6, 2
	s_branch .Lm2_loop
;     ...
;     auto lstore = [&](const u32x4 (&ra)[4], const u32x4 (&rb)[NRB]) __attribute__((always_inline)) {
; #pragma unroll
;         for (int i = 0; i < 4; ++i) { const int row = (tid >> 3) + 32 * i, kc = tid & 7;
;             const u32x4 v = (kc & 1) ? (u32x4){ra[i][2], ra[i][3], ra[i][0], ra[i][1]} : ra[i];
;             *(u32x4*)(lds + (kc >> 2) * GA_KH + row * 64 + (kc & 3) * 16) = v; }
; #pragma unroll
;         for (int i = 0; i < 4; ++i) { const int k = bk + 16 * i;
;             u32x4 v;
;             if (B_F32) { const f32x4 x = __builtin_bit_cast(f32x4, rb[2 * i]), y = __builtin_bit_cast(f32x4, rb[2 * i + 1]);
;                 v[0] = pk2bf(x[0], x[1]); v[1] = pk2bf(x[2], x[3]); v[2] = pk2bf(y[0], y[1]); v[3] = pk2bf(y[2], y[3]); }
;             else v = rb[i];
;             *(u32x4*)(lds + GB_OFF + k * GB_ST + bnc * 16) = v; }
;     };
;     const lds_cptr la = (lds_cptr)lds + (wr * 64 + fr) * 64 + fq * 16;
;     const lds_cptr lb = (lds_cptr)lds + GB_OFF + (8 * fq + (fr >> 2) + (fq & 1) * 4) * GB_ST + wc * 128 + (fr & 3) * 8;
;     const int bsw = (fq & 1) ? -4 * GB_ST : 4 * GB_ST;
;     auto compute = [&]() __attribute__((always_inline)) {
; #pragma unroll
;         for (int kh = 0; kh < 2; ++kh) {
;             bf16x8 af[4], bfr[4];
; #pragma unroll
;             for (int m = 0; m < 4; ++m) af[m] = *(const LAS bf16x8*)(la + kh * GA_KH + m * 1024);
; #pragma unroll
;             for (int n = 0; n < 4; ++n) {
;                 const s16x4 r0 = lds_tr(lb + kh * 32 * GB_ST + n * 32), r1 = lds_tr(lb + kh * 32 * GB_ST + n * 32 + bsw);
;                 bfr[n] = (bf16x8){r0[0], r0[1], r0[2], r0[3], r1[0], r1[1], r1[2], r1[3]};
;             }
; #pragma unroll
;             for (int m = 0; m < 4; ++m)
; #pragma unroll
;                 for (int n = 0; n < 4; ++n) acc[m][n] = __builtin_amdgcn_mfma_f32_16x16x32_bf16(bfr[n], af[m], acc[m][n], 0, 0, 0);
;         }
;     };
;     ...
;     gloadB(0, rb0); gloadA(0, ra0); gloadB(1, rb1);
;     for (int kt = 0; kt < nk; kt += 2) {
;         __syncthreads();
;         lstore(ra0, rb0);
;         __syncthreads();
;         gloadA(kt + 1, ra0);
;         if (kt + 2 < nk) gloadB(kt + 2, rb0);
;         compute();
;         __syncthreads();
;         lstore(ra0, rb1);
;         __syncthreads();
;         if (kt + 2 < nk) gloadA(kt + 2, ra0);
;         if (kt + 3 < nk) gloadB(kt + 3, rb1);
;         compute();
;     }
.Lm2_h1_last:
	ds_read_b64_tr_b16 v[166:167], v214 offset:53376
	ds_read_b64_tr_b16 v[168:169], v214 offset:54528
	ds_read_b128 v[136:139], v211 offset:36864
	ds_read_b64_tr_b16 v[170:171], v214 offset:53408
	ds_read_b64_tr_b16 v[172:173], v214 offset:54560
	s_waitcnt lgkmcnt(2)
	v_mfma_f32_16x16x32_bf16 v[4:7], v[166:169], v[136:139], v[4:7]
	ds_read_b64_tr_b16 v[174:175], v214 offset:53440
	ds_read_b64_tr_b16 v[176:177], v214 offset:54592
	s_waitcnt lgkmcnt(2)
	v_mfma_f32_16x16x32_bf16 v[8:11], v[170:173], v[136:139], v[8:11]
	ds_read_b64_tr_b16 v[178:179], v214 offset:53472
	ds_read_b64_tr_b16 v[180:181], v214 offset:54624
	s_waitcnt lgkmcnt(2)
	v_mfma_f32_16x16x32_bf16 v[12:15], v[174:177], v[136:139], v[12:15]
	ds_read_b128 v[140:143], v211 offset:37888
	s_waitcnt lgkmcnt(1)
	v_mfma_f32_16x16x32_bf16 v[16:19], v[178:181], v[136:139], v[16:19]
	ds_read_b128 v[158:161], v211 offset:38912
	s_waitcnt lgkmcnt(1)
	v_mfma_f32_16x16x32_bf16 v[20:23], v[166:169], v[140:143], v[20:23]
	ds_read_b128 v[162:165], v211 offset:39936
	v_mfma_f32_16x16x32_bf16 v[24:27], v[170:173], v[140:143], v[24:27]
	ds_read_b64_tr_b16 v[182:183], v214 offset:62592
	ds_read_b64_tr_b16 v[184:185], v214 offset:63744
	v_mfma_f32_16x16x32_bf16 v[28:31], v[174:177], v[140:143], v[28:31]
	ds_read_b64_tr_b16 v[186:187], v214 offset:62624
	ds_read_b64_tr_b16 v[188:189], v214 offset:63776
	v_mfma_f32_16x16x32_bf16 v[32:35], v[178:181], v[140:143], v[32:35]
	ds_read_b128 v[136:139], v211 offset:45120
	s_waitcnt lgkmcnt(6)
	v_mfma_f32_16x16x32_bf16 v[36:39], v[166:169], v[158:161], v[36:39]
	ds_read_b64_tr_b16 v[190:191], v214 offset:62656
	ds_read_b64_tr_b16 v[192:193], v214 offset:63808
	v_mfma_f32_16x16x32_bf16 v[40:43], v[170:173], v[158:161], v[40:43]
	ds_read_b64_tr_b16 v[198:199], v214 offset:62688
	ds_read_b64_tr_b16 v[200:201], v214 offset:63840
	v_mfma_f32_16x16x32_bf16 v[44:47], v[174:177], v[158:161], v[44:47]
	s_waitcnt vmcnt(8)
	ds_write_b128 v210, v[68:71]
	v_mfma_f32_16x16x32_bf16 v[48:51], v[178:181], v[158:161], v[48:51]
	ds_read_b128 v[140:143], v211 offset:46144
	s_waitcnt lgkmcnt(11)
	v_mfma_f32_16x16x32_bf16 v[52:55], v[166:169], v[162:165], v[52:55]
	ds_write_b128 v210, v[72:75] offset:2048
	v_mfma_f32_16x16x32_bf16 v[56:59], v[170:173], v[162:165], v[56:59]
	ds_write_b128 v210, v[76:79] offset:4096
	v_mfma_f32_16x16x32_bf16 v[60:63], v[174:177], v[162:165], v[60:63]
	ds_write_b128 v210, v[80:83] offset:6144
	v_mfma_f32_16x16x32_bf16 v[64:67], v[178:181], v[162:165], v[64:67]
	s_waitcnt lgkmcnt(10)
	ds_read_b128 v[158:161], v211 offset:47168
	s_waitcnt lgkmcnt(10)
	v_mfma_f32_16x16x32_bf16 v[4:7], v[182:185], v[136:139], v[4:7]
	ds_write_b128 v212, v[100:103] offset:16512
	v_mfma_f32_16x16x32_bf16 v[8:11], v[186:189], v[136:139], v[8:11]
	ds_write_b128 v212, v[104:107] offset:21120
	s_waitcnt lgkmcnt(10)
	v_mfma_f32_16x16x32_bf16 v[12:15], v[190:193], v[136:139], v[12:15]
	ds_write_b128 v212, v[108:111] offset:25728
	s_waitcnt lgkmcnt(9)
	v_mfma_f32_16x16x32_bf16 v[16:19], v[198:201], v[136:139], v[16:19]
	ds_read_b128 v[162:165], v211 offset:48192
	s_waitcnt lgkmcnt(8)
	v_mfma_f32_16x16x32_bf16 v[20:23], v[182:185], v[140:143], v[20:23]
	ds_write_b128 v212, v[112:115] offset:30336
	v_mfma_f32_16x16x32_bf16 v[24:27], v[186:189], v[140:143], v[24:27]
	v_mfma_f32_16x16x32_bf16 v[28:31], v[190:193], v[140:143], v[28:31]
	v_mfma_f32_16x16x32_bf16 v[32:35], v[198:201], v[140:143], v[32:35]
	s_waitcnt lgkmcnt(5)
	v_mfma_f32_16x16x32_bf16 v[36:39], v[182:185], v[158:161], v[36:39]
	v_mfma_f32_16x16x32_bf16 v[40:43], v[186:189], v[158:161], v[40:43]
	v_mfma_f32_16x16x32_bf16 v[44:47], v[190:193], v[158:161], v[44:47]
	v_mfma_f32_16x16x32_bf16 v[48:51], v[198:201], v[158:161], v[48:51]
	s_waitcnt lgkmcnt(1)
	v_mfma_f32_16x16x32_bf16 v[52:55], v[182:185], v[162:165], v[52:55]
	v_mfma_f32_16x16x32_bf16 v[56:59], v[186:189], v[162:165], v[56:59]
	v_mfma_f32_16x16x32_bf16 v[60:63], v[190:193], v[162:165], v[60:63]
	v_mfma_f32_16x16x32_bf16 v[64:67], v[198:201], v[162:165], v[64:67]
	s_waitcnt lgkmcnt(0)
	s_barrier
	ds_read_b64_tr_b16 v[166:167], v214 offset:16512
	ds_read_b64_tr_b16 v[168:169], v214 offset:17664
	ds_read_b128 v[136:139], v211
	ds_read_b64_tr_b16 v[170:171], v214 offset:16544
	ds_read_b64_tr_b16 v[172:173], v214 offset:17696
	s_waitcnt lgkmcnt(2)
	v_mfma_f32_16x16x32_bf16 v[4:7], v[166:169], v[136:139], v[4:7]
	ds_read_b64_tr_b16 v[174:175], v214 offset:16576
	ds_read_b64_tr_b16 v[176:177], v214 offset:17728
	s_waitcnt lgkmcnt(2)
	v_mfma_f32_16x16x32_bf16 v[8:11], v[170:173], v[136:139], v[8:11]
	ds_read_b64_tr_b16 v[178:179], v214 offset:16608
	ds_read_b64_tr_b16 v[180:181], v214 offset:17760
	s_waitcnt lgkmcnt(2)
	v_mfma_f32_16x16x32_bf16 v[12:15], v[174:177], v[136:139], v[12:15]
	ds_read_b128 v[140:143], v211 offset:1024
	s_waitcnt lgkmcnt(1)
	v_mfma_f32_16x16x32_bf16 v[16:19], v[178:181], v[136:139], v[16:19]
	ds_read_b128 v[158:161], v211 offset:2048
	s_waitcnt lgkmcnt(1)
	v_mfma_f32_16x16x32_bf16 v[20:23], v[166:169], v[140:143], v[20:23]
	ds_read_b128 v[162:165], v211 offset:3072
	v_mfma_f32_16x16x32_bf16 v[24:27], v[170:173], v[140:143], v[24:27]
	ds_read_b64_tr_b16 v[182:183], v214 offset:25728
	ds_read_b64_tr_b16 v[184:185], v214 offset:26880
	v_mfma_f32_16x16x32_bf16 v[28:31], v[174:177], v[140:143], v[28:31]
	ds_read_b64_tr_b16 v[186:187], v214 offset:25760
	ds_read_b64_tr_b16 v[188:189], v214 offset:26912
	v_mfma_f32_16x16x32_bf16 v[32:35], v[178:181], v[140:143], v[32:35]
	ds_read_b128 v[136:139], v211 offset:8256
	s_waitcnt lgkmcnt(6)
;     ...
;     auto lstore = [&](const u32x4 (&ra)[4], const u32x4 (&rb)[NRB]) __attribute__((always_inline)) {
; #pragma unroll
;         for (int i = 0; i < 4; ++i) { const int row = (tid >> 3) + 32 * i, kc = tid & 7;
;             const u32x4 v = (kc & 1) ? (u32x4){ra[i][2], ra[i][3], ra[i][0], ra[i][1]} : ra[i];
;             *(u32x4*)(lds + (kc >> 2) * GA_KH + row * 64 + (kc & 3) * 16) = v; }
; #pragma unroll
;         for (int i = 0; i < 4; ++i) { const int k = bk + 16 * i;
;             u32x4 v;
;             if (B_F32) { const f32x4 x = __builtin_bit_cast(f32x4, rb[2 * i]), y = __builtin_bit_cast(f32x4, rb[2 * i + 1]);
;                 v[0] = pk2bf(x[0], x[1]); v[1] = pk2bf(x[2], x[3]); v[2] = pk2bf(y[0], y[1]); v[3] = pk2bf(y[2], y[3]); }
;             else v = rb[i];
;             *(u32x4*)(lds + GB_OFF + k * GB_ST + bnc * 16) = v; }
;     };
;     const lds_cptr la = (lds_cptr)lds + (wr * 64 + fr) * 64 + fq * 16;
;     const lds_cptr lb = (lds_cptr)lds + GB_OFF + (8 * fq + (fr >> 2) + (fq & 1) * 4) * GB_ST + wc * 128 + (fr & 3) * 8;
;     const int bsw = (fq & 1) ? -4 * GB_ST : 4 * GB_ST;
;     auto compute = [&]() __attribute__((always_inline)) {
; #pragma unroll
;         for (int kh = 0; kh < 2; ++kh) {
;             bf16x8 af[4], bfr[4];
; #pragma unroll
;             for (int m = 0; m < 4; ++m) af[m] = *(const LAS bf16x8*)(la + kh * GA_KH + m * 1024);
; #pragma unroll
;             for (int n = 0; n < 4; ++n) {
;                 const s16x4 r0 = lds_tr(lb + kh * 32 * GB_ST + n * 32), r1 = lds_tr(lb + kh * 32 * GB_ST + n * 32 + bsw);
;                 bfr[n] = (bf16x8){r0[0], r0[1], r0[2], r0[3], r1[0], r1[1], r1[2], r1[3]};
;             }
; #pragma unroll
;             for (int m = 0; m < 4; ++m)
; #pragma unroll
;                 for (int n = 0; n < 4; ++n) acc[m][n] = __builtin_amdgcn_mfma_f32_16x16x32_bf16(bfr[n], af[m], acc[m][n], 0, 0, 0);
;         }
;     };
;     ...
;     gloadB(0, rb0); gloadA(0, ra0); gloadB(1, rb1);
;     for (int kt = 0; kt < nk; kt += 2) {
;         __syncthreads();
;         lstore(ra0, rb0);
;         __syncthreads();
;         gloadA(kt + 1, ra0);
;         if (kt + 2 < nk) gloadB(kt + 2, rb0);
;         compute();
;         __syncthreads();
;         lstore(ra0, rb1);
;         __syncthreads();
;         if (kt + 2 < nk) gloadA(kt + 2, ra0);
;         if (kt + 3 < nk) gloadB(kt + 3, rb1);
;         compute();
;     }
	v_mfma_f32_16x16x32_bf16 v[36:39], v[166:169], v[158:161], v[36:39]
	ds_read_b64_tr_b16 v[190:191], v214 offset:25792
	ds_read_b64_tr_b16 v[192:193], v214 offset:26944
	v_mfma_f32_16x16x32_bf16 v[40:43], v[170:173], v[158:161], v[40:43]
	ds_read_b64_tr_b16 v[198:199], v214 offset:25824
	ds_read_b64_tr_b16 v[200:201], v214 offset:26976
	v_mfma_f32_16x16x32_bf16 v[44:47], v[174:177], v[158:161], v[44:47]
	s_waitcnt vmcnt(0)
	ds_write_b128 v210, v[84:87] offset:36864
	v_mfma_f32_16x16x32_bf16 v[48:51], v[178:181], v[158:161], v[48:51]
	ds_read_b128 v[140:143], v211 offset:9280
	s_waitcnt lgkmcnt(11)
	v_mfma_f32_16x16x32_bf16 v[52:55], v[166:169], v[162:165], v[52:55]
	ds_write_b128 v210, v[88:91] offset:38912
	v_mfma_f32_16x16x32_bf16 v[56:59], v[170:173], v[162:165], v[56:59]
	ds_write_b128 v210, v[92:95] offset:40960
	v_mfma_f32_16x16x32_bf16 v[60:63], v[174:177], v[162:165], v[60:63]
	ds_write_b128 v210, v[96:99] offset:43008
	v_mfma_f32_16x16x32_bf16 v[64:67], v[178:181], v[162:165], v[64:67]
	s_waitcnt lgkmcnt(10)
	ds_read_b128 v[158:161], v211 offset:10304
	s_waitcnt lgkmcnt(10)
	v_mfma_f32_16x16x32_bf16 v[4:7], v[182:185], v[136:139], v[4:7]
	ds_write_b128 v213, v[120:123] offset:16512
	v_mfma_f32_16x16x32_bf16 v[8:11], v[186:189], v[136:139], v[8:11]
	ds_write_b128 v213, v[124:127] offset:21120
	s_waitcnt lgkmcnt(10)
	v_mfma_f32_16x16x32_bf16 v[12:15], v[190:193], v[136:139], v[12:15]
	ds_write_b128 v213, v[128:131] offset:25728
	s_waitcnt lgkmcnt(9)
	v_mfma_f32_16x16x32_bf16 v[16:19], v[198:201], v[136:139], v[16:19]
	ds_read_b128 v[162:165], v211 offset:11328
	s_waitcnt lgkmcnt(8)
	v_mfma_f32_16x16x32_bf16 v[20:23], v[182:185], v[140:143], v[20:23]
	ds_write_b128 v213, v[132:135] offset:30336
	v_mfma_f32_16x16x32_bf16 v[24:27], v[186:189], v[140:143], v[24:27]
	v_mfma_f32_16x16x32_bf16 v[28:31], v[190:193], v[140:143], v[28:31]
	v_mfma_f32_16x16x32_bf16 v[32:35], v[198:201], v[140:143], v[32:35]
	s_waitcnt lgkmcnt(5)
	v_mfma_f32_16x16x32_bf16 v[36:39], v[182:185], v[158:161], v[36:39]
	v_mfma_f32_16x16x32_bf16 v[40:43], v[186:189], v[158:161], v[40:43]
	v_mfma_f32_16x16x32_bf16 v[44:47], v[190:193], v[158:161], v[44:47]
	v_mfma_f32_16x16x32_bf16 v[48:51], v[198:201], v[158:161], v[48:51]
	s_waitcnt lgkmcnt(1)
	v_mfma_f32_16x16x32_bf16 v[52:55], v[182:185], v[162:165], v[52:55]
	v_mfma_f32_16x16x32_bf16 v[56:59], v[186:189], v[162:165], v[56:59]
	v_mfma_f32_16x16x32_bf16 v[60:63], v[190:193], v[162:165], v[60:63]
	v_mfma_f32_16x16x32_bf16 v[64:67], v[198:201], v[162:165], v[64:67]
	s_waitcnt lgkmcnt(0)
	s_barrier
	ds_read_b64_tr_b16 v[166:167], v214 offset:53376
	ds_read_b64_tr_b16 v[168:169], v214 offset:54528
	ds_read_b128 v[136:139], v211 offset:36864
	ds_read_b64_tr_b16 v[170:171], v214 offset:53408
	ds_read_b64_tr_b16 v[172:173], v214 offset:54560
	s_waitcnt lgkmcnt(2)
	v_mfma_f32_16x16x32_bf16 v[4:7], v[166:169], v[136:139], v[4:7]
	ds_read_b64_tr_b16 v[174:175], v214 offset:53440
	ds_read_b64_tr_b16 v[176:177], v214 offset:54592
	s_waitcnt lgkmcnt(2)
	v_mfma_f32_16x16x32_bf16 v[8:11], v[170:173], v[136:139], v[8:11]
	ds_read_b64_tr_b16 v[178:179], v214 offset:53472
	ds_read_b64_tr_b16 v[180:181], v214 offset:54624
	s_waitcnt lgkmcnt(2)
	v_mfma_f32_16x16x32_bf16 v[12:15], v[174:177], v[136:139], v[12:15]
	ds_read_b128 v[140:143], v211 offset:37888
	s_waitcnt lgkmcnt(1)
	v_mfma_f32_16x16x32_bf16 v[16:19], v[178:181], v[136:139], v[16:19]
	ds_read_b128 v[158:161], v211 offset:38912
	s_waitcnt lgkmcnt(1)
	v_mfma_f32_16x16x32_bf16 v[20:23], v[166:169], v[140:143], v[20:23]
	ds_read_b128 v[162:165], v211 offset:39936
	v_mfma_f32_16x16x32_bf16 v[24:27], v[170:173], v[140:143], v[24:27]
	ds_read_b64_tr_b16 v[182:183], v214 offset:62592
	ds_read_b64_tr_b16 v[184:185], v214 offset:63744
	v_mfma_f32_16x16x32_bf16 v[28:31], v[174:177], v[140:143], v[28:31]
	ds_read_b64_tr_b16 v[186:187], v214 offset:62624
	ds_read_b64_tr_b16 v[188:189], v214 offset:63776
	v_mfma_f32_16x16x32_bf16 v[32:35], v[178:181], v[140:143], v[32:35]
	ds_read_b128 v[136:139], v211 offset:45120
	s_waitcnt lgkmcnt(6)
	v_mfma_f32_16x16x32_bf16 v[36:39], v[166:169], v[158:161], v[36:39]
	ds_read_b64_tr_b16 v[190:191], v214 offset:62656
	ds_read_b64_tr_b16 v[192:193], v214 offset:63808
	v_mfma_f32_16x16x32_bf16 v[40:43], v[170:173], v[158:161], v[40:43]
	ds_read_b64_tr_b16 v[198:199], v214 offset:62688
	ds_read_b64_tr_b16 v[200:201], v214 offset:63840
	v_mfma_f32_16x16x32_bf16 v[44:47], v[174:177], v[158:161], v[44:47]
	v_mfma_f32_16x16x32_bf16 v[48:51], v[178:181], v[158:161], v[48:51]
	ds_read_b128 v[140:143], v211 offset:46144
	s_waitcnt lgkmcnt(10)
	v_mfma_f32_16x16x32_bf16 v[52:55], v[166:169], v[162:165], v[52:55]
	v_mfma_f32_16x16x32_bf16 v[56:59], v[170:173], v[162:165], v[56:59]
	v_mfma_f32_16x16x32_bf16 v[60:63], v[174:177], v[162:165], v[60:63]
	v_mfma_f32_16x16x32_bf16 v[64:67], v[178:181], v[162:165], v[64:67]
	ds_read_b128 v[158:161], v211 offset:47168
	s_waitcnt lgkmcnt(6)
	v_mfma_f32_16x16x32_bf16 v[4:7], v[182:185], v[136:139], v[4:7]
	v_mfma_f32_16x16x32_bf16 v[8:11], v[186:189], v[136:139], v[8:11]
	s_waitcnt lgkmcnt(4)
	v_mfma_f32_16x16x32_bf16 v[12:15], v[190:193], v[136:139], v[12:15]
	s_waitcnt lgkmcnt(2)
	v_mfma_f32_16x16x32_bf16 v[16:19], v[198:201], v[136:139], v[16:19]
	ds_read_b128 v[162:165], v211 offset:48192
	s_waitcnt lgkmcnt(2)
	v_mfma_f32_16x16x32_bf16 v[20:23], v[182:185], v[140:143], v[20:23]
	v_mfma_f32_16x16x32_bf16 v[24:27], v[186:189], v[140:143], v[24:27]
	v_mfma_f32_16x16x32_bf16 v[28:31], v[190:193], v[140:143], v[28:31]
	v_mfma_f32_16x16x32_bf16 v[32:35], v[198:201], v[140:143], v[32:35]
	s_waitcnt lgkmcnt(1)
	v_mfma_f32_16x16x32_bf16 v[36:39], v[182:185], v[158:161], v[36:39]
	v_mfma_f32_16x16x32_bf16 v[40:43], v[186:189], v[158:161], v[40:43]
	v_mfma_f32_16x16x32_bf16 v[44:47], v[190:193], v[158:161], v[44:47]
	v_mfma_f32_16x16x32_bf16 v[48:51], v[198:201], v[158:161], v[48:51]
	s_waitcnt lgkmcnt(0)
	v_mfma_f32_16x16x32_bf16 v[52:55], v[182:185], v[162:165], v[52:55]
	v_mfma_f32_16x16x32_bf16 v[56:59], v[186:189], v[162:165], v[56:59]
	v_mfma_f32_16x16x32_bf16 v[60:63], v[190:193], v[162:165], v[60:63]
	v_mfma_f32_16x16x32_bf16 v[64:67], v[198:201], v[162:165], v[64:67]
	s_waitcnt lgkmcnt(0)
	s_barrier
; __device__ __forceinline__ unsigned pk2bf(float lo, float hi) { const f32x2 v = {lo, hi}; return __builtin_bit_cast(unsigned, __builtin_convertvector(v, bf16x2_t)); }
;     template <class T> __device__ __forceinline__ T* w(size_t off) const { return (T*)(p->ws + off); }
; __device__ __forceinline__ void ph_moe2_mfma(const Ctx& c, int layer, int tile, const int* sm, unsigned char* lds) {
;     ...
;     bf16* OUT = c.w<bf16>(WS_OUT);
; #pragma unroll
;     for (int m = 0; m < 4; ++m)
; #pragma unroll
;         for (int n = 0; n < 4; ++n) {
;             const int rl = wr * 64 + m * 16 + fr, col = nt * 128 + wc * 64 + n * 16 + fq * 4;
;             uint2 o; o.x = pk2bf(acc[m][n][0], acc[m][n][1]); o.y = pk2bf(acc[m][n][2], acc[m][n][3]);
;             *(uint2*)(OUT + (size_t)(s0 + rl) * D + col) = o;
;         }
	s_lshl_b64 s[16:17], s[72:73], 11
	s_add_u32 s16, s42, s16
	s_addc_u32 s17, s43, s17
	s_add_u32 s16, s16, 0x67c6000
	s_addc_u32 s17, s17, 0
	s_lshl_b32 s6, s59, 8
	s_and_b32 s6, s6, 0x700
	s_add_u32 s16, s16, s6
	s_addc_u32 s17, s17, 0
	v_lshrrev_b32_e32 v217, 7, v118
	v_lshlrev_b32_e32 v217, 6, v217
	v_and_b32_e32 v215, 15, v118
	v_or_b32_e32 v217, v217, v215
	v_lshlrev_b32_e32 v217, 11, v217
	v_bfe_u32 v215, v118, 6, 1
	v_lshlrev_b32_e32 v215, 7, v215
	v_or_b32_e32 v217, v217, v215
	v_bfe_u32 v215, v118, 4, 2
	v_lshlrev_b32_e32 v215, 3, v215
	v_or_b32_e32 v217, v217, v215
	v_cvt_pk_bf16_f32 v218, v4, v5
	v_cvt_pk_bf16_f32 v219, v6, v7
	global_store_dwordx2 v217, v[218:219], s[16:17]
	s_nop 1
	v_cvt_pk_bf16_f32 v218, v8, v9
	v_cvt_pk_bf16_f32 v219, v10, v11
	global_store_dwordx2 v217, v[218:219], s[16:17] offset:32
	s_nop 1
	v_cvt_pk_bf16_f32 v218, v12, v13
	v_cvt_pk_bf16_f32 v219, v14, v15
	global_store_dwordx2 v217, v[218:219], s[16:17] offset:64
	s_nop 1
	v_cvt_pk_bf16_f32 v218, v16, v17
	v_cvt_pk_bf16_f32 v219, v18, v19
	global_store_dwordx2 v217, v[218:219], s[16:17] offset:96
	s_nop 1
	s_add_u32 s16, s16, 0x8000
	s_addc_u32 s17, s17, 0
	v_cvt_pk_bf16_f32 v218, v20, v21
	v_cvt_pk_bf16_f32 v219, v22, v23
	global_store_dwordx2 v217, v[218:219], s[16:17]
	s_nop 1
	v_cvt_pk_bf16_f32 v218, v24, v25
	v_cvt_pk_bf16_f32 v219, v26, v27
	global_store_dwordx2 v217, v[218:219], s[16:17] offset:32
	s_nop 1
	v_cvt_pk_bf16_f32 v218, v28, v29
	v_cvt_pk_bf16_f32 v219, v30, v31
	global_store_dwordx2 v217, v[218:219], s[16:17] offset:64
	s_nop 1
	v_cvt_pk_bf16_f32 v218, v32, v33
	v_cvt_pk_bf16_f32 v219, v34, v35
	global_store_dwordx2 v217, v[218:219], s[16:17] offset:96
	s_nop 1
	s_add_u32 s16, s16, 0x8000
	s_addc_u32 s17, s17, 0
	v_cvt_pk_bf16_f32 v218, v36, v37
	v_cvt_pk_bf16_f32 v219, v38, v39
	global_store_dwordx2 v217, v[218:219], s[16:17]
	s_nop 1
	v_cvt_pk_bf16_f32 v218, v40, v41
	v_cvt_pk_bf16_f32 v219, v42, v43
	global_store_dwordx2 v217, v[218:219], s[16:17] offset:32
	s_nop 1
	v_cvt_pk_bf16_f32 v218, v44, v45
	v_cvt_pk_bf16_f32 v219, v46, v47
	global_store_dwordx2 v217, v[218:219], s[16:17] offset:64
	s_nop 1
	v_cvt_pk_bf16_f32 v218, v48, v49
	v_cvt_pk_bf16_f32 v219, v50, v51
	global_store_dwordx2 v217, v[218:219], s[16:17] offset:96
	s_nop 1
	s_add_u32 s16, s16, 0x8000
	s_addc_u32 s17, s17, 0
	v_cvt_pk_bf16_f32 v218, v52, v53
	v_cvt_pk_bf16_f32 v219, v54, v55
	global_store_dwordx2 v217, v[218:219], s[16:17]
	s_nop 1
	v_cvt_pk_bf16_f32 v218, v56, v57
	v_cvt_pk_bf16_f32 v219, v58, v59
	global_store_dwordx2 v217, v[218:219], s[16:17] offset:32
	s_nop 1
	v_cvt_pk_bf16_f32 v218, v60, v61
	v_cvt_pk_bf16_f32 v219, v62, v63
	global_store_dwordx2 v217, v[218:219], s[16:17] offset:64
	s_nop 1
	v_cvt_pk_bf16_f32 v218, v64, v65
	v_cvt_pk_bf16_f32 v219, v66, v67
	global_store_dwordx2 v217, v[218:219], s[16:17] offset:96
	s_nop 1

;     template <class T> __device__ __forceinline__ T* w(size_t off) const { return (T*)(p->ws + off); }
;     ...
;     unsigned ao[4];
; #pragma unroll
;     for (int i = 0; i < 4; ++i) ao[i] = arow((tid >> 3) + 32 * i) + (tid & 7) * 8;
;     const int bk = tid >> 4, bnc = tid & 15;
;     constexpr int NRB = B_F32 ? 8 : 4;
;     u32x4 ra0[4], ra1[4]; u32x4 rb0[NRB], rb1[NRB];
;     auto gloadA = [&](int kt, u32x4 (&ra)[4]) __attribute__((always_inline)) {
; #pragma unroll
;         for (int i = 0; i < 4; ++i) ra[i] = *(const u32x4*)(Abase + (ao[i] + kt * 64));
;     };
;     auto gloadB = [&](int kt, u32x4 (&rb)[NRB]) __attribute__((always_inline)) {
;         if (B_F32) {
;             const float* bp = (const float*)Bbase + (boff + (unsigned)((kt * 64 + bk) * ldb));
; #pragma unroll
;             for (int i = 0; i < 4; ++i) {
;                 if (bval) { rb[2 * i] = *(const u32x4*)(bp + (unsigned)(16 * i * ldb)); rb[2 * i + 1] = *(const u32x4*)(bp + (unsigned)(16 * i * ldb) + 4); }
;                 else { rb[2 * i] = (u32x4){0u, 0u, 0u, 0u}; rb[2 * i + 1] = rb[2 * i]; }
;             }
;         } else {
;             const bf16* bp = (const bf16*)Bbase + (boff + (unsigned)((kt * 64 + bk) * ldb));
; #pragma unroll
;             for (int i = 0; i < 4; ++i) rb[i] = bval ? *(const u32x4*)(bp + (unsigned)(16 * i * ldb)) : (u32x4){0u, 0u, 0u, 0u};
;         }
;     };
; __device__ __forceinline__ void ph_moe1_mfma(const Ctx& c, int layer, int tile, const int* sm, unsigned char* lds) {
;     ...
;     const bf16* HA = c.w<bf16>(WS_HA); const int* LI = c.w<int>(WS_LIST) + (size_t)e * NT;
;     f32x4 acc[4][4];
;     gemm_tile<false>(c.tid, lds, HA, [&](int r) __attribute__((always_inline)) { const int tok = LI[(base + r < ce) ? (base + r) : base]; return (unsigned)(tok * D); }, c.w<bf16>(WS_BGU) + (size_t)e * D * 1024, (unsigned)(nt * 128 + (c.tid & 15) * 8), 1024, true, D, acc);
.LBB0_162:
	s_and_b32 s7, s58, 7
	s_and_b32 s6, s59, 7
	s_lshl_b32 s15, s7, 7
	v_ashrrev_i32_e32 v4, 3, v118
	s_add_u32 s28, s42, 0x45c6000
	v_add_u32_e32 v4, v2, v4
	s_addc_u32 s29, s43, 0
	s_mul_i32 s7, s18, 0x11000
	v_cmp_lt_i32_e32 vcc, v4, v5
	v_add_u32_e32 v8, 32, v4
	s_add_u32 s7, s42, s7
	v_cndmask_b32_e32 v6, v2, v4, vcc
	v_cmp_lt_i32_e32 vcc, v8, v5
	v_add_u32_e32 v10, 64, v4
	s_addc_u32 s19, s43, 0
	v_cndmask_b32_e32 v8, v2, v8, vcc
	v_cmp_lt_i32_e32 vcc, v10, v5
	v_add_u32_e32 v4, 0x60, v4
	s_add_u32 s44, s7, 0x1012c000
	v_cndmask_b32_e32 v10, v2, v10, vcc
	v_cmp_lt_i32_e32 vcc, v4, v5
	s_addc_u32 s45, s19, 0
	v_ashrrev_i32_e32 v7, 31, v6
	v_cndmask_b32_e32 v4, v2, v4, vcc
	v_lshl_add_u64 v[6:7], v[6:7], 2, s[44:45]
	v_ashrrev_i32_e32 v9, 31, v8
	v_ashrrev_i32_e32 v11, 31, v10
	v_ashrrev_i32_e32 v5, 31, v4
	v_lshl_add_u64 v[8:9], v[8:9], 2, s[44:45]
	v_lshl_add_u64 v[10:11], v[10:11], 2, s[44:45]
	v_lshl_add_u64 v[4:5], v[4:5], 2, s[44:45]
	global_load_dword v12, v[6:7], off
	global_load_dword v13, v[8:9], off
	global_load_dword v14, v[10:11], off
	global_load_dword v15, v[4:5], off
	s_lshl_b32 s18, s18, 21
	v_bfe_u32 v2, v118, 4, 2
	v_ashrrev_i32_e32 v4, 1, v118
	v_bfe_u32 v6, v118, 4, 1
	s_add_u32 s18, s42, s18
	v_bfe_u32 v5, v118, 2, 2
	v_lshlrev_b32_e32 v7, 1, v118
	v_and_b32_e32 v120, 0xffffffc0, v4
	v_lshlrev_b32_e32 v19, 4, v2
	v_lshlrev_b32_e32 v2, 3, v2
	v_lshlrev_b32_e32 v4, 2, v6
	s_addc_u32 s19, s43, 0
	v_lshlrev_b32_e32 v16, 3, v118
	v_ashrrev_i32_e32 v17, 4, v118
	v_and_b32_e32 v7, 0x80, v7
	v_or3_b32 v2, v2, v5, v4
	s_movk_i32 s48, 0x120
	s_add_u32 s44, s18, 0x18dd5100
	v_and_b32_e32 v18, 0x78, v16
	v_lshlrev_b32_e32 v21, 10, v17
	v_mad_u32_u24 v2, v2, s48, v7
	s_addc_u32 s45, s19, 0
	s_lshl_b32 s18, s6, 7
	v_and_b32_e32 v119, 15, v118
	v_and_or_b32 v122, v16, 24, v2
	v_or3_b32 v2, v18, s18, v21
	v_cmp_eq_u32_e32 vcc, 0, v6
	v_or_b32_e32 v6, v120, v119
	v_lshl_add_u64 v[4:5], v[2:3], 1, s[44:45]
	v_cndmask_b32_e32 v20, v236, v237, vcc
	v_lshlrev_b32_e32 v22, 6, v6
	v_add_co_u32_e32 v6, vcc, s40, v4
	s_mov_b32 s18, 0x10000
	s_nop 0
	v_addc_co_u32_e32 v7, vcc, 0, v5, vcc
	v_add_co_u32_e32 v8, vcc, s18, v4
	s_mov_b32 s19, 0x18000
	s_nop 0
	v_addc_co_u32_e32 v9, vcc, 0, v5, vcc
	v_and_b32_e32 v121, 56, v16
	v_add_co_u32_e32 v10, vcc, s19, v4
	v_add_u32_e32 v2, 0x10000, v2
	s_nop 0
	v_addc_co_u32_e32 v11, vcc, 0, v5, vcc
	v_mov_b32_e32 v5, v3
	v_mov_b32_e32 v7, v3
	v_mov_b32_e32 v9, v3
	v_mov_b32_e32 v11, v3
	s_mov_b32 s7, 0
	v_add_u32_e32 v129, v22, v19
	v_add_u32_e32 v130, v122, v20
	s_waitcnt vmcnt(0)
	v_lshlrev_b32_e32 v123, 10, v12
	v_lshlrev_b32_e32 v124, 10, v13
	v_lshlrev_b32_e32 v125, 10, v14
	v_or_b32_e32 v4, v123, v121
	v_lshlrev_b32_e32 v126, 10, v15
	v_or_b32_e32 v6, v124, v121
	v_or_b32_e32 v8, v125, v121
	v_lshl_add_u64 v[4:5], v[4:5], 1, s[28:29]
	v_or_b32_e32 v10, v126, v121
	v_lshl_add_u64 v[6:7], v[6:7], 1, s[28:29]
	v_lshl_add_u64 v[4:5], v[8:9], 1, s[28:29]
	v_lshl_add_u64 v[6:7], v[10:11], 1, s[28:29]
	v_lshl_add_u64 v[4:5], v[2:3], 1, s[44:45]
	v_add_co_u32_e32 v6, vcc, s40, v4
	v_and_b32_e32 v2, 1, v118
	s_nop 0
	v_addc_co_u32_e32 v7, vcc, 0, v5, vcc
	v_add_co_u32_e32 v6, vcc, s18, v4
	v_cmp_eq_u32_e64 s[46:47], 0, v2
	s_nop 0
	v_addc_co_u32_e32 v7, vcc, 0, v5, vcc
	v_add_co_u32_e32 v4, vcc, s19, v4
	v_bfe_i32 v2, v118, 2, 1
	s_nop 0
	v_addc_co_u32_e32 v5, vcc, 0, v5, vcc
	v_and_b32_e32 v2, 0x2040, v2
	v_and_b32_e32 v4, 0xffffffc0, v16
	v_add_u32_e32 v2, v2, v4
	v_lshlrev_b32_e32 v4, 4, v118
	v_and_b32_e32 v5, 48, v4
	v_or3_b32 v4, v21, s15, v18
	v_mul_lo_u32 v6, v17, s48
	v_lshlrev_b32_e32 v7, 4, v119
	v_add_u32_e32 v116, 0x30000, v4
	v_mov_b32_e32 v4, 0
	v_add_u32_e32 v127, v2, v5
	v_add_u32_e32 v128, v6, v7
	v_or_b32_e32 v123, v123, v121
	v_lshlrev_b32_e32 v123, 1, v123
	v_or_b32_e32 v124, v124, v121
	v_lshlrev_b32_e32 v124, 1, v124
	v_or_b32_e32 v125, v125, v121
	v_lshlrev_b32_e32 v125, 1, v125
	v_or_b32_e32 v126, v126, v121
	v_lshlrev_b32_e32 v126, 1, v126
	s_lshl_b32 s48, s6, 7
	v_or3_b32 v214, v18, s48, v21
	v_lshlrev_b32_e32 v214, 1, v214
	v_add_u32_e32 v215, 0x8000, v214
	v_add_u32_e32 v216, 0x10000, v214
	v_add_u32_e32 v217, 0x18000, v214
	v_bfe_u32 v116, v118, 5, 2
	v_sub_u32_e32 v116, 0, v116
	v_and_b32_e32 v116, 3, v116
	v_lshlrev_b32_e32 v116, 4, v116
	v_xor_b32_e32 v127, v127, v116
	v_bfe_u32 v116, v118, 2, 2
	v_sub_u32_e32 v116, 0, v116
	v_and_b32_e32 v116, 3, v116
	v_lshlrev_b32_e32 v116, 4, v116
	v_xor_b32_e32 v129, v129, v116
	v_and_b32_e32 v128, 15, v118
	v_lshlrev_b32_e32 v128, 4, v128
	v_bfe_u32 v116, v118, 7, 1
	v_lshlrev_b32_e32 v116, 7, v116
	v_xor_b32_e32 v128, v128, v116
	v_lshrrev_b32_e32 v116, 4, v118
	v_mul_u32_u24_e32 v116, 0x120, v116
	v_add_u32_e32 v128, v128, v116
	v_add_u32_e32 v130, 0x9000, v128
	v_bfe_u32 v122, v118, 4, 2
	v_lshlrev_b32_e32 v122, 3, v122
	v_bfe_u32 v116, v118, 2, 2
	v_add_u32_e32 v122, v122, v116
	v_mul_u32_u24_e32 v122, 0x120, v122
	v_lshrrev_b32_e32 v116, 6, v118
	v_lshrrev_b32_e32 v117, 4, v118
	v_xor_b32_e32 v116, v116, v117
	v_and_b32_e32 v116, 1, v116
	v_lshlrev_b32_e32 v116, 7, v116
	v_and_b32_e32 v117, 3, v118
	v_lshlrev_b32_e32 v117, 3, v117
	v_or3_b32 v122, v122, v116, v117
	global_load_dwordx4 v[68:71], v123, s[28:29]
	global_load_dwordx4 v[64:67], v124, s[28:29]
	global_load_dwordx4 v[80:83], v125, s[28:29]
	global_load_dwordx4 v[76:79], v126, s[28:29]
	global_load_dwordx4 v[24:27], v214, s[44:45]
	global_load_dwordx4 v[32:35], v215, s[44:45]
	global_load_dwordx4 v[36:39], v216, s[44:45]
	global_load_dwordx4 v[40:43], v217, s[44:45]
	s_add_u32 s44, s44, 0x20000
	s_addc_u32 s45, s45, 0
	global_load_dwordx4 v[198:201], v123, s[28:29] offset:128
; __device__ __forceinline__ unsigned pk2bf(float lo, float hi) { const f32x2 v = {lo, hi}; return __builtin_bit_cast(unsigned, __builtin_convertvector(v, bf16x2_t)); }
;     ...
;     auto lstore = [&](const u32x4 (&ra)[4], const u32x4 (&rb)[NRB]) __attribute__((always_inline)) {
; #pragma unroll
;         for (int i = 0; i < 4; ++i) { const int row = (tid >> 3) + 32 * i, kc = tid & 7;
;             const u32x4 v = (kc & 1) ? (u32x4){ra[i][2], ra[i][3], ra[i][0], ra[i][1]} : ra[i];
;             *(u32x4*)(lds + (kc >> 2) * GA_KH + row * 64 + (kc & 3) * 16) = v; }
; #pragma unroll
;         for (int i = 0; i < 4; ++i) { const int k = bk + 16 * i;
;             u32x4 v;
;             if (B_F32) { const f32x4 x = __builtin_bit_cast(f32x4, rb[2 * i]), y = __builtin_bit_cast(f32x4, rb[2 * i + 1]);
;                 v[0] = pk2bf(x[0], x[1]); v[1] = pk2bf(x[2], x[3]); v[2] = pk2bf(y[0], y[1]); v[3] = pk2bf(y[2], y[3]); }
;             else v = rb[i];
;             *(u32x4*)(lds + GB_OFF + k * GB_ST + bnc * 16) = v; }
;     };
;     const lds_cptr la = (lds_cptr)lds + (wr * 64 + fr) * 64 + fq * 16;
;     const lds_cptr lb = (lds_cptr)lds + GB_OFF + (8 * fq + (fr >> 2) + (fq & 1) * 4) * GB_ST + wc * 128 + (fr & 3) * 8;
;     const int bsw = (fq & 1) ? -4 * GB_ST : 4 * GB_ST;
;     ...
;     gloadB(0, rb0); gloadA(0, ra0); gloadB(1, rb1);
;     for (int kt = 0; kt < nk; kt += 2) {
;         __syncthreads();
;         lstore(ra0, rb0);
;         __syncthreads();
;         gloadA(kt + 1, ra0);
;         if (kt + 2 < nk) gloadB(kt + 2, rb0);
;         compute();
;         __syncthreads();
;         lstore(ra0, rb1);
;         __syncthreads();
;         if (kt + 2 < nk) gloadA(kt + 2, ra0);
;         if (kt + 3 < nk) gloadB(kt + 3, rb1);
;         compute();
;     }
	global_load_dwordx4 v[202:205], v124, s[28:29] offset:128
	global_load_dwordx4 v[206:209], v125, s[28:29] offset:128
	global_load_dwordx4 v[210:213], v126, s[28:29] offset:128
	global_load_dwordx4 v[44:47], v214, s[44:45]
	global_load_dwordx4 v[48:51], v215, s[44:45]
	global_load_dwordx4 v[52:55], v216, s[44:45]
	global_load_dwordx4 v[56:59], v217, s[44:45]
	s_add_u32 s44, s44, 0x20000
	s_addc_u32 s45, s45, 0
	v_mov_b32_e32 v5, v4
	v_mov_b32_e32 v6, v4
	v_mov_b32_e32 v7, v4
	v_mov_b32_e32 v16, v4
	v_mov_b32_e32 v17, v4
	v_mov_b32_e32 v18, v4
	v_mov_b32_e32 v19, v4
	v_mov_b32_e32 v8, v4
	v_mov_b32_e32 v9, v4
	v_mov_b32_e32 v10, v4
	v_mov_b32_e32 v11, v4
	v_mov_b32_e32 v12, v4
	v_mov_b32_e32 v13, v4
	v_mov_b32_e32 v14, v4
	v_mov_b32_e32 v15, v4
	v_mov_b32_e32 v20, v4
	v_mov_b32_e32 v21, v4
	v_mov_b32_e32 v22, v4
	v_mov_b32_e32 v23, v4
	v_mov_b32_e32 v60, v4
	v_mov_b32_e32 v61, v4
	v_mov_b32_e32 v62, v4
	v_mov_b32_e32 v63, v4
	v_mov_b32_e32 v28, v4
	v_mov_b32_e32 v29, v4
	v_mov_b32_e32 v30, v4
	v_mov_b32_e32 v31, v4
	v_mov_b32_e32 v72, v4
	v_mov_b32_e32 v73, v4
	v_mov_b32_e32 v74, v4
	v_mov_b32_e32 v75, v4
	v_mov_b32_e32 v84, v4
	v_mov_b32_e32 v85, v4
	v_mov_b32_e32 v86, v4
	v_mov_b32_e32 v87, v4
	v_mov_b32_e32 v92, v4
	v_mov_b32_e32 v93, v4
	v_mov_b32_e32 v94, v4
	v_mov_b32_e32 v95, v4
	v_mov_b32_e32 v88, v4
	v_mov_b32_e32 v89, v4
	v_mov_b32_e32 v90, v4
	v_mov_b32_e32 v91, v4
	v_mov_b32_e32 v96, v4
	v_mov_b32_e32 v97, v4
	v_mov_b32_e32 v98, v4
	v_mov_b32_e32 v99, v4
	v_mov_b32_e32 v100, v4
	v_mov_b32_e32 v101, v4
	v_mov_b32_e32 v102, v4
	v_mov_b32_e32 v103, v4
	v_mov_b32_e32 v108, v4
	v_mov_b32_e32 v109, v4
	v_mov_b32_e32 v110, v4
	v_mov_b32_e32 v111, v4
	v_mov_b32_e32 v104, v4
	v_mov_b32_e32 v105, v4
	v_mov_b32_e32 v106, v4
	v_mov_b32_e32 v107, v4
	v_mov_b32_e32 v112, v4
	v_mov_b32_e32 v113, v4
	v_mov_b32_e32 v114, v4
	v_mov_b32_e32 v115, v4
	s_waitcnt vmcnt(8)
	s_barrier
	ds_write_b128 v127, v[68:71]
	ds_write_b128 v127, v[64:67] offset:2048
	ds_write_b128 v127, v[80:83] offset:4096
	ds_write_b128 v127, v[76:79] offset:6144
	ds_write_b128 v128, v[24:27] offset:16512
	ds_write_b128 v128, v[32:35] offset:21120
	ds_write_b128 v128, v[36:39] offset:25728
	ds_write_b128 v128, v[40:43] offset:30336
	global_load_dwordx4 v[68:71], v123, s[28:29] offset:256
	global_load_dwordx4 v[64:67], v124, s[28:29] offset:256
	global_load_dwordx4 v[80:83], v125, s[28:29] offset:256
	global_load_dwordx4 v[76:79], v126, s[28:29] offset:256
	global_load_dwordx4 v[24:27], v214, s[44:45]
	global_load_dwordx4 v[32:35], v215, s[44:45]
	global_load_dwordx4 v[36:39], v216, s[44:45]
	global_load_dwordx4 v[40:43], v217, s[44:45]
	s_add_u32 s44, s44, 0x20000
	s_addc_u32 s45, s45, 0
	s_add_u32 s100, s44, 0x20000
	s_addc_u32 s101, s45, 0
	s_waitcnt lgkmcnt(0)
	s_barrier
.Lm1_loop:
	ds_read_b64_tr_b16 v[174:175], v122 offset:16512
	ds_read_b64_tr_b16 v[176:177], v122 offset:17664
	ds_read_b128 v[158:161], v129
	ds_read_b64_tr_b16 v[178:179], v122 offset:16544
	ds_read_b64_tr_b16 v[180:181], v122 offset:17696
	s_waitcnt lgkmcnt(2)
	v_mfma_f32_16x16x32_bf16 v[112:115], v[174:177], v[158:161], v[112:115]
	ds_read_b64_tr_b16 v[182:183], v122 offset:16576
	ds_read_b64_tr_b16 v[184:185], v122 offset:17728
	s_waitcnt lgkmcnt(2)
	v_mfma_f32_16x16x32_bf16 v[104:107], v[178:181], v[158:161], v[104:107]
	ds_read_b64_tr_b16 v[186:187], v122 offset:16608
	ds_read_b64_tr_b16 v[188:189], v122 offset:17760
	s_waitcnt lgkmcnt(2)
	v_mfma_f32_16x16x32_bf16 v[108:111], v[182:185], v[158:161], v[108:111]
	ds_read_b128 v[162:165], v129 offset:1024
	s_waitcnt lgkmcnt(1)
	v_mfma_f32_16x16x32_bf16 v[100:103], v[186:189], v[158:161], v[100:103]
	ds_read_b128 v[166:169], v129 offset:2048
	s_waitcnt lgkmcnt(1)
	v_mfma_f32_16x16x32_bf16 v[96:99], v[174:177], v[162:165], v[96:99]
	ds_read_b128 v[170:173], v129 offset:3072
	v_mfma_f32_16x16x32_bf16 v[88:91], v[178:181], v[162:165], v[88:91]
	ds_read_b64_tr_b16 v[190:191], v122 offset:25728
	ds_read_b64_tr_b16 v[192:193], v122 offset:26880
	v_mfma_f32_16x16x32_bf16 v[92:95], v[182:185], v[162:165], v[92:95]
	ds_read_b64_tr_b16 v[132:133], v122 offset:25760
	ds_read_b64_tr_b16 v[134:135], v122 offset:26912
	v_mfma_f32_16x16x32_bf16 v[84:87], v[186:189], v[162:165], v[84:87]
	ds_read_b128 v[158:161], v129 offset:8256
	s_waitcnt lgkmcnt(6)
	v_mfma_f32_16x16x32_bf16 v[72:75], v[174:177], v[166:169], v[72:75]
	ds_read_b64_tr_b16 v[136:137], v122 offset:25792
	ds_read_b64_tr_b16 v[138:139], v122 offset:26944
	v_mfma_f32_16x16x32_bf16 v[28:31], v[178:181], v[166:169], v[28:31]
	ds_read_b64_tr_b16 v[140:141], v122 offset:25824
	ds_read_b64_tr_b16 v[142:143], v122 offset:26976
	v_mfma_f32_16x16x32_bf16 v[60:63], v[182:185], v[166:169], v[60:63]
	s_waitcnt vmcnt(8)
	ds_write_b128 v127, v[198:201] offset:36864
	v_mfma_f32_16x16x32_bf16 v[20:23], v[186:189], v[166:169], v[20:23]
	ds_read_b128 v[162:165], v129 offset:9280
	s_waitcnt lgkmcnt(11)
	v_mfma_f32_16x16x32_bf16 v[12:15], v[174:177], v[170:173], v[12:15]
	ds_write_b128 v127, v[202:205] offset:38912
	v_mfma_f32_16x16x32_bf16 v[8:11], v[178:181], v[170:173], v[8:11]
	ds_write_b128 v127, v[206:209] offset:40960
	v_mfma_f32_16x16x32_bf16 v[16:19], v[182:185], v[170:173], v[16:19]
	ds_write_b128 v127, v[210:213] offset:43008
	v_mfma_f32_16x16x32_bf16 v[4:7], v[186:189], v[170:173], v[4:7]
	s_waitcnt lgkmcnt(10)
	ds_read_b128 v[166:169], v129 offset:10304
	s_waitcnt lgkmcnt(10)
	v_mfma_f32_16x16x32_bf16 v[112:115], v[190:193], v[158:161], v[112:115]
	ds_write_b128 v130, v[44:47] offset:16512
	v_mfma_f32_16x16x32_bf16 v[104:107], v[132:135], v[158:161], v[104:107]
	ds_write_b128 v130, v[48:51] offset:21120
	s_waitcnt lgkmcnt(10)
; #define LAS __attribute__((address_space(3)))
; __device__ __forceinline__ s16x4 lds_tr(lds_cptr p) { return __builtin_bit_cast(s16x4, __builtin_amdgcn_ds_read_tr16_b64_v4i16((LAS s16x4*)p)); }
;     ...
;     auto compute = [&]() __attribute__((always_inline)) {
; #pragma unroll
;         for (int kh = 0; kh < 2; ++kh) {
;             bf16x8 af[4], bfr[4];
; #pragma unroll
;             for (int m = 0; m < 4; ++m) af[m] = *(const LAS bf16x8*)(la + kh * GA_KH + m * 1024);
; #pragma unroll
;             for (int n = 0; n < 4; ++n) {
;                 const s16x4 r0 = lds_tr(lb + kh * 32 * GB_ST + n * 32), r1 = lds_tr(lb + kh * 32 * GB_ST + n * 32 + bsw);
;                 bfr[n] = (bf16x8){r0[0], r0[1], r0[2], r0[3], r1[0], r1[1], r1[2], r1[3]};
;             }
; #pragma unroll
;             for (int m = 0; m < 4; ++m)
; #pragma unroll
;                 for (int n = 0; n < 4; ++n) acc[m][n] = __builtin_amdgcn_mfma_f32_16x16x32_bf16(bfr[n], af[m], acc[m][n], 0, 0, 0);
;         }
;     };
;     ...
;     gloadB(0, rb0); gloadA(0, ra0); gloadB(1, rb1);
;     for (int kt = 0; kt < nk; kt += 2) {
;         __syncthreads();
;         lstore(ra0, rb0);
;         __syncthreads();
;         gloadA(kt + 1, ra0);
;         if (kt + 2 < nk) gloadB(kt + 2, rb0);
;         compute();
;         __syncthreads();
;         lstore(ra0, rb1);
;         __syncthreads();
;         if (kt + 2 < nk) gloadA(kt + 2, ra0);
;         if (kt + 3 < nk) gloadB(kt + 3, rb1);
;         compute();
;     }
	v_mfma_f32_16x16x32_bf16 v[108:111], v[136:139], v[158:161], v[108:111]
	ds_write_b128 v130, v[52:55] offset:25728
	s_waitcnt lgkmcnt(9)
	v_mfma_f32_16x16x32_bf16 v[100:103], v[140:143], v[158:161], v[100:103]
	ds_read_b128 v[170:173], v129 offset:11328
	s_waitcnt lgkmcnt(8)
	v_mfma_f32_16x16x32_bf16 v[96:99], v[190:193], v[162:165], v[96:99]
	ds_write_b128 v130, v[56:59] offset:30336
	v_mfma_f32_16x16x32_bf16 v[88:91], v[132:135], v[162:165], v[88:91]
	global_load_dwordx4 v[198:201], v123, s[28:29] offset:384
	v_mfma_f32_16x16x32_bf16 v[92:95], v[136:139], v[162:165], v[92:95]
	global_load_dwordx4 v[202:205], v124, s[28:29] offset:384
	v_mfma_f32_16x16x32_bf16 v[84:87], v[140:143], v[162:165], v[84:87]
	global_load_dwordx4 v[206:209], v125, s[28:29] offset:384
	s_waitcnt lgkmcnt(5)
	v_mfma_f32_16x16x32_bf16 v[72:75], v[190:193], v[166:169], v[72:75]
	global_load_dwordx4 v[210:213], v126, s[28:29] offset:384
	v_mfma_f32_16x16x32_bf16 v[28:31], v[132:135], v[166:169], v[28:31]
	global_load_dwordx4 v[44:47], v214, s[44:45]
	v_mfma_f32_16x16x32_bf16 v[60:63], v[136:139], v[166:169], v[60:63]
	global_load_dwordx4 v[48:51], v215, s[44:45]
	v_mfma_f32_16x16x32_bf16 v[20:23], v[140:143], v[166:169], v[20:23]
	global_load_dwordx4 v[52:55], v216, s[44:45]
	s_waitcnt lgkmcnt(1)
	v_mfma_f32_16x16x32_bf16 v[12:15], v[190:193], v[170:173], v[12:15]
	global_load_dwordx4 v[56:59], v217, s[44:45]
	v_mfma_f32_16x16x32_bf16 v[8:11], v[132:135], v[170:173], v[8:11]
	v_mfma_f32_16x16x32_bf16 v[16:19], v[136:139], v[170:173], v[16:19]
	v_mfma_f32_16x16x32_bf16 v[4:7], v[140:143], v[170:173], v[4:7]
	s_waitcnt lgkmcnt(0)
	s_barrier
	s_cmp_lt_u32 s7, 12
	s_cbranch_scc0 .Lm1_h1_last
	ds_read_b64_tr_b16 v[174:175], v122 offset:53376
	ds_read_b64_tr_b16 v[176:177], v122 offset:54528
	ds_read_b128 v[158:161], v129 offset:36864
	ds_read_b64_tr_b16 v[178:179], v122 offset:53408
	ds_read_b64_tr_b16 v[180:181], v122 offset:54560
	s_waitcnt lgkmcnt(2)
	v_mfma_f32_16x16x32_bf16 v[112:115], v[174:177], v[158:161], v[112:115]
	ds_read_b64_tr_b16 v[182:183], v122 offset:53440
	ds_read_b64_tr_b16 v[184:185], v122 offset:54592
	s_waitcnt lgkmcnt(2)
	v_mfma_f32_16x16x32_bf16 v[104:107], v[178:181], v[158:161], v[104:107]
	ds_read_b64_tr_b16 v[186:187], v122 offset:53472
	ds_read_b64_tr_b16 v[188:189], v122 offset:54624
	s_waitcnt lgkmcnt(2)
	v_mfma_f32_16x16x32_bf16 v[108:111], v[182:185], v[158:161], v[108:111]
	ds_read_b128 v[162:165], v129 offset:37888
	s_waitcnt lgkmcnt(1)
	v_mfma_f32_16x16x32_bf16 v[100:103], v[186:189], v[158:161], v[100:103]
	ds_read_b128 v[166:169], v129 offset:38912
	s_waitcnt lgkmcnt(1)
	v_mfma_f32_16x16x32_bf16 v[96:99], v[174:177], v[162:165], v[96:99]
	ds_read_b128 v[170:173], v129 offset:39936
	v_mfma_f32_16x16x32_bf16 v[88:91], v[178:181], v[162:165], v[88:91]
	ds_read_b64_tr_b16 v[190:191], v122 offset:62592
	ds_read_b64_tr_b16 v[192:193], v122 offset:63744
	v_mfma_f32_16x16x32_bf16 v[92:95], v[182:185], v[162:165], v[92:95]
	ds_read_b64_tr_b16 v[132:133], v122 offset:62624
	ds_read_b64_tr_b16 v[134:135], v122 offset:63776
	v_mfma_f32_16x16x32_bf16 v[84:87], v[186:189], v[162:165], v[84:87]
	ds_read_b128 v[158:161], v129 offset:45120
	s_waitcnt lgkmcnt(6)
	v_mfma_f32_16x16x32_bf16 v[72:75], v[174:177], v[166:169], v[72:75]
	ds_read_b64_tr_b16 v[136:137], v122 offset:62656
	ds_read_b64_tr_b16 v[138:139], v122 offset:63808
	v_mfma_f32_16x16x32_bf16 v[28:31], v[178:181], v[166:169], v[28:31]
	ds_read_b64_tr_b16 v[140:141], v122 offset:62688
	ds_read_b64_tr_b16 v[142:143], v122 offset:63840
	v_mfma_f32_16x16x32_bf16 v[60:63], v[182:185], v[166:169], v[60:63]
	s_waitcnt vmcnt(8)
	ds_write_b128 v127, v[68:71]
	v_mfma_f32_16x16x32_bf16 v[20:23], v[186:189], v[166:169], v[20:23]
	ds_read_b128 v[162:165], v129 offset:46144
	s_waitcnt lgkmcnt(11)
	v_mfma_f32_16x16x32_bf16 v[12:15], v[174:177], v[170:173], v[12:15]
	ds_write_b128 v127, v[64:67] offset:2048
	v_mfma_f32_16x16x32_bf16 v[8:11], v[178:181], v[170:173], v[8:11]
	ds_write_b128 v127, v[80:83] offset:4096
	v_mfma_f32_16x16x32_bf16 v[16:19], v[182:185], v[170:173], v[16:19]
	ds_write_b128 v127, v[76:79] offset:6144
	v_mfma_f32_16x16x32_bf16 v[4:7], v[186:189], v[170:173], v[4:7]
	s_waitcnt lgkmcnt(10)
	ds_read_b128 v[166:169], v129 offset:47168
	s_waitcnt lgkmcnt(10)
	v_mfma_f32_16x16x32_bf16 v[112:115], v[190:193], v[158:161], v[112:115]
	ds_write_b128 v128, v[24:27] offset:16512
	v_mfma_f32_16x16x32_bf16 v[104:107], v[132:135], v[158:161], v[104:107]
	ds_write_b128 v128, v[32:35] offset:21120
	s_waitcnt lgkmcnt(10)
	v_mfma_f32_16x16x32_bf16 v[108:111], v[136:139], v[158:161], v[108:111]
	ds_write_b128 v128, v[36:39] offset:25728
	s_waitcnt lgkmcnt(9)
	v_mfma_f32_16x16x32_bf16 v[100:103], v[140:143], v[158:161], v[100:103]
	ds_read_b128 v[170:173], v129 offset:48192
	s_waitcnt lgkmcnt(8)
	v_mfma_f32_16x16x32_bf16 v[96:99], v[190:193], v[162:165], v[96:99]
	ds_write_b128 v128, v[40:43] offset:30336
	v_mfma_f32_16x16x32_bf16 v[88:91], v[132:135], v[162:165], v[88:91]
	global_load_dwordx4 v[68:71], v123, s[28:29] offset:512
	v_mfma_f32_16x16x32_bf16 v[92:95], v[136:139], v[162:165], v[92:95]
	global_load_dwordx4 v[64:67], v124, s[28:29] offset:512
	v_mfma_f32_16x16x32_bf16 v[84:87], v[140:143], v[162:165], v[84:87]
	global_load_dwordx4 v[80:83], v125, s[28:29] offset:512
	s_waitcnt lgkmcnt(5)
	v_mfma_f32_16x16x32_bf16 v[72:75], v[190:193], v[166:169], v[72:75]
	global_load_dwordx4 v[76:79], v126, s[28:29] offset:512
	v_mfma_f32_16x16x32_bf16 v[28:31], v[132:135], v[166:169], v[28:31]
	global_load_dwordx4 v[24:27], v214, s[100:101]
	v_mfma_f32_16x16x32_bf16 v[60:63], v[136:139], v[166:169], v[60:63]
	global_load_dwordx4 v[32:35], v215, s[100:101]
	v_mfma_f32_16x16x32_bf16 v[20:23], v[140:143], v[166:169], v[20:23]
	global_load_dwordx4 v[36:39], v216, s[100:101]
	s_waitcnt lgkmcnt(1)
	v_mfma_f32_16x16x32_bf16 v[12:15], v[190:193], v[170:173], v[12:15]
	global_load_dwordx4 v[40:43], v217, s[100:101]
	v_mfma_f32_16x16x32_bf16 v[8:11], v[132:135], v[170:173], v[8:11]
	v_mfma_f32_16x16x32_bf16 v[16:19], v[136:139], v[170:173], v[16:19]
	v_mfma_f32_16x16x32_bf16 v[4:7], v[140:143], v[170:173], v[4:7]
	s_waitcnt lgkmcnt(0)
	s_barrier
	s_add_u32 s28, s28, 0x100
	s_addc_u32 s29, s29, 0
	s_add_u32 s44, s44, 0x40000
	s_addc_u32 s45, s45, 0
	s_add_u32 s100, s100, 0x40000
	s_addc_u32 s101, s101, 0
	s_add_i32 s7, s7, 2
	s_branch .Lm1_loop
; #define LAS __attribute__((address_space(3)))
; __device__ __forceinline__ s16x4 lds_tr(lds_cptr p) { return __builtin_bit_cast(s16x4, __builtin_amdgcn_ds_read_tr16_b64_v4i16((LAS s16x4*)p)); }
;     ...
;     auto compute = [&]() __attribute__((always_inline)) {
; #pragma unroll
;         for (int kh = 0; kh < 2; ++kh) {
;             bf16x8 af[4], bfr[4];
; #pragma unroll
;             for (int m = 0; m < 4; ++m) af[m] = *(const LAS bf16x8*)(la + kh * GA_KH + m * 1024);
; #pragma unroll
;             for (int n = 0; n < 4; ++n) {
;                 const s16x4 r0 = lds_tr(lb + kh * 32 * GB_ST + n * 32), r1 = lds_tr(lb + kh * 32 * GB_ST + n * 32 + bsw);
;                 bfr[n] = (bf16x8){r0[0], r0[1], r0[2], r0[3], r1[0], r1[1], r1[2], r1[3]};
;             }
; #pragma unroll
;             for (int m = 0; m < 4; ++m)
; #pragma unroll
;                 for (int n = 0; n < 4; ++n) acc[m][n] = __builtin_amdgcn_mfma_f32_16x16x32_bf16(bfr[n], af[m], acc[m][n], 0, 0, 0);
;         }
;     };
;     ...
;     gloadB(0, rb0); gloadA(0, ra0); gloadB(1, rb1);
;     for (int kt = 0; kt < nk; kt += 2) {
;         __syncthreads();
;         lstore(ra0, rb0);
;         __syncthreads();
;         gloadA(kt + 1, ra0);
;         if (kt + 2 < nk) gloadB(kt + 2, rb0);
;         compute();
;         __syncthreads();
;         lstore(ra0, rb1);
;         __syncthreads();
;         if (kt + 2 < nk) gloadA(kt + 2, ra0);
;         if (kt + 3 < nk) gloadB(kt + 3, rb1);
;         compute();
;     }
.Lm1_h1_last:
	ds_read_b64_tr_b16 v[174:175], v122 offset:53376
	ds_read_b64_tr_b16 v[176:177], v122 offset:54528
	ds_read_b128 v[158:161], v129 offset:36864
	ds_read_b64_tr_b16 v[178:179], v122 offset:53408
	ds_read_b64_tr_b16 v[180:181], v122 offset:54560
	s_waitcnt lgkmcnt(2)
	v_mfma_f32_16x16x32_bf16 v[112:115], v[174:177], v[158:161], v[112:115]
	ds_read_b64_tr_b16 v[182:183], v122 offset:53440
	ds_read_b64_tr_b16 v[184:185], v122 offset:54592
	s_waitcnt lgkmcnt(2)
	v_mfma_f32_16x16x32_bf16 v[104:107], v[178:181], v[158:161], v[104:107]
	ds_read_b64_tr_b16 v[186:187], v122 offset:53472
	ds_read_b64_tr_b16 v[188:189], v122 offset:54624
	s_waitcnt lgkmcnt(2)
	v_mfma_f32_16x16x32_bf16 v[108:111], v[182:185], v[158:161], v[108:111]
	ds_read_b128 v[162:165], v129 offset:37888
	s_waitcnt lgkmcnt(1)
	v_mfma_f32_16x16x32_bf16 v[100:103], v[186:189], v[158:161], v[100:103]
	ds_read_b128 v[166:169], v129 offset:38912
	s_waitcnt lgkmcnt(1)
	v_mfma_f32_16x16x32_bf16 v[96:99], v[174:177], v[162:165], v[96:99]
	ds_read_b128 v[170:173], v129 offset:39936
	v_mfma_f32_16x16x32_bf16 v[88:91], v[178:181], v[162:165], v[88:91]
	ds_read_b64_tr_b16 v[190:191], v122 offset:62592
	ds_read_b64_tr_b16 v[192:193], v122 offset:63744
	v_mfma_f32_16x16x32_bf16 v[92:95], v[182:185], v[162:165], v[92:95]
	ds_read_b64_tr_b16 v[132:133], v122 offset:62624
	ds_read_b64_tr_b16 v[134:135], v122 offset:63776
	v_mfma_f32_16x16x32_bf16 v[84:87], v[186:189], v[162:165], v[84:87]
	ds_read_b128 v[158:161], v129 offset:45120
	s_waitcnt lgkmcnt(6)
	v_mfma_f32_16x16x32_bf16 v[72:75], v[174:177], v[166:169], v[72:75]
	ds_read_b64_tr_b16 v[136:137], v122 offset:62656
	ds_read_b64_tr_b16 v[138:139], v122 offset:63808
	v_mfma_f32_16x16x32_bf16 v[28:31], v[178:181], v[166:169], v[28:31]
	ds_read_b64_tr_b16 v[140:141], v122 offset:62688
	ds_read_b64_tr_b16 v[142:143], v122 offset:63840
	v_mfma_f32_16x16x32_bf16 v[60:63], v[182:185], v[166:169], v[60:63]
	s_waitcnt vmcnt(8)
	ds_write_b128 v127, v[68:71]
	v_mfma_f32_16x16x32_bf16 v[20:23], v[186:189], v[166:169], v[20:23]
	ds_read_b128 v[162:165], v129 offset:46144
	s_waitcnt lgkmcnt(11)
	v_mfma_f32_16x16x32_bf16 v[12:15], v[174:177], v[170:173], v[12:15]
	ds_write_b128 v127, v[64:67] offset:2048
	v_mfma_f32_16x16x32_bf16 v[8:11], v[178:181], v[170:173], v[8:11]
	ds_write_b128 v127, v[80:83] offset:4096
	v_mfma_f32_16x16x32_bf16 v[16:19], v[182:185], v[170:173], v[16:19]
	ds_write_b128 v127, v[76:79] offset:6144
	v_mfma_f32_16x16x32_bf16 v[4:7], v[186:189], v[170:173], v[4:7]
	s_waitcnt lgkmcnt(10)
	ds_read_b128 v[166:169], v129 offset:47168
	s_waitcnt lgkmcnt(10)
	v_mfma_f32_16x16x32_bf16 v[112:115], v[190:193], v[158:161], v[112:115]
	ds_write_b128 v128, v[24:27] offset:16512
	v_mfma_f32_16x16x32_bf16 v[104:107], v[132:135], v[158:161], v[104:107]
	ds_write_b128 v128, v[32:35] offset:21120
	s_waitcnt lgkmcnt(10)
	v_mfma_f32_16x16x32_bf16 v[108:111], v[136:139], v[158:161], v[108:111]
	ds_write_b128 v128, v[36:39] offset:25728
	s_waitcnt lgkmcnt(9)
	v_mfma_f32_16x16x32_bf16 v[100:103], v[140:143], v[158:161], v[100:103]
	ds_read_b128 v[170:173], v129 offset:48192
	s_waitcnt lgkmcnt(8)
	v_mfma_f32_16x16x32_bf16 v[96:99], v[190:193], v[162:165], v[96:99]
	ds_write_b128 v128, v[40:43] offset:30336
	v_mfma_f32_16x16x32_bf16 v[88:91], v[132:135], v[162:165], v[88:91]
	v_mfma_f32_16x16x32_bf16 v[92:95], v[136:139], v[162:165], v[92:95]
	v_mfma_f32_16x16x32_bf16 v[84:87], v[140:143], v[162:165], v[84:87]
	s_waitcnt lgkmcnt(5)
	v_mfma_f32_16x16x32_bf16 v[72:75], v[190:193], v[166:169], v[72:75]
	v_mfma_f32_16x16x32_bf16 v[28:31], v[132:135], v[166:169], v[28:31]
	v_mfma_f32_16x16x32_bf16 v[60:63], v[136:139], v[166:169], v[60:63]
	v_mfma_f32_16x16x32_bf16 v[20:23], v[140:143], v[166:169], v[20:23]
	s_waitcnt lgkmcnt(1)
	v_mfma_f32_16x16x32_bf16 v[12:15], v[190:193], v[170:173], v[12:15]
	v_mfma_f32_16x16x32_bf16 v[8:11], v[132:135], v[170:173], v[8:11]
	v_mfma_f32_16x16x32_bf16 v[16:19], v[136:139], v[170:173], v[16:19]
	v_mfma_f32_16x16x32_bf16 v[4:7], v[140:143], v[170:173], v[4:7]
	s_waitcnt lgkmcnt(0)
	s_barrier
	ds_read_b64_tr_b16 v[174:175], v122 offset:16512
	ds_read_b64_tr_b16 v[176:177], v122 offset:17664
	ds_read_b128 v[158:161], v129
	ds_read_b64_tr_b16 v[178:179], v122 offset:16544
	ds_read_b64_tr_b16 v[180:181], v122 offset:17696
	s_waitcnt lgkmcnt(2)
	v_mfma_f32_16x16x32_bf16 v[112:115], v[174:177], v[158:161], v[112:115]
	ds_read_b64_tr_b16 v[182:183], v122 offset:16576
	ds_read_b64_tr_b16 v[184:185], v122 offset:17728
	s_waitcnt lgkmcnt(2)
	v_mfma_f32_16x16x32_bf16 v[104:107], v[178:181], v[158:161], v[104:107]
	ds_read_b64_tr_b16 v[186:187], v122 offset:16608
	ds_read_b64_tr_b16 v[188:189], v122 offset:17760
	s_waitcnt lgkmcnt(2)
	v_mfma_f32_16x16x32_bf16 v[108:111], v[182:185], v[158:161], v[108:111]
	ds_read_b128 v[162:165], v129 offset:1024
	s_waitcnt lgkmcnt(1)
	v_mfma_f32_16x16x32_bf16 v[100:103], v[186:189], v[158:161], v[100:103]
	ds_read_b128 v[166:169], v129 offset:2048
	s_waitcnt lgkmcnt(1)
	v_mfma_f32_16x16x32_bf16 v[96:99], v[174:177], v[162:165], v[96:99]
	ds_read_b128 v[170:173], v129 offset:3072
	v_mfma_f32_16x16x32_bf16 v[88:91], v[178:181], v[162:165], v[88:91]
	ds_read_b64_tr_b16 v[190:191], v122 offset:25728
	ds_read_b64_tr_b16 v[192:193], v122 offset:26880
	v_mfma_f32_16x16x32_bf16 v[92:95], v[182:185], v[162:165], v[92:95]
	ds_read_b64_tr_b16 v[132:133], v122 offset:25760
	ds_read_b64_tr_b16 v[134:135], v122 offset:26912
	v_mfma_f32_16x16x32_bf16 v[84:87], v[186:189], v[162:165], v[84:87]
	ds_read_b128 v[158:161], v129 offset:8256
	s_waitcnt lgkmcnt(6)
; #define LAS __attribute__((address_space(3)))
; __device__ __forceinline__ s16x4 lds_tr(lds_cptr p) { return __builtin_bit_cast(s16x4, __builtin_amdgcn_ds_read_tr16_b64_v4i16((LAS s16x4*)p)); }
;     ...
;     auto compute = [&]() __attribute__((always_inline)) {
; #pragma unroll
;         for (int kh = 0; kh < 2; ++kh) {
;             bf16x8 af[4], bfr[4];
; #pragma unroll
;             for (int m = 0; m < 4; ++m) af[m] = *(const LAS bf16x8*)(la + kh * GA_KH + m * 1024);
; #pragma unroll
;             for (int n = 0; n < 4; ++n) {
;                 const s16x4 r0 = lds_tr(lb + kh * 32 * GB_ST + n * 32), r1 = lds_tr(lb + kh * 32 * GB_ST + n * 32 + bsw);
;                 bfr[n] = (bf16x8){r0[0], r0[1], r0[2], r0[3], r1[0], r1[1], r1[2], r1[3]};
;             }
; #pragma unroll
;             for (int m = 0; m < 4; ++m)
; #pragma unroll
;                 for (int n = 0; n < 4; ++n) acc[m][n] = __builtin_amdgcn_mfma_f32_16x16x32_bf16(bfr[n], af[m], acc[m][n], 0, 0, 0);
;         }
;     };
;     ...
;     gloadB(0, rb0); gloadA(0, ra0); gloadB(1, rb1);
;     for (int kt = 0; kt < nk; kt += 2) {
;         __syncthreads();
;         lstore(ra0, rb0);
;         __syncthreads();
;         gloadA(kt + 1, ra0);
;         if (kt + 2 < nk) gloadB(kt + 2, rb0);
;         compute();
;         __syncthreads();
;         lstore(ra0, rb1);
;         __syncthreads();
;         if (kt + 2 < nk) gloadA(kt + 2, ra0);
;         if (kt + 3 < nk) gloadB(kt + 3, rb1);
;         compute();
;     }
	v_mfma_f32_16x16x32_bf16 v[72:75], v[174:177], v[166:169], v[72:75]
	ds_read_b64_tr_b16 v[136:137], v122 offset:25792
	ds_read_b64_tr_b16 v[138:139], v122 offset:26944
	v_mfma_f32_16x16x32_bf16 v[28:31], v[178:181], v[166:169], v[28:31]
	ds_read_b64_tr_b16 v[140:141], v122 offset:25824
	ds_read_b64_tr_b16 v[142:143], v122 offset:26976
	v_mfma_f32_16x16x32_bf16 v[60:63], v[182:185], v[166:169], v[60:63]
	s_waitcnt vmcnt(0)
	ds_write_b128 v127, v[198:201] offset:36864
	v_mfma_f32_16x16x32_bf16 v[20:23], v[186:189], v[166:169], v[20:23]
	ds_read_b128 v[162:165], v129 offset:9280
	s_waitcnt lgkmcnt(11)
	v_mfma_f32_16x16x32_bf16 v[12:15], v[174:177], v[170:173], v[12:15]
	ds_write_b128 v127, v[202:205] offset:38912
	v_mfma_f32_16x16x32_bf16 v[8:11], v[178:181], v[170:173], v[8:11]
	ds_write_b128 v127, v[206:209] offset:40960
	v_mfma_f32_16x16x32_bf16 v[16:19], v[182:185], v[170:173], v[16:19]
	ds_write_b128 v127, v[210:213] offset:43008
	v_mfma_f32_16x16x32_bf16 v[4:7], v[186:189], v[170:173], v[4:7]
	s_waitcnt lgkmcnt(10)
	ds_read_b128 v[166:169], v129 offset:10304
	s_waitcnt lgkmcnt(10)
	v_mfma_f32_16x16x32_bf16 v[112:115], v[190:193], v[158:161], v[112:115]
	ds_write_b128 v130, v[44:47] offset:16512
	v_mfma_f32_16x16x32_bf16 v[104:107], v[132:135], v[158:161], v[104:107]
	ds_write_b128 v130, v[48:51] offset:21120
	s_waitcnt lgkmcnt(10)
	v_mfma_f32_16x16x32_bf16 v[108:111], v[136:139], v[158:161], v[108:111]
	ds_write_b128 v130, v[52:55] offset:25728
	s_waitcnt lgkmcnt(9)
	v_mfma_f32_16x16x32_bf16 v[100:103], v[140:143], v[158:161], v[100:103]
	ds_read_b128 v[170:173], v129 offset:11328
	s_waitcnt lgkmcnt(8)
	v_mfma_f32_16x16x32_bf16 v[96:99], v[190:193], v[162:165], v[96:99]
	ds_write_b128 v130, v[56:59] offset:30336
	v_mfma_f32_16x16x32_bf16 v[88:91], v[132:135], v[162:165], v[88:91]
	v_mfma_f32_16x16x32_bf16 v[92:95], v[136:139], v[162:165], v[92:95]
	v_mfma_f32_16x16x32_bf16 v[84:87], v[140:143], v[162:165], v[84:87]
	s_waitcnt lgkmcnt(5)
	v_mfma_f32_16x16x32_bf16 v[72:75], v[190:193], v[166:169], v[72:75]
	v_mfma_f32_16x16x32_bf16 v[28:31], v[132:135], v[166:169], v[28:31]
	v_mfma_f32_16x16x32_bf16 v[60:63], v[136:139], v[166:169], v[60:63]
	v_mfma_f32_16x16x32_bf16 v[20:23], v[140:143], v[166:169], v[20:23]
	s_waitcnt lgkmcnt(1)
	v_mfma_f32_16x16x32_bf16 v[12:15], v[190:193], v[170:173], v[12:15]
	v_mfma_f32_16x16x32_bf16 v[8:11], v[132:135], v[170:173], v[8:11]
	v_mfma_f32_16x16x32_bf16 v[16:19], v[136:139], v[170:173], v[16:19]
	v_mfma_f32_16x16x32_bf16 v[4:7], v[140:143], v[170:173], v[4:7]
	s_waitcnt lgkmcnt(0)
	s_barrier
	ds_read_b64_tr_b16 v[174:175], v122 offset:53376
	ds_read_b64_tr_b16 v[176:177], v122 offset:54528
	ds_read_b128 v[158:161], v129 offset:36864
	ds_read_b64_tr_b16 v[178:179], v122 offset:53408
	ds_read_b64_tr_b16 v[180:181], v122 offset:54560
	s_waitcnt lgkmcnt(2)
	v_mfma_f32_16x16x32_bf16 v[112:115], v[174:177], v[158:161], v[112:115]
	ds_read_b64_tr_b16 v[182:183], v122 offset:53440
	ds_read_b64_tr_b16 v[184:185], v122 offset:54592
	s_waitcnt lgkmcnt(2)
	v_mfma_f32_16x16x32_bf16 v[104:107], v[178:181], v[158:161], v[104:107]
	ds_read_b64_tr_b16 v[186:187], v122 offset:53472
	ds_read_b64_tr_b16 v[188:189], v122 offset:54624
	s_waitcnt lgkmcnt(2)
	v_mfma_f32_16x16x32_bf16 v[108:111], v[182:185], v[158:161], v[108:111]
	ds_read_b128 v[162:165], v129 offset:37888
	s_waitcnt lgkmcnt(1)
	v_mfma_f32_16x16x32_bf16 v[100:103], v[186:189], v[158:161], v[100:103]
	ds_read_b128 v[166:169], v129 offset:38912
	s_waitcnt lgkmcnt(1)
	v_mfma_f32_16x16x32_bf16 v[96:99], v[174:177], v[162:165], v[96:99]
	ds_read_b128 v[170:173], v129 offset:39936
	v_mfma_f32_16x16x32_bf16 v[88:91], v[178:181], v[162:165], v[88:91]
	ds_read_b64_tr_b16 v[190:191], v122 offset:62592
	ds_read_b64_tr_b16 v[192:193], v122 offset:63744
	v_mfma_f32_16x16x32_bf16 v[92:95], v[182:185], v[162:165], v[92:95]
	ds_read_b64_tr_b16 v[132:133], v122 offset:62624
	ds_read_b64_tr_b16 v[134:135], v122 offset:63776
	v_mfma_f32_16x16x32_bf16 v[84:87], v[186:189], v[162:165], v[84:87]
	ds_read_b128 v[158:161], v129 offset:45120
	s_waitcnt lgkmcnt(6)
	v_mfma_f32_16x16x32_bf16 v[72:75], v[174:177], v[166:169], v[72:75]
	ds_read_b64_tr_b16 v[136:137], v122 offset:62656
	ds_read_b64_tr_b16 v[138:139], v122 offset:63808
	v_mfma_f32_16x16x32_bf16 v[28:31], v[178:181], v[166:169], v[28:31]
	ds_read_b64_tr_b16 v[140:141], v122 offset:62688
	ds_read_b64_tr_b16 v[142:143], v122 offset:63840
	v_mfma_f32_16x16x32_bf16 v[60:63], v[182:185], v[166:169], v[60:63]
	v_mfma_f32_16x16x32_bf16 v[20:23], v[186:189], v[166:169], v[20:23]
	ds_read_b128 v[162:165], v129 offset:46144
	s_waitcnt lgkmcnt(10)
	v_mfma_f32_16x16x32_bf16 v[12:15], v[174:177], v[170:173], v[12:15]
	v_mfma_f32_16x16x32_bf16 v[8:11], v[178:181], v[170:173], v[8:11]
	v_mfma_f32_16x16x32_bf16 v[16:19], v[182:185], v[170:173], v[16:19]
	v_mfma_f32_16x16x32_bf16 v[4:7], v[186:189], v[170:173], v[4:7]
	ds_read_b128 v[166:169], v129 offset:47168
	s_waitcnt lgkmcnt(6)
	v_mfma_f32_16x16x32_bf16 v[112:115], v[190:193], v[158:161], v[112:115]
	v_mfma_f32_16x16x32_bf16 v[104:107], v[132:135], v[158:161], v[104:107]
	s_waitcnt lgkmcnt(4)
	v_mfma_f32_16x16x32_bf16 v[108:111], v[136:139], v[158:161], v[108:111]
	s_waitcnt lgkmcnt(2)
	v_mfma_f32_16x16x32_bf16 v[100:103], v[140:143], v[158:161], v[100:103]
	ds_read_b128 v[170:173], v129 offset:48192
	s_waitcnt lgkmcnt(2)
	v_mfma_f32_16x16x32_bf16 v[96:99], v[190:193], v[162:165], v[96:99]
	v_mfma_f32_16x16x32_bf16 v[88:91], v[132:135], v[162:165], v[88:91]
	v_mfma_f32_16x16x32_bf16 v[92:95], v[136:139], v[162:165], v[92:95]
	v_mfma_f32_16x16x32_bf16 v[84:87], v[140:143], v[162:165], v[84:87]
	s_waitcnt lgkmcnt(1)
	v_mfma_f32_16x16x32_bf16 v[72:75], v[190:193], v[166:169], v[72:75]
	v_mfma_f32_16x16x32_bf16 v[28:31], v[132:135], v[166:169], v[28:31]
	v_mfma_f32_16x16x32_bf16 v[60:63], v[136:139], v[166:169], v[60:63]
	v_mfma_f32_16x16x32_bf16 v[20:23], v[140:143], v[166:169], v[20:23]
	s_waitcnt lgkmcnt(0)
	v_mfma_f32_16x16x32_bf16 v[12:15], v[190:193], v[170:173], v[12:15]
	v_mfma_f32_16x16x32_bf16 v[8:11], v[132:135], v[170:173], v[8:11]
	v_mfma_f32_16x16x32_bf16 v[16:19], v[136:139], v[170:173], v[16:19]
	v_mfma_f32_16x16x32_bf16 v[4:7], v[140:143], v[170:173], v[4:7]
	s_waitcnt lgkmcnt(0)
	s_barrier

;     ...
;     for (int i = 0; i < 4; ++i) ao[i] = arow((tid >> 3) + 32 * i) + (tid & 7) * 8;
;     const int bk = tid >> 4, bnc = tid & 15;
;     constexpr int NRB = B_F32 ? 8 : 4;
;     u32x4 ra0[4], ra1[4]; u32x4 rb0[NRB], rb1[NRB];
;     auto gloadA = [&](int kt, u32x4 (&ra)[4]) __attribute__((always_inline)) {
; #pragma unroll
;         for (int i = 0; i < 4; ++i) ra[i] = *(const u32x4*)(Abase + (ao[i] + kt * 64));
;     };
;     auto gloadB = [&](int kt, u32x4 (&rb)[NRB]) __attribute__((always_inline)) {
;         if (B_F32) {
;             const float* bp = (const float*)Bbase + (boff + (unsigned)((kt * 64 + bk) * ldb));
; #pragma unroll
;             for (int i = 0; i < 4; ++i) {
;                 if (bval) { rb[2 * i] = *(const u32x4*)(bp + (unsigned)(16 * i * ldb)); rb[2 * i + 1] = *(const u32x4*)(bp + (unsigned)(16 * i * ldb) + 4); }
;                 else { rb[2 * i] = (u32x4){0u, 0u, 0u, 0u}; rb[2 * i + 1] = rb[2 * i]; }
;             }
;         } else {
;             const bf16* bp = (const bf16*)Bbase + (boff + (unsigned)((kt * 64 + bk) * ldb));
; #pragma unroll
;             for (int i = 0; i < 4; ++i) rb[i] = bval ? *(const u32x4*)(bp + (unsigned)(16 * i * ldb)) : (u32x4){0u, 0u, 0u, 0u};
;         }
;     };
;     auto lstore = [&](const u32x4 (&ra)[4], const u32x4 (&rb)[NRB]) __attribute__((always_inline)) {
; #pragma unroll
;         for (int i = 0; i < 4; ++i) { const int row = (tid >> 3) + 32 * i, kc = tid & 7;
;             const u32x4 v = (kc & 1) ? (u32x4){ra[i][2], ra[i][3], ra[i][0], ra[i][1]} : ra[i];
;             *(u32x4*)(lds + (kc >> 2) * GA_KH + row * 64 + (kc & 3) * 16) = v; }
; #pragma unroll
;         for (int i = 0; i < 4; ++i) { const int k = bk + 16 * i;
;             u32x4 v;
;             if (B_F32) { const f32x4 x = __builtin_bit_cast(f32x4, rb[2 * i]), y = __builtin_bit_cast(f32x4, rb[2 * i + 1]);
;                 v[0] = pk2bf(x[0], x[1]); v[1] = pk2bf(x[2], x[3]); v[2] = pk2bf(y[0], y[1]); v[3] = pk2bf(y[2], y[3]); }
;             else v = rb[i];
;             *(u32x4*)(lds + GB_OFF + k * GB_ST + bnc * 16) = v; }
;     };
;     const lds_cptr la = (lds_cptr)lds + (wr * 64 + fr) * 64 + fq * 16;
;     const lds_cptr lb = (lds_cptr)lds + GB_OFF + (8 * fq + (fr >> 2) + (fq & 1) * 4) * GB_ST + wc * 128 + (fr & 3) * 8;
;     const int bsw = (fq & 1) ? -4 * GB_ST : 4 * GB_ST;
.LBB0_253:
	s_and_b64 vcc, exec, s[6:7]
	s_cbranch_vccz .LBB0_249
	s_waitcnt lgkmcnt(0)
	s_load_dwordx2 s[46:47], s[4:5], 0x130
	s_ashr_i32 s29, s28, 31
	s_and_b32 s6, s15, 0x380
	s_lshl_b64 s[18:19], s[28:29], 18
	v_mov_b32_e32 v12, 0
	s_waitcnt lgkmcnt(0)
	s_add_u32 s7, s46, s18
	s_addc_u32 s17, s47, s19
	s_add_u32 s50, s7, 0xdec6000
	s_addc_u32 s51, s17, 0
	s_lshl_b32 s7, s16, 7
	s_and_b32 s17, s7, 0x380
	s_add_u32 s7, s46, s44
	s_addc_u32 s29, s47, s45
	s_add_u32 s56, s7, 0x18995100
	s_addc_u32 s57, s29, 0
	v_lshl_add_u64 v[6:7], v[134:135], 1, s[50:51]
	v_lshl_add_u64 v[8:9], v[136:137], 1, s[50:51]
	v_or3_b32 v2, s17, v147, v155
	v_lshl_add_u64 v[6:7], v[138:139], 1, s[50:51]
	v_lshl_add_u64 v[8:9], v[2:3], 1, s[56:57]
	v_add_co_u32_e32 v6, vcc, s40, v8
	s_mov_b32 s7, 0x10000
	s_nop 0
	v_addc_co_u32_e32 v7, vcc, 0, v9, vcc
	v_add_co_u32_e32 v10, vcc, s7, v8
	s_mov_b32 s7, 0x18000
	s_nop 0
	v_addc_co_u32_e32 v11, vcc, 0, v9, vcc
	v_lshl_add_u64 v[4:5], v[132:133], 1, s[50:51]
	v_add_co_u32_e32 v6, vcc, s7, v8
	v_addc_co_u32_e32 v7, vcc, 0, v9, vcc
	v_lshl_add_u64 v[4:5], v[140:141], 1, s[50:51]
	v_lshl_add_u64 v[4:5], v[142:143], 1, s[50:51]
	v_lshl_add_u64 v[6:7], v[158:159], 1, s[50:51]
	v_lshl_add_u64 v[4:5], s[46:47], 0, v[164:165]
	v_lshl_add_u64 v[4:5], v[4:5], 0, s[18:19]
	s_mov_b64 s[18:19], 0xdec6180
	v_add_u32_e32 v2, s6, v163
	s_mov_b32 s6, 0
	v_lshl_add_u64 v[116:117], v[4:5], 0, s[18:19]
	v_mov_b32_e32 v118, v161
	v_lshlrev_b32_e32 v202, 1, v132
	v_add_u32_e32 v203, 0x10000, v202
	v_add_u32_e32 v204, 0x20000, v202
	v_add_u32_e32 v205, 0x30000, v202
	v_or3_b32 v206, s17, v147, v155
	v_lshlrev_b32_e32 v206, 1, v206
	v_add_u32_e32 v207, 0x8000, v206
	v_add_u32_e32 v208, 0x10000, v206
	v_add_u32_e32 v209, 0x18000, v206
	s_mov_b64 s[100:101], s[50:51]
	s_mov_b64 s[18:19], s[56:57]
	v_bfe_u32 v215, v156, 5, 2
	v_sub_u32_e32 v215, 0, v215
	v_and_b32_e32 v215, 3, v215
	v_lshlrev_b32_e32 v215, 4, v215
	v_xor_b32_e32 v210, v182, v215
	v_bfe_u32 v215, v156, 2, 2
	v_sub_u32_e32 v215, 0, v215
	v_and_b32_e32 v215, 3, v215
	v_lshlrev_b32_e32 v215, 4, v215
	v_xor_b32_e32 v211, v184, v215
	v_and_b32_e32 v212, 15, v156
	v_lshlrev_b32_e32 v212, 4, v212
	v_bfe_u32 v215, v156, 7, 1
	v_lshlrev_b32_e32 v215, 7, v215
	v_xor_b32_e32 v212, v212, v215
	v_lshrrev_b32_e32 v215, 4, v156
	v_mul_u32_u24_e32 v215, 0x120, v215
	v_add_u32_e32 v212, v212, v215
	v_add_u32_e32 v213, 0x9000, v212
	v_bfe_u32 v214, v156, 4, 2
	v_lshlrev_b32_e32 v214, 3, v214
	v_bfe_u32 v215, v156, 2, 2
	v_add_u32_e32 v214, v214, v215
	v_mul_u32_u24_e32 v214, 0x120, v214
	v_lshrrev_b32_e32 v215, 6, v156
	v_lshrrev_b32_e32 v216, 4, v156
	v_xor_b32_e32 v215, v215, v216
	v_and_b32_e32 v215, 1, v215
	v_lshlrev_b32_e32 v215, 7, v215
	v_and_b32_e32 v216, 3, v156
	v_lshlrev_b32_e32 v216, 3, v216
	v_or3_b32 v214, v214, v215, v216
	global_load_dwordx4 v[60:63], v202, s[100:101]
	global_load_dwordx4 v[68:71], v203, s[100:101]
	global_load_dwordx4 v[76:79], v204, s[100:101]
	global_load_dwordx4 v[80:83], v205, s[100:101]
	global_load_dwordx4 v[100:103], v206, s[18:19]
	global_load_dwordx4 v[104:107], v207, s[18:19]
	global_load_dwordx4 v[108:111], v208, s[18:19]
	global_load_dwordx4 v[112:115], v209, s[18:19]
	s_add_u32 s18, s18, 0x20000
	s_addc_u32 s19, s19, 0
	global_load_dwordx4 v[84:87], v202, s[100:101] offset:128
	global_load_dwordx4 v[88:91], v203, s[100:101] offset:128
	global_load_dwordx4 v[92:95], v204, s[100:101] offset:128
	global_load_dwordx4 v[96:99], v205, s[100:101] offset:128
	v_mov_b32_e32 v13, v12
	v_mov_b32_e32 v14, v12
	v_mov_b32_e32 v15, v12
	v_mov_b32_e32 v20, v12
	v_mov_b32_e32 v21, v12
	v_mov_b32_e32 v22, v12
	v_mov_b32_e32 v23, v12
	v_mov_b32_e32 v4, v12
	v_mov_b32_e32 v5, v12
	v_mov_b32_e32 v6, v12
	v_mov_b32_e32 v7, v12
	v_mov_b32_e32 v8, v12
	v_mov_b32_e32 v9, v12
	v_mov_b32_e32 v10, v12
	v_mov_b32_e32 v11, v12
	v_mov_b32_e32 v16, v12
	v_mov_b32_e32 v17, v12
	v_mov_b32_e32 v18, v12
	v_mov_b32_e32 v19, v12
	v_mov_b32_e32 v24, v12
	v_mov_b32_e32 v25, v12
	v_mov_b32_e32 v26, v12
	v_mov_b32_e32 v27, v12
	v_mov_b32_e32 v28, v12
	v_mov_b32_e32 v29, v12
	v_mov_b32_e32 v30, v12
	v_mov_b32_e32 v31, v12
	v_mov_b32_e32 v32, v12
	v_mov_b32_e32 v33, v12
	v_mov_b32_e32 v34, v12
	v_mov_b32_e32 v35, v12
	v_mov_b32_e32 v36, v12
	v_mov_b32_e32 v37, v12
	v_mov_b32_e32 v38, v12
	v_mov_b32_e32 v39, v12
	v_mov_b32_e32 v40, v12
	v_mov_b32_e32 v41, v12
	v_mov_b32_e32 v42, v12
	v_mov_b32_e32 v43, v12
	v_mov_b32_e32 v44, v12
	v_mov_b32_e32 v45, v12
	v_mov_b32_e32 v46, v12
	v_mov_b32_e32 v47, v12
	v_mov_b32_e32 v48, v12
	v_mov_b32_e32 v49, v12
	v_mov_b32_e32 v50, v12
	v_mov_b32_e32 v51, v12
	v_mov_b32_e32 v52, v12
	v_mov_b32_e32 v53, v12
	v_mov_b32_e32 v54, v12
	v_mov_b32_e32 v55, v12
	v_mov_b32_e32 v56, v12
	v_mov_b32_e32 v57, v12
	v_mov_b32_e32 v58, v12
	v_mov_b32_e32 v59, v12
	v_mov_b32_e32 v64, v12
	v_mov_b32_e32 v65, v12
	v_mov_b32_e32 v66, v12
	v_mov_b32_e32 v67, v12
	v_mov_b32_e32 v72, v12
	v_mov_b32_e32 v73, v12
	v_mov_b32_e32 v74, v12
	v_mov_b32_e32 v75, v12
	s_waitcnt vmcnt(4)
	s_barrier
	ds_write_b128 v210, v[60:63]
	ds_write_b128 v210, v[68:71] offset:2048
	ds_write_b128 v210, v[76:79] offset:4096
	ds_write_b128 v210, v[80:83] offset:6144
	ds_write_b128 v212, v[100:103] offset:16512
	ds_write_b128 v212, v[104:107] offset:21120
	ds_write_b128 v212, v[108:111] offset:25728
	ds_write_b128 v212, v[112:115] offset:30336
	global_load_dwordx4 v[100:103], v206, s[18:19]
	global_load_dwordx4 v[104:107], v207, s[18:19]
	global_load_dwordx4 v[108:111], v208, s[18:19]
	global_load_dwordx4 v[112:115], v209, s[18:19]
	global_load_dwordx4 v[60:63], v202, s[100:101] offset:256
	global_load_dwordx4 v[68:71], v203, s[100:101] offset:256
	global_load_dwordx4 v[76:79], v204, s[100:101] offset:256
	global_load_dwordx4 v[80:83], v205, s[100:101] offset:256
	s_add_u32 s18, s18, 0x20000
	s_addc_u32 s19, s19, 0
	s_add_u32 s98, s18, 0x20000
	s_addc_u32 s99, s19, 0
	s_waitcnt lgkmcnt(0)
	s_barrier
;     ...
;     auto lstore = [&](const u32x4 (&ra)[4], const u32x4 (&rb)[NRB]) __attribute__((always_inline)) {
; #pragma unroll
;         for (int i = 0; i < 4; ++i) { const int row = (tid >> 3) + 32 * i, kc = tid & 7;
;             const u32x4 v = (kc & 1) ? (u32x4){ra[i][2], ra[i][3], ra[i][0], ra[i][1]} : ra[i];
;             *(u32x4*)(lds + (kc >> 2) * GA_KH + row * 64 + (kc & 3) * 16) = v; }
; #pragma unroll
;         for (int i = 0; i < 4; ++i) { const int k = bk + 16 * i;
;             u32x4 v;
;             if (B_F32) { const f32x4 x = __builtin_bit_cast(f32x4, rb[2 * i]), y = __builtin_bit_cast(f32x4, rb[2 * i + 1]);
;                 v[0] = pk2bf(x[0], x[1]); v[1] = pk2bf(x[2], x[3]); v[2] = pk2bf(y[0], y[1]); v[3] = pk2bf(y[2], y[3]); }
;             else v = rb[i];
;             *(u32x4*)(lds + GB_OFF + k * GB_ST + bnc * 16) = v; }
;     };
;     const lds_cptr la = (lds_cptr)lds + (wr * 64 + fr) * 64 + fq * 16;
;     const lds_cptr lb = (lds_cptr)lds + GB_OFF + (8 * fq + (fr >> 2) + (fq & 1) * 4) * GB_ST + wc * 128 + (fr & 3) * 8;
;     const int bsw = (fq & 1) ? -4 * GB_ST : 4 * GB_ST;
;     auto compute = [&]() __attribute__((always_inline)) {
; #pragma unroll
;         for (int kh = 0; kh < 2; ++kh) {
;             bf16x8 af[4], bfr[4];
; #pragma unroll
;             for (int m = 0; m < 4; ++m) af[m] = *(const LAS bf16x8*)(la + kh * GA_KH + m * 1024);
; #pragma unroll
;             for (int n = 0; n < 4; ++n) {
;                 const s16x4 r0 = lds_tr(lb + kh * 32 * GB_ST + n * 32), r1 = lds_tr(lb + kh * 32 * GB_ST + n * 32 + bsw);
;                 bfr[n] = (bf16x8){r0[0], r0[1], r0[2], r0[3], r1[0], r1[1], r1[2], r1[3]};
;             }
; #pragma unroll
;             for (int m = 0; m < 4; ++m)
; #pragma unroll
;                 for (int n = 0; n < 4; ++n) acc[m][n] = __builtin_amdgcn_mfma_f32_16x16x32_bf16(bfr[n], af[m], acc[m][n], 0, 0, 0);
;         }
;     };
;     ...
;     gloadB(0, rb0); gloadA(0, ra0); gloadB(1, rb1);
;     for (int kt = 0; kt < nk; kt += 2) {
;         __syncthreads();
;         lstore(ra0, rb0);
;         __syncthreads();
;         gloadA(kt + 1, ra0);
;         if (kt + 2 < nk) gloadB(kt + 2, rb0);
;         compute();
;         __syncthreads();
;         lstore(ra0, rb1);
;         __syncthreads();
;         if (kt + 2 < nk) gloadA(kt + 2, ra0);
;         if (kt + 3 < nk) gloadB(kt + 3, rb1);
;         compute();
;     }
.Lop_loop:
	ds_read_b64_tr_b16 v[166:167], v214 offset:16512
	ds_read_b64_tr_b16 v[168:169], v214 offset:17664
	ds_read_b128 v[116:119], v211
	ds_read_b64_tr_b16 v[170:171], v214 offset:16544
	ds_read_b64_tr_b16 v[172:173], v214 offset:17696
	s_waitcnt lgkmcnt(2)
	v_mfma_f32_16x16x32_bf16 v[72:75], v[166:169], v[116:119], v[72:75]
	ds_read_b64_tr_b16 v[174:175], v214 offset:16576
	ds_read_b64_tr_b16 v[176:177], v214 offset:17728
	s_waitcnt lgkmcnt(2)
	v_mfma_f32_16x16x32_bf16 v[64:67], v[170:173], v[116:119], v[64:67]
	ds_read_b64_tr_b16 v[178:179], v214 offset:16608
	ds_read_b64_tr_b16 v[180:181], v214 offset:17760
	s_waitcnt lgkmcnt(2)
	v_mfma_f32_16x16x32_bf16 v[56:59], v[174:177], v[116:119], v[56:59]
	ds_read_b128 v[120:123], v211 offset:1024
	s_waitcnt lgkmcnt(1)
	v_mfma_f32_16x16x32_bf16 v[52:55], v[178:181], v[116:119], v[52:55]
	ds_read_b128 v[124:127], v211 offset:2048
	s_waitcnt lgkmcnt(1)
	v_mfma_f32_16x16x32_bf16 v[48:51], v[166:169], v[120:123], v[48:51]
	ds_read_b128 v[128:131], v211 offset:3072
	v_mfma_f32_16x16x32_bf16 v[44:47], v[170:173], v[120:123], v[44:47]
	ds_read_b64_tr_b16 v[186:187], v214 offset:25728
	ds_read_b64_tr_b16 v[188:189], v214 offset:26880
	v_mfma_f32_16x16x32_bf16 v[40:43], v[174:177], v[120:123], v[40:43]
	ds_read_b64_tr_b16 v[190:191], v214 offset:25760
	ds_read_b64_tr_b16 v[192:193], v214 offset:26912
	v_mfma_f32_16x16x32_bf16 v[36:39], v[178:181], v[120:123], v[36:39]
	ds_read_b128 v[116:119], v211 offset:8256
	s_waitcnt lgkmcnt(6)
	v_mfma_f32_16x16x32_bf16 v[32:35], v[166:169], v[124:127], v[32:35]
	ds_read_b64_tr_b16 v[194:195], v214 offset:25792
	ds_read_b64_tr_b16 v[196:197], v214 offset:26944
	v_mfma_f32_16x16x32_bf16 v[28:31], v[170:173], v[124:127], v[28:31]
	ds_read_b64_tr_b16 v[198:199], v214 offset:25824
	ds_read_b64_tr_b16 v[200:201], v214 offset:26976
	v_mfma_f32_16x16x32_bf16 v[24:27], v[174:177], v[124:127], v[24:27]
	s_waitcnt vmcnt(4)
	ds_write_b128 v210, v[84:87] offset:36864
	v_mfma_f32_16x16x32_bf16 v[16:19], v[178:181], v[124:127], v[16:19]
	ds_read_b128 v[120:123], v211 offset:9280
	s_waitcnt lgkmcnt(11)
	v_mfma_f32_16x16x32_bf16 v[8:11], v[166:169], v[128:131], v[8:11]
	ds_write_b128 v210, v[88:91] offset:38912
	v_mfma_f32_16x16x32_bf16 v[4:7], v[170:173], v[128:131], v[4:7]
	ds_write_b128 v210, v[92:95] offset:40960
	v_mfma_f32_16x16x32_bf16 v[20:23], v[174:177], v[128:131], v[20:23]
	ds_write_b128 v210, v[96:99] offset:43008
	v_mfma_f32_16x16x32_bf16 v[12:15], v[178:181], v[128:131], v[12:15]
	s_waitcnt lgkmcnt(10)
	ds_read_b128 v[124:127], v211 offset:10304
	s_waitcnt lgkmcnt(10)
	v_mfma_f32_16x16x32_bf16 v[72:75], v[186:189], v[116:119], v[72:75]
	ds_write_b128 v213, v[100:103] offset:16512
	v_mfma_f32_16x16x32_bf16 v[64:67], v[190:193], v[116:119], v[64:67]
	ds_write_b128 v213, v[104:107] offset:21120
	s_waitcnt lgkmcnt(10)
	v_mfma_f32_16x16x32_bf16 v[56:59], v[194:197], v[116:119], v[56:59]
	ds_write_b128 v213, v[108:111] offset:25728
	s_waitcnt lgkmcnt(9)
	v_mfma_f32_16x16x32_bf16 v[52:55], v[198:201], v[116:119], v[52:55]
	ds_read_b128 v[128:131], v211 offset:11328
	s_waitcnt lgkmcnt(8)
	v_mfma_f32_16x16x32_bf16 v[48:51], v[186:189], v[120:123], v[48:51]
	ds_write_b128 v213, v[112:115] offset:30336
	v_mfma_f32_16x16x32_bf16 v[44:47], v[190:193], v[120:123], v[44:47]
	global_load_dwordx4 v[100:103], v206, s[18:19]
	v_mfma_f32_16x16x32_bf16 v[40:43], v[194:197], v[120:123], v[40:43]
	global_load_dwordx4 v[104:107], v207, s[18:19]
	v_mfma_f32_16x16x32_bf16 v[36:39], v[198:201], v[120:123], v[36:39]
	global_load_dwordx4 v[108:111], v208, s[18:19]
	s_waitcnt lgkmcnt(5)
	v_mfma_f32_16x16x32_bf16 v[32:35], v[186:189], v[124:127], v[32:35]
	global_load_dwordx4 v[112:115], v209, s[18:19]
	v_mfma_f32_16x16x32_bf16 v[28:31], v[190:193], v[124:127], v[28:31]
	global_load_dwordx4 v[84:87], v202, s[100:101] offset:384
	v_mfma_f32_16x16x32_bf16 v[24:27], v[194:197], v[124:127], v[24:27]
	global_load_dwordx4 v[88:91], v203, s[100:101] offset:384
	v_mfma_f32_16x16x32_bf16 v[16:19], v[198:201], v[124:127], v[16:19]
	global_load_dwordx4 v[92:95], v204, s[100:101] offset:384
	s_waitcnt lgkmcnt(1)
	v_mfma_f32_16x16x32_bf16 v[8:11], v[186:189], v[128:131], v[8:11]
	global_load_dwordx4 v[96:99], v205, s[100:101] offset:384
	v_mfma_f32_16x16x32_bf16 v[4:7], v[190:193], v[128:131], v[4:7]
	v_mfma_f32_16x16x32_bf16 v[20:23], v[194:197], v[128:131], v[20:23]
	v_mfma_f32_16x16x32_bf16 v[12:15], v[198:201], v[128:131], v[12:15]
	s_waitcnt lgkmcnt(0)
	s_barrier
	s_cmp_lt_u32 s6, 12
	s_cbranch_scc0 .Lop_h1_last
;     ...
;     auto lstore = [&](const u32x4 (&ra)[4], const u32x4 (&rb)[NRB]) __attribute__((always_inline)) {
; #pragma unroll
;         for (int i = 0; i < 4; ++i) { const int row = (tid >> 3) + 32 * i, kc = tid & 7;
;             const u32x4 v = (kc & 1) ? (u32x4){ra[i][2], ra[i][3], ra[i][0], ra[i][1]} : ra[i];
;             *(u32x4*)(lds + (kc >> 2) * GA_KH + row * 64 + (kc & 3) * 16) = v; }
; #pragma unroll
;         for (int i = 0; i < 4; ++i) { const int k = bk + 16 * i;
;             u32x4 v;
;             if (B_F32) { const f32x4 x = __builtin_bit_cast(f32x4, rb[2 * i]), y = __builtin_bit_cast(f32x4, rb[2 * i + 1]);
;                 v[0] = pk2bf(x[0], x[1]); v[1] = pk2bf(x[2], x[3]); v[2] = pk2bf(y[0], y[1]); v[3] = pk2bf(y[2], y[3]); }
;             else v = rb[i];
;             *(u32x4*)(lds + GB_OFF + k * GB_ST + bnc * 16) = v; }
;     };
;     const lds_cptr la = (lds_cptr)lds + (wr * 64 + fr) * 64 + fq * 16;
;     const lds_cptr lb = (lds_cptr)lds + GB_OFF + (8 * fq + (fr >> 2) + (fq & 1) * 4) * GB_ST + wc * 128 + (fr & 3) * 8;
;     const int bsw = (fq & 1) ? -4 * GB_ST : 4 * GB_ST;
;     auto compute = [&]() __attribute__((always_inline)) {
; #pragma unroll
;         for (int kh = 0; kh < 2; ++kh) {
;             bf16x8 af[4], bfr[4];
; #pragma unroll
;             for (int m = 0; m < 4; ++m) af[m] = *(const LAS bf16x8*)(la + kh * GA_KH + m * 1024);
; #pragma unroll
;             for (int n = 0; n < 4; ++n) {
;                 const s16x4 r0 = lds_tr(lb + kh * 32 * GB_ST + n * 32), r1 = lds_tr(lb + kh * 32 * GB_ST + n * 32 + bsw);
;                 bfr[n] = (bf16x8){r0[0], r0[1], r0[2], r0[3], r1[0], r1[1], r1[2], r1[3]};
;             }
; #pragma unroll
;             for (int m = 0; m < 4; ++m)
; #pragma unroll
;                 for (int n = 0; n < 4; ++n) acc[m][n] = __builtin_amdgcn_mfma_f32_16x16x32_bf16(bfr[n], af[m], acc[m][n], 0, 0, 0);
;         }
;     };
;     ...
;     gloadB(0, rb0); gloadA(0, ra0); gloadB(1, rb1);
;     for (int kt = 0; kt < nk; kt += 2) {
;         __syncthreads();
;         lstore(ra0, rb0);
;         __syncthreads();
;         gloadA(kt + 1, ra0);
;         if (kt + 2 < nk) gloadB(kt + 2, rb0);
;         compute();
;         __syncthreads();
;         lstore(ra0, rb1);
;         __syncthreads();
;         if (kt + 2 < nk) gloadA(kt + 2, ra0);
;         if (kt + 3 < nk) gloadB(kt + 3, rb1);
;         compute();
;     }
	ds_read_b64_tr_b16 v[166:167], v214 offset:53376
	ds_read_b64_tr_b16 v[168:169], v214 offset:54528
	ds_read_b128 v[116:119], v211 offset:36864
	ds_read_b64_tr_b16 v[170:171], v214 offset:53408
	ds_read_b64_tr_b16 v[172:173], v214 offset:54560
	s_waitcnt lgkmcnt(2)
	v_mfma_f32_16x16x32_bf16 v[72:75], v[166:169], v[116:119], v[72:75]
	ds_read_b64_tr_b16 v[174:175], v214 offset:53440
	ds_read_b64_tr_b16 v[176:177], v214 offset:54592
	s_waitcnt lgkmcnt(2)
	v_mfma_f32_16x16x32_bf16 v[64:67], v[170:173], v[116:119], v[64:67]
	ds_read_b64_tr_b16 v[178:179], v214 offset:53472
	ds_read_b64_tr_b16 v[180:181], v214 offset:54624
	s_waitcnt lgkmcnt(2)
	v_mfma_f32_16x16x32_bf16 v[56:59], v[174:177], v[116:119], v[56:59]
	ds_read_b128 v[120:123], v211 offset:37888
	s_waitcnt lgkmcnt(1)
	v_mfma_f32_16x16x32_bf16 v[52:55], v[178:181], v[116:119], v[52:55]
	ds_read_b128 v[124:127], v211 offset:38912
	s_waitcnt lgkmcnt(1)
	v_mfma_f32_16x16x32_bf16 v[48:51], v[166:169], v[120:123], v[48:51]
	ds_read_b128 v[128:131], v211 offset:39936
	v_mfma_f32_16x16x32_bf16 v[44:47], v[170:173], v[120:123], v[44:47]
	ds_read_b64_tr_b16 v[186:187], v214 offset:62592
	ds_read_b64_tr_b16 v[188:189], v214 offset:63744
	v_mfma_f32_16x16x32_bf16 v[40:43], v[174:177], v[120:123], v[40:43]
	ds_read_b64_tr_b16 v[190:191], v214 offset:62624
	ds_read_b64_tr_b16 v[192:193], v214 offset:63776
	v_mfma_f32_16x16x32_bf16 v[36:39], v[178:181], v[120:123], v[36:39]
	ds_read_b128 v[116:119], v211 offset:45120
	s_waitcnt lgkmcnt(6)
	v_mfma_f32_16x16x32_bf16 v[32:35], v[166:169], v[124:127], v[32:35]
	ds_read_b64_tr_b16 v[194:195], v214 offset:62656
	ds_read_b64_tr_b16 v[196:197], v214 offset:63808
	v_mfma_f32_16x16x32_bf16 v[28:31], v[170:173], v[124:127], v[28:31]
	ds_read_b64_tr_b16 v[198:199], v214 offset:62688
	ds_read_b64_tr_b16 v[200:201], v214 offset:63840
	v_mfma_f32_16x16x32_bf16 v[24:27], v[174:177], v[124:127], v[24:27]
	s_waitcnt vmcnt(4)
	ds_write_b128 v210, v[60:63]
	v_mfma_f32_16x16x32_bf16 v[16:19], v[178:181], v[124:127], v[16:19]
	ds_read_b128 v[120:123], v211 offset:46144
	s_waitcnt lgkmcnt(11)
	v_mfma_f32_16x16x32_bf16 v[8:11], v[166:169], v[128:131], v[8:11]
	ds_write_b128 v210, v[68:71] offset:2048
	v_mfma_f32_16x16x32_bf16 v[4:7], v[170:173], v[128:131], v[4:7]
	ds_write_b128 v210, v[76:79] offset:4096
	v_mfma_f32_16x16x32_bf16 v[20:23], v[174:177], v[128:131], v[20:23]
	ds_write_b128 v210, v[80:83] offset:6144
	v_mfma_f32_16x16x32_bf16 v[12:15], v[178:181], v[128:131], v[12:15]
	s_waitcnt lgkmcnt(10)
	ds_read_b128 v[124:127], v211 offset:47168
	s_waitcnt lgkmcnt(10)
	v_mfma_f32_16x16x32_bf16 v[72:75], v[186:189], v[116:119], v[72:75]
	ds_write_b128 v212, v[100:103] offset:16512
	v_mfma_f32_16x16x32_bf16 v[64:67], v[190:193], v[116:119], v[64:67]
	ds_write_b128 v212, v[104:107] offset:21120
	s_waitcnt lgkmcnt(10)
	v_mfma_f32_16x16x32_bf16 v[56:59], v[194:197], v[116:119], v[56:59]
	ds_write_b128 v212, v[108:111] offset:25728
	s_waitcnt lgkmcnt(9)
	v_mfma_f32_16x16x32_bf16 v[52:55], v[198:201], v[116:119], v[52:55]
	ds_read_b128 v[128:131], v211 offset:48192
	s_waitcnt lgkmcnt(8)
	v_mfma_f32_16x16x32_bf16 v[48:51], v[186:189], v[120:123], v[48:51]
	ds_write_b128 v212, v[112:115] offset:30336
	v_mfma_f32_16x16x32_bf16 v[44:47], v[190:193], v[120:123], v[44:47]
	global_load_dwordx4 v[100:103], v206, s[98:99]
	v_mfma_f32_16x16x32_bf16 v[40:43], v[194:197], v[120:123], v[40:43]
	global_load_dwordx4 v[104:107], v207, s[98:99]
	v_mfma_f32_16x16x32_bf16 v[36:39], v[198:201], v[120:123], v[36:39]
	global_load_dwordx4 v[108:111], v208, s[98:99]
	s_waitcnt lgkmcnt(5)
	v_mfma_f32_16x16x32_bf16 v[32:35], v[186:189], v[124:127], v[32:35]
	global_load_dwordx4 v[112:115], v209, s[98:99]
	v_mfma_f32_16x16x32_bf16 v[28:31], v[190:193], v[124:127], v[28:31]
	global_load_dwordx4 v[60:63], v202, s[100:101] offset:512
	v_mfma_f32_16x16x32_bf16 v[24:27], v[194:197], v[124:127], v[24:27]
	global_load_dwordx4 v[68:71], v203, s[100:101] offset:512
	v_mfma_f32_16x16x32_bf16 v[16:19], v[198:201], v[124:127], v[16:19]
	global_load_dwordx4 v[76:79], v204, s[100:101] offset:512
	s_waitcnt lgkmcnt(1)
	v_mfma_f32_16x16x32_bf16 v[8:11], v[186:189], v[128:131], v[8:11]
	global_load_dwordx4 v[80:83], v205, s[100:101] offset:512
	v_mfma_f32_16x16x32_bf16 v[4:7], v[190:193], v[128:131], v[4:7]
	v_mfma_f32_16x16x32_bf16 v[20:23], v[194:197], v[128:131], v[20:23]
	v_mfma_f32_16x16x32_bf16 v[12:15], v[198:201], v[128:131], v[12:15]
	s_waitcnt lgkmcnt(0)
	s_barrier
	s_add_u32 s100, s100, 0x100
	s_addc_u32 s101, s101, 0
	s_add_u32 s18, s18, 0x40000
	s_addc_u32 s19, s19, 0
	s_add_u32 s98, s98, 0x40000
	s_addc_u32 s99, s99, 0
	s_add_i32 s6, s6, 2
	s_branch .Lop_loop
;     ...
;     auto lstore = [&](const u32x4 (&ra)[4], const u32x4 (&rb)[NRB]) __attribute__((always_inline)) {
; #pragma unroll
;         for (int i = 0; i < 4; ++i) { const int row = (tid >> 3) + 32 * i, kc = tid & 7;
;             const u32x4 v = (kc & 1) ? (u32x4){ra[i][2], ra[i][3], ra[i][0], ra[i][1]} : ra[i];
;             *(u32x4*)(lds + (kc >> 2) * GA_KH + row * 64 + (kc & 3) * 16) = v; }
; #pragma unroll
;         for (int i = 0; i < 4; ++i) { const int k = bk + 16 * i;
;             u32x4 v;
;             if (B_F32) { const f32x4 x = __builtin_bit_cast(f32x4, rb[2 * i]), y = __builtin_bit_cast(f32x4, rb[2 * i + 1]);
;                 v[0] = pk2bf(x[0], x[1]); v[1] = pk2bf(x[2], x[3]); v[2] = pk2bf(y[0], y[1]); v[3] = pk2bf(y[2], y[3]); }
;             else v = rb[i];
;             *(u32x4*)(lds + GB_OFF + k * GB_ST + bnc * 16) = v; }
;     };
;     const lds_cptr la = (lds_cptr)lds + (wr * 64 + fr) * 64 + fq * 16;
;     const lds_cptr lb = (lds_cptr)lds + GB_OFF + (8 * fq + (fr >> 2) + (fq & 1) * 4) * GB_ST + wc * 128 + (fr & 3) * 8;
;     const int bsw = (fq & 1) ? -4 * GB_ST : 4 * GB_ST;
;     auto compute = [&]() __attribute__((always_inline)) {
; #pragma unroll
;         for (int kh = 0; kh < 2; ++kh) {
;             bf16x8 af[4], bfr[4];
; #pragma unroll
;             for (int m = 0; m < 4; ++m) af[m] = *(const LAS bf16x8*)(la + kh * GA_KH + m * 1024);
; #pragma unroll
;             for (int n = 0; n < 4; ++n) {
;                 const s16x4 r0 = lds_tr(lb + kh * 32 * GB_ST + n * 32), r1 = lds_tr(lb + kh * 32 * GB_ST + n * 32 + bsw);
;                 bfr[n] = (bf16x8){r0[0], r0[1], r0[2], r0[3], r1[0], r1[1], r1[2], r1[3]};
;             }
; #pragma unroll
;             for (int m = 0; m < 4; ++m)
; #pragma unroll
;                 for (int n = 0; n < 4; ++n) acc[m][n] = __builtin_amdgcn_mfma_f32_16x16x32_bf16(bfr[n], af[m], acc[m][n], 0, 0, 0);
;         }
;     };
;     ...
;     gloadB(0, rb0); gloadA(0, ra0); gloadB(1, rb1);
;     for (int kt = 0; kt < nk; kt += 2) {
;         __syncthreads();
;         lstore(ra0, rb0);
;         __syncthreads();
;         gloadA(kt + 1, ra0);
;         if (kt + 2 < nk) gloadB(kt + 2, rb0);
;         compute();
;         __syncthreads();
;         lstore(ra0, rb1);
;         __syncthreads();
;         if (kt + 2 < nk) gloadA(kt + 2, ra0);
;         if (kt + 3 < nk) gloadB(kt + 3, rb1);
;         compute();
;     }
.Lop_h1_last:
	ds_read_b64_tr_b16 v[166:167], v214 offset:53376
	ds_read_b64_tr_b16 v[168:169], v214 offset:54528
	ds_read_b128 v[116:119], v211 offset:36864
	ds_read_b64_tr_b16 v[170:171], v214 offset:53408
	ds_read_b64_tr_b16 v[172:173], v214 offset:54560
	s_waitcnt lgkmcnt(2)
	v_mfma_f32_16x16x32_bf16 v[72:75], v[166:169], v[116:119], v[72:75]
	ds_read_b64_tr_b16 v[174:175], v214 offset:53440
	ds_read_b64_tr_b16 v[176:177], v214 offset:54592
	s_waitcnt lgkmcnt(2)
	v_mfma_f32_16x16x32_bf16 v[64:67], v[170:173], v[116:119], v[64:67]
	ds_read_b64_tr_b16 v[178:179], v214 offset:53472
	ds_read_b64_tr_b16 v[180:181], v214 offset:54624
	s_waitcnt lgkmcnt(2)
	v_mfma_f32_16x16x32_bf16 v[56:59], v[174:177], v[116:119], v[56:59]
	ds_read_b128 v[120:123], v211 offset:37888
	s_waitcnt lgkmcnt(1)
	v_mfma_f32_16x16x32_bf16 v[52:55], v[178:181], v[116:119], v[52:55]
	ds_read_b128 v[124:127], v211 offset:38912
	s_waitcnt lgkmcnt(1)
	v_mfma_f32_16x16x32_bf16 v[48:51], v[166:169], v[120:123], v[48:51]
	ds_read_b128 v[128:131], v211 offset:39936
	v_mfma_f32_16x16x32_bf16 v[44:47], v[170:173], v[120:123], v[44:47]
	ds_read_b64_tr_b16 v[186:187], v214 offset:62592
	ds_read_b64_tr_b16 v[188:189], v214 offset:63744
	v_mfma_f32_16x16x32_bf16 v[40:43], v[174:177], v[120:123], v[40:43]
	ds_read_b64_tr_b16 v[190:191], v214 offset:62624
	ds_read_b64_tr_b16 v[192:193], v214 offset:63776
	v_mfma_f32_16x16x32_bf16 v[36:39], v[178:181], v[120:123], v[36:39]
	ds_read_b128 v[116:119], v211 offset:45120
	s_waitcnt lgkmcnt(6)
	v_mfma_f32_16x16x32_bf16 v[32:35], v[166:169], v[124:127], v[32:35]
	ds_read_b64_tr_b16 v[194:195], v214 offset:62656
	ds_read_b64_tr_b16 v[196:197], v214 offset:63808
	v_mfma_f32_16x16x32_bf16 v[28:31], v[170:173], v[124:127], v[28:31]
	ds_read_b64_tr_b16 v[198:199], v214 offset:62688
	ds_read_b64_tr_b16 v[200:201], v214 offset:63840
	v_mfma_f32_16x16x32_bf16 v[24:27], v[174:177], v[124:127], v[24:27]
	s_waitcnt vmcnt(4)
	ds_write_b128 v210, v[60:63]
	v_mfma_f32_16x16x32_bf16 v[16:19], v[178:181], v[124:127], v[16:19]
	ds_read_b128 v[120:123], v211 offset:46144
	s_waitcnt lgkmcnt(11)
	v_mfma_f32_16x16x32_bf16 v[8:11], v[166:169], v[128:131], v[8:11]
	ds_write_b128 v210, v[68:71] offset:2048
	v_mfma_f32_16x16x32_bf16 v[4:7], v[170:173], v[128:131], v[4:7]
	ds_write_b128 v210, v[76:79] offset:4096
	v_mfma_f32_16x16x32_bf16 v[20:23], v[174:177], v[128:131], v[20:23]
	ds_write_b128 v210, v[80:83] offset:6144
	v_mfma_f32_16x16x32_bf16 v[12:15], v[178:181], v[128:131], v[12:15]
	s_waitcnt lgkmcnt(10)
	ds_read_b128 v[124:127], v211 offset:47168
	s_waitcnt lgkmcnt(10)
	v_mfma_f32_16x16x32_bf16 v[72:75], v[186:189], v[116:119], v[72:75]
	ds_write_b128 v212, v[100:103] offset:16512
	v_mfma_f32_16x16x32_bf16 v[64:67], v[190:193], v[116:119], v[64:67]
	ds_write_b128 v212, v[104:107] offset:21120
	s_waitcnt lgkmcnt(10)
	v_mfma_f32_16x16x32_bf16 v[56:59], v[194:197], v[116:119], v[56:59]
	ds_write_b128 v212, v[108:111] offset:25728
	s_waitcnt lgkmcnt(9)
	v_mfma_f32_16x16x32_bf16 v[52:55], v[198:201], v[116:119], v[52:55]
	ds_read_b128 v[128:131], v211 offset:48192
	s_waitcnt lgkmcnt(8)
	v_mfma_f32_16x16x32_bf16 v[48:51], v[186:189], v[120:123], v[48:51]
	ds_write_b128 v212, v[112:115] offset:30336
	v_mfma_f32_16x16x32_bf16 v[44:47], v[190:193], v[120:123], v[44:47]
	global_load_dwordx4 v[100:103], v206, s[98:99]
	v_mfma_f32_16x16x32_bf16 v[40:43], v[194:197], v[120:123], v[40:43]
	global_load_dwordx4 v[104:107], v207, s[98:99]
	v_mfma_f32_16x16x32_bf16 v[36:39], v[198:201], v[120:123], v[36:39]
	global_load_dwordx4 v[108:111], v208, s[98:99]
	s_waitcnt lgkmcnt(5)
	v_mfma_f32_16x16x32_bf16 v[32:35], v[186:189], v[124:127], v[32:35]
	global_load_dwordx4 v[112:115], v209, s[98:99]
	v_mfma_f32_16x16x32_bf16 v[28:31], v[190:193], v[124:127], v[28:31]
	v_mfma_f32_16x16x32_bf16 v[24:27], v[194:197], v[124:127], v[24:27]
	v_mfma_f32_16x16x32_bf16 v[16:19], v[198:201], v[124:127], v[16:19]
	s_waitcnt lgkmcnt(1)
	v_mfma_f32_16x16x32_bf16 v[8:11], v[186:189], v[128:131], v[8:11]
	v_mfma_f32_16x16x32_bf16 v[4:7], v[190:193], v[128:131], v[4:7]
	v_mfma_f32_16x16x32_bf16 v[20:23], v[194:197], v[128:131], v[20:23]
	v_mfma_f32_16x16x32_bf16 v[12:15], v[198:201], v[128:131], v[12:15]
	s_waitcnt lgkmcnt(0)
	s_barrier
;     ...
;     auto lstore = [&](const u32x4 (&ra)[4], const u32x4 (&rb)[NRB]) __attribute__((always_inline)) {
; #pragma unroll
;         for (int i = 0; i < 4; ++i) { const int row = (tid >> 3) + 32 * i, kc = tid & 7;
;             const u32x4 v = (kc & 1) ? (u32x4){ra[i][2], ra[i][3], ra[i][0], ra[i][1]} : ra[i];
;             *(u32x4*)(lds + (kc >> 2) * GA_KH + row * 64 + (kc & 3) * 16) = v; }
; #pragma unroll
;         for (int i = 0; i < 4; ++i) { const int k = bk + 16 * i;
;             u32x4 v;
;             if (B_F32) { const f32x4 x = __builtin_bit_cast(f32x4, rb[2 * i]), y = __builtin_bit_cast(f32x4, rb[2 * i + 1]);
;                 v[0] = pk2bf(x[0], x[1]); v[1] = pk2bf(x[2], x[3]); v[2] = pk2bf(y[0], y[1]); v[3] = pk2bf(y[2], y[3]); }
;             else v = rb[i];
;             *(u32x4*)(lds + GB_OFF + k * GB_ST + bnc * 16) = v; }
;     };
;     const lds_cptr la = (lds_cptr)lds + (wr * 64 + fr) * 64 + fq * 16;
;     const lds_cptr lb = (lds_cptr)lds + GB_OFF + (8 * fq + (fr >> 2) + (fq & 1) * 4) * GB_ST + wc * 128 + (fr & 3) * 8;
;     const int bsw = (fq & 1) ? -4 * GB_ST : 4 * GB_ST;
;     auto compute = [&]() __attribute__((always_inline)) {
; #pragma unroll
;         for (int kh = 0; kh < 2; ++kh) {
;             bf16x8 af[4], bfr[4];
; #pragma unroll
;             for (int m = 0; m < 4; ++m) af[m] = *(const LAS bf16x8*)(la + kh * GA_KH + m * 1024);
; #pragma unroll
;             for (int n = 0; n < 4; ++n) {
;                 const s16x4 r0 = lds_tr(lb + kh * 32 * GB_ST + n * 32), r1 = lds_tr(lb + kh * 32 * GB_ST + n * 32 + bsw);
;                 bfr[n] = (bf16x8){r0[0], r0[1], r0[2], r0[3], r1[0], r1[1], r1[2], r1[3]};
;             }
; #pragma unroll
;             for (int m = 0; m < 4; ++m)
; #pragma unroll
;                 for (int n = 0; n < 4; ++n) acc[m][n] = __builtin_amdgcn_mfma_f32_16x16x32_bf16(bfr[n], af[m], acc[m][n], 0, 0, 0);
;         }
;     };
;     ...
;     gloadB(0, rb0); gloadA(0, ra0); gloadB(1, rb1);
;     for (int kt = 0; kt < nk; kt += 2) {
;         __syncthreads();
;         lstore(ra0, rb0);
;         __syncthreads();
;         gloadA(kt + 1, ra0);
;         if (kt + 2 < nk) gloadB(kt + 2, rb0);
;         compute();
;         __syncthreads();
;         lstore(ra0, rb1);
;         __syncthreads();
;         if (kt + 2 < nk) gloadA(kt + 2, ra0);
;         if (kt + 3 < nk) gloadB(kt + 3, rb1);
;         compute();
;     }
	ds_read_b64_tr_b16 v[166:167], v214 offset:16512
	ds_read_b64_tr_b16 v[168:169], v214 offset:17664
	ds_read_b128 v[116:119], v211
	ds_read_b64_tr_b16 v[170:171], v214 offset:16544
	ds_read_b64_tr_b16 v[172:173], v214 offset:17696
	s_waitcnt lgkmcnt(2)
	v_mfma_f32_16x16x32_bf16 v[72:75], v[166:169], v[116:119], v[72:75]
	ds_read_b64_tr_b16 v[174:175], v214 offset:16576
	ds_read_b64_tr_b16 v[176:177], v214 offset:17728
	s_waitcnt lgkmcnt(2)
	v_mfma_f32_16x16x32_bf16 v[64:67], v[170:173], v[116:119], v[64:67]
	ds_read_b64_tr_b16 v[178:179], v214 offset:16608
	ds_read_b64_tr_b16 v[180:181], v214 offset:17760
	s_waitcnt lgkmcnt(2)
	v_mfma_f32_16x16x32_bf16 v[56:59], v[174:177], v[116:119], v[56:59]
	ds_read_b128 v[120:123], v211 offset:1024
	s_waitcnt lgkmcnt(1)
	v_mfma_f32_16x16x32_bf16 v[52:55], v[178:181], v[116:119], v[52:55]
	ds_read_b128 v[124:127], v211 offset:2048
	s_waitcnt lgkmcnt(1)
	v_mfma_f32_16x16x32_bf16 v[48:51], v[166:169], v[120:123], v[48:51]
	ds_read_b128 v[128:131], v211 offset:3072
	v_mfma_f32_16x16x32_bf16 v[44:47], v[170:173], v[120:123], v[44:47]
	ds_read_b64_tr_b16 v[186:187], v214 offset:25728
	ds_read_b64_tr_b16 v[188:189], v214 offset:26880
	v_mfma_f32_16x16x32_bf16 v[40:43], v[174:177], v[120:123], v[40:43]
	ds_read_b64_tr_b16 v[190:191], v214 offset:25760
	ds_read_b64_tr_b16 v[192:193], v214 offset:26912
	v_mfma_f32_16x16x32_bf16 v[36:39], v[178:181], v[120:123], v[36:39]
	ds_read_b128 v[116:119], v211 offset:8256
	s_waitcnt lgkmcnt(6)
	v_mfma_f32_16x16x32_bf16 v[32:35], v[166:169], v[124:127], v[32:35]
	ds_read_b64_tr_b16 v[194:195], v214 offset:25792
	ds_read_b64_tr_b16 v[196:197], v214 offset:26944
	v_mfma_f32_16x16x32_bf16 v[28:31], v[170:173], v[124:127], v[28:31]
	ds_read_b64_tr_b16 v[198:199], v214 offset:25824
	ds_read_b64_tr_b16 v[200:201], v214 offset:26976
	v_mfma_f32_16x16x32_bf16 v[24:27], v[174:177], v[124:127], v[24:27]
	s_waitcnt vmcnt(0)
	ds_write_b128 v210, v[84:87] offset:36864
	v_mfma_f32_16x16x32_bf16 v[16:19], v[178:181], v[124:127], v[16:19]
	ds_read_b128 v[120:123], v211 offset:9280
	s_waitcnt lgkmcnt(11)
	v_mfma_f32_16x16x32_bf16 v[8:11], v[166:169], v[128:131], v[8:11]
	ds_write_b128 v210, v[88:91] offset:38912
	v_mfma_f32_16x16x32_bf16 v[4:7], v[170:173], v[128:131], v[4:7]
	ds_write_b128 v210, v[92:95] offset:40960
	v_mfma_f32_16x16x32_bf16 v[20:23], v[174:177], v[128:131], v[20:23]
	ds_write_b128 v210, v[96:99] offset:43008
	v_mfma_f32_16x16x32_bf16 v[12:15], v[178:181], v[128:131], v[12:15]
	s_waitcnt lgkmcnt(10)
	ds_read_b128 v[124:127], v211 offset:10304
	s_waitcnt lgkmcnt(10)
	v_mfma_f32_16x16x32_bf16 v[72:75], v[186:189], v[116:119], v[72:75]
	ds_write_b128 v213, v[100:103] offset:16512
	v_mfma_f32_16x16x32_bf16 v[64:67], v[190:193], v[116:119], v[64:67]
	ds_write_b128 v213, v[104:107] offset:21120
	s_waitcnt lgkmcnt(10)
	v_mfma_f32_16x16x32_bf16 v[56:59], v[194:197], v[116:119], v[56:59]
	ds_write_b128 v213, v[108:111] offset:25728
	s_waitcnt lgkmcnt(9)
	v_mfma_f32_16x16x32_bf16 v[52:55], v[198:201], v[116:119], v[52:55]
	ds_read_b128 v[128:131], v211 offset:11328
	s_waitcnt lgkmcnt(8)
	v_mfma_f32_16x16x32_bf16 v[48:51], v[186:189], v[120:123], v[48:51]
	ds_write_b128 v213, v[112:115] offset:30336
	v_mfma_f32_16x16x32_bf16 v[44:47], v[190:193], v[120:123], v[44:47]
	v_mfma_f32_16x16x32_bf16 v[40:43], v[194:197], v[120:123], v[40:43]
	v_mfma_f32_16x16x32_bf16 v[36:39], v[198:201], v[120:123], v[36:39]
	s_waitcnt lgkmcnt(5)
	v_mfma_f32_16x16x32_bf16 v[32:35], v[186:189], v[124:127], v[32:35]
	v_mfma_f32_16x16x32_bf16 v[28:31], v[190:193], v[124:127], v[28:31]
	v_mfma_f32_16x16x32_bf16 v[24:27], v[194:197], v[124:127], v[24:27]
	v_mfma_f32_16x16x32_bf16 v[16:19], v[198:201], v[124:127], v[16:19]
	s_waitcnt lgkmcnt(1)
	v_mfma_f32_16x16x32_bf16 v[8:11], v[186:189], v[128:131], v[8:11]
	v_mfma_f32_16x16x32_bf16 v[4:7], v[190:193], v[128:131], v[4:7]
	v_mfma_f32_16x16x32_bf16 v[20:23], v[194:197], v[128:131], v[20:23]
	v_mfma_f32_16x16x32_bf16 v[12:15], v[198:201], v[128:131], v[12:15]
	s_waitcnt lgkmcnt(0)
	s_barrier
;     ...
;     auto lstore = [&](const u32x4 (&ra)[4], const u32x4 (&rb)[NRB]) __attribute__((always_inline)) {
; #pragma unroll
;         for (int i = 0; i < 4; ++i) { const int row = (tid >> 3) + 32 * i, kc = tid & 7;
;             const u32x4 v = (kc & 1) ? (u32x4){ra[i][2], ra[i][3], ra[i][0], ra[i][1]} : ra[i];
;             *(u32x4*)(lds + (kc >> 2) * GA_KH + row * 64 + (kc & 3) * 16) = v; }
; #pragma unroll
;         for (int i = 0; i < 4; ++i) { const int k = bk + 16 * i;
;             u32x4 v;
;             if (B_F32) { const f32x4 x = __builtin_bit_cast(f32x4, rb[2 * i]), y = __builtin_bit_cast(f32x4, rb[2 * i + 1]);
;                 v[0] = pk2bf(x[0], x[1]); v[1] = pk2bf(x[2], x[3]); v[2] = pk2bf(y[0], y[1]); v[3] = pk2bf(y[2], y[3]); }
;             else v = rb[i];
;             *(u32x4*)(lds + GB_OFF + k * GB_ST + bnc * 16) = v; }
;     };
;     const lds_cptr la = (lds_cptr)lds + (wr * 64 + fr) * 64 + fq * 16;
;     const lds_cptr lb = (lds_cptr)lds + GB_OFF + (8 * fq + (fr >> 2) + (fq & 1) * 4) * GB_ST + wc * 128 + (fr & 3) * 8;
;     const int bsw = (fq & 1) ? -4 * GB_ST : 4 * GB_ST;
;     auto compute = [&]() __attribute__((always_inline)) {
; #pragma unroll
;         for (int kh = 0; kh < 2; ++kh) {
;             bf16x8 af[4], bfr[4];
; #pragma unroll
;             for (int m = 0; m < 4; ++m) af[m] = *(const LAS bf16x8*)(la + kh * GA_KH + m * 1024);
; #pragma unroll
;             for (int n = 0; n < 4; ++n) {
;                 const s16x4 r0 = lds_tr(lb + kh * 32 * GB_ST + n * 32), r1 = lds_tr(lb + kh * 32 * GB_ST + n * 32 + bsw);
;                 bfr[n] = (bf16x8){r0[0], r0[1], r0[2], r0[3], r1[0], r1[1], r1[2], r1[3]};
;             }
; #pragma unroll
;             for (int m = 0; m < 4; ++m)
; #pragma unroll
;                 for (int n = 0; n < 4; ++n) acc[m][n] = __builtin_amdgcn_mfma_f32_16x16x32_bf16(bfr[n], af[m], acc[m][n], 0, 0, 0);
;         }
;     };
;     ...
;     gloadB(0, rb0); gloadA(0, ra0); gloadB(1, rb1);
;     for (int kt = 0; kt < nk; kt += 2) {
;         __syncthreads();
;         lstore(ra0, rb0);
;         __syncthreads();
;         gloadA(kt + 1, ra0);
;         if (kt + 2 < nk) gloadB(kt + 2, rb0);
;         compute();
;         __syncthreads();
;         lstore(ra0, rb1);
;         __syncthreads();
;         if (kt + 2 < nk) gloadA(kt + 2, ra0);
;         if (kt + 3 < nk) gloadB(kt + 3, rb1);
;         compute();
;     }
	ds_read_b64_tr_b16 v[166:167], v214 offset:53376
	ds_read_b64_tr_b16 v[168:169], v214 offset:54528
	ds_read_b128 v[116:119], v211 offset:36864
	ds_read_b64_tr_b16 v[170:171], v214 offset:53408
	ds_read_b64_tr_b16 v[172:173], v214 offset:54560
	s_waitcnt lgkmcnt(2)
	v_mfma_f32_16x16x32_bf16 v[72:75], v[166:169], v[116:119], v[72:75]
	ds_read_b64_tr_b16 v[174:175], v214 offset:53440
	ds_read_b64_tr_b16 v[176:177], v214 offset:54592
	s_waitcnt lgkmcnt(2)
	v_mfma_f32_16x16x32_bf16 v[64:67], v[170:173], v[116:119], v[64:67]
	ds_read_b64_tr_b16 v[178:179], v214 offset:53472
	ds_read_b64_tr_b16 v[180:181], v214 offset:54624
	s_waitcnt lgkmcnt(2)
	v_mfma_f32_16x16x32_bf16 v[56:59], v[174:177], v[116:119], v[56:59]
	ds_read_b128 v[120:123], v211 offset:37888
	s_waitcnt lgkmcnt(1)
	v_mfma_f32_16x16x32_bf16 v[52:55], v[178:181], v[116:119], v[52:55]
	ds_read_b128 v[124:127], v211 offset:38912
	s_waitcnt lgkmcnt(1)
	v_mfma_f32_16x16x32_bf16 v[48:51], v[166:169], v[120:123], v[48:51]
	ds_read_b128 v[128:131], v211 offset:39936
	v_mfma_f32_16x16x32_bf16 v[44:47], v[170:173], v[120:123], v[44:47]
	ds_read_b64_tr_b16 v[186:187], v214 offset:62592
	ds_read_b64_tr_b16 v[188:189], v214 offset:63744
	v_mfma_f32_16x16x32_bf16 v[40:43], v[174:177], v[120:123], v[40:43]
	ds_read_b64_tr_b16 v[190:191], v214 offset:62624
	ds_read_b64_tr_b16 v[192:193], v214 offset:63776
	v_mfma_f32_16x16x32_bf16 v[36:39], v[178:181], v[120:123], v[36:39]
	ds_read_b128 v[116:119], v211 offset:45120
	s_waitcnt lgkmcnt(6)
	v_mfma_f32_16x16x32_bf16 v[32:35], v[166:169], v[124:127], v[32:35]
	ds_read_b64_tr_b16 v[194:195], v214 offset:62656
	ds_read_b64_tr_b16 v[196:197], v214 offset:63808
	v_mfma_f32_16x16x32_bf16 v[28:31], v[170:173], v[124:127], v[28:31]
	ds_read_b64_tr_b16 v[198:199], v214 offset:62688
	ds_read_b64_tr_b16 v[200:201], v214 offset:63840
	v_mfma_f32_16x16x32_bf16 v[24:27], v[174:177], v[124:127], v[24:27]
	v_mfma_f32_16x16x32_bf16 v[16:19], v[178:181], v[124:127], v[16:19]
	ds_read_b128 v[120:123], v211 offset:46144
	s_waitcnt lgkmcnt(10)
	v_mfma_f32_16x16x32_bf16 v[8:11], v[166:169], v[128:131], v[8:11]
	v_mfma_f32_16x16x32_bf16 v[4:7], v[170:173], v[128:131], v[4:7]
	v_mfma_f32_16x16x32_bf16 v[20:23], v[174:177], v[128:131], v[20:23]
	v_mfma_f32_16x16x32_bf16 v[12:15], v[178:181], v[128:131], v[12:15]
	ds_read_b128 v[124:127], v211 offset:47168
	s_waitcnt lgkmcnt(6)
	v_mfma_f32_16x16x32_bf16 v[72:75], v[186:189], v[116:119], v[72:75]
	v_mfma_f32_16x16x32_bf16 v[64:67], v[190:193], v[116:119], v[64:67]
	s_waitcnt lgkmcnt(4)
	v_mfma_f32_16x16x32_bf16 v[56:59], v[194:197], v[116:119], v[56:59]
	s_waitcnt lgkmcnt(2)
	v_mfma_f32_16x16x32_bf16 v[52:55], v[198:201], v[116:119], v[52:55]
	ds_read_b128 v[128:131], v211 offset:48192
	s_waitcnt lgkmcnt(2)
	v_mfma_f32_16x16x32_bf16 v[48:51], v[186:189], v[120:123], v[48:51]
	v_mfma_f32_16x16x32_bf16 v[44:47], v[190:193], v[120:123], v[44:47]
	v_mfma_f32_16x16x32_bf16 v[40:43], v[194:197], v[120:123], v[40:43]
	v_mfma_f32_16x16x32_bf16 v[36:39], v[198:201], v[120:123], v[36:39]
	s_waitcnt lgkmcnt(1)
	v_mfma_f32_16x16x32_bf16 v[32:35], v[186:189], v[124:127], v[32:35]
	v_mfma_f32_16x16x32_bf16 v[28:31], v[190:193], v[124:127], v[28:31]
	v_mfma_f32_16x16x32_bf16 v[24:27], v[194:197], v[124:127], v[24:27]
	v_mfma_f32_16x16x32_bf16 v[16:19], v[198:201], v[124:127], v[16:19]
	s_waitcnt lgkmcnt(0)
	v_mfma_f32_16x16x32_bf16 v[8:11], v[186:189], v[128:131], v[8:11]
	v_mfma_f32_16x16x32_bf16 v[4:7], v[190:193], v[128:131], v[4:7]
	v_mfma_f32_16x16x32_bf16 v[20:23], v[194:197], v[128:131], v[20:23]
	v_mfma_f32_16x16x32_bf16 v[12:15], v[198:201], v[128:131], v[12:15]
	s_waitcnt lgkmcnt(0)
	s_barrier

;     ...
;     for (int i = 0; i < 4; ++i) ao[i] = arow((tid >> 3) + 32 * i) + (tid & 7) * 8;
;     const int bk = tid >> 4, bnc = tid & 15;
;     constexpr int NRB = B_F32 ? 8 : 4;
;     u32x4 ra0[4], ra1[4]; u32x4 rb0[NRB], rb1[NRB];
;     auto gloadA = [&](int kt, u32x4 (&ra)[4]) __attribute__((always_inline)) {
; #pragma unroll
;         for (int i = 0; i < 4; ++i) ra[i] = *(const u32x4*)(Abase + (ao[i] + kt * 64));
;     };
;     auto gloadB = [&](int kt, u32x4 (&rb)[NRB]) __attribute__((always_inline)) {
;         if (B_F32) {
;             const float* bp = (const float*)Bbase + (boff + (unsigned)((kt * 64 + bk) * ldb));
; #pragma unroll
;             for (int i = 0; i < 4; ++i) {
;                 if (bval) { rb[2 * i] = *(const u32x4*)(bp + (unsigned)(16 * i * ldb)); rb[2 * i + 1] = *(const u32x4*)(bp + (unsigned)(16 * i * ldb) + 4); }
;                 else { rb[2 * i] = (u32x4){0u, 0u, 0u, 0u}; rb[2 * i + 1] = rb[2 * i]; }
;             }
;         } else {
;             const bf16* bp = (const bf16*)Bbase + (boff + (unsigned)((kt * 64 + bk) * ldb));
; #pragma unroll
;             for (int i = 0; i < 4; ++i) rb[i] = bval ? *(const u32x4*)(bp + (unsigned)(16 * i * ldb)) : (u32x4){0u, 0u, 0u, 0u};
;         }
;     };
;     auto lstore = [&](const u32x4 (&ra)[4], const u32x4 (&rb)[NRB]) __attribute__((always_inline)) {
; #pragma unroll
;         for (int i = 0; i < 4; ++i) { const int row = (tid >> 3) + 32 * i, kc = tid & 7;
;             const u32x4 v = (kc & 1) ? (u32x4){ra[i][2], ra[i][3], ra[i][0], ra[i][1]} : ra[i];
;             *(u32x4*)(lds + (kc >> 2) * GA_KH + row * 64 + (kc & 3) * 16) = v; }
; #pragma unroll
;         for (int i = 0; i < 4; ++i) { const int k = bk + 16 * i;
;             u32x4 v;
;             if (B_F32) { const f32x4 x = __builtin_bit_cast(f32x4, rb[2 * i]), y = __builtin_bit_cast(f32x4, rb[2 * i + 1]);
;                 v[0] = pk2bf(x[0], x[1]); v[1] = pk2bf(x[2], x[3]); v[2] = pk2bf(y[0], y[1]); v[3] = pk2bf(y[2], y[3]); }
;             else v = rb[i];
;             *(u32x4*)(lds + GB_OFF + k * GB_ST + bnc * 16) = v; }
;     };
;     const lds_cptr la = (lds_cptr)lds + (wr * 64 + fr) * 64 + fq * 16;
;     const lds_cptr lb = (lds_cptr)lds + GB_OFF + (8 * fq + (fr >> 2) + (fq & 1) * 4) * GB_ST + wc * 128 + (fr & 3) * 8;
;     const int bsw = (fq & 1) ? -4 * GB_ST : 4 * GB_ST;
.LBB0_544:
	s_andn2_b64 vcc, exec, s[0:1]
	s_cbranch_vccnz .LBB0_533
	s_mul_hi_i32 s0, s60, 0x38e38e39
	s_load_dwordx2 s[42:43], s[4:5], 0x130
	s_lshr_b32 s1, s0, 31
	s_ashr_i32 s0, s0, 2
	s_add_i32 s28, s0, s1
	s_mul_i32 s0, s28, 18
	s_ashr_i32 s29, s28, 31
	s_sub_i32 s17, s60, s0
	s_lshl_b64 s[0:1], s[28:29], 18
	s_waitcnt lgkmcnt(0)
	s_add_u32 s0, s42, s0
	s_addc_u32 s1, s43, s1
	s_add_u32 s44, s0, 0x45c6000
	s_addc_u32 s45, s1, 0
	s_lshl_b32 s61, s17, 7
	s_add_u32 s0, s42, s59
	s_waitcnt vmcnt(0)
	v_lshlrev_b32_e32 v12, 3, v147
	s_addc_u32 s1, s43, s58
	s_add_u32 s46, s0, 0x18095100
	v_lshlrev_b32_e32 v2, 7, v147
	v_and_b32_e32 v4, 56, v12
	s_movk_i32 s0, 0xfc00
	v_and_b32_e32 v155, 15, v147
	v_and_or_b32 v2, v2, s0, v4
	v_lshrrev_b32_e32 v5, 1, v147
	s_mov_b32 s0, 0x3ffffc0
	v_bfe_u32 v157, v147, 4, 2
	v_and_or_b32 v5, v5, s0, v155
	v_bfe_u32 v7, v147, 4, 1
	v_lshlrev_b32_e32 v16, 6, v5
	v_lshlrev_b32_e32 v118, 3, v157
	v_bfe_u32 v5, v147, 2, 2
	v_lshlrev_b32_e32 v9, 2, v7
	v_or3_b32 v5, v9, v5, v118
	v_lshlrev_b32_e32 v9, 1, v147
	v_and_b32_e32 v9, 0x80, v9
	s_movk_i32 s7, 0x120
	v_mad_u32_u24 v5, v5, s7, v9
	v_and_b32_e32 v13, 0x78, v12
	v_add_u32_e32 v4, 0x8000, v2
	v_add_u32_e32 v6, 0x10000, v2
	v_ashrrev_i32_e32 v15, 4, v147
	v_and_or_b32 v119, v12, 24, v5
	v_cmp_eq_u32_e32 vcc, 0, v7
	v_mov_b32_e32 v5, v3
	v_mov_b32_e32 v7, v3
	s_movk_i32 s0, 0x900
	v_or_b32_e32 v14, s61, v13
	v_lshl_add_u64 v[4:5], v[4:5], 1, s[44:45]
	v_lshl_add_u64 v[6:7], v[6:7], 1, s[44:45]
	v_mul_lo_u32 v18, v15, s0
	s_addc_u32 s47, s1, 0
	v_add_u32_e32 v8, 0x18000, v2
	v_mov_b32_e32 v9, v3
	v_add_u32_e32 v6, v14, v18
	v_mov_b32_e32 v7, v3
	v_lshl_add_u64 v[4:5], v[8:9], 1, s[44:45]
	v_lshl_add_u64 v[6:7], v[6:7], 1, s[46:47]
	s_mov_b32 s0, 0x12000
	v_cndmask_b32_e32 v17, v236, v237, vcc
	v_add_co_u32_e32 v4, vcc, s0, v6
	s_mov_b32 s0, 0x24000
	s_nop 0
	v_addc_co_u32_e32 v5, vcc, 0, v7, vcc
	v_add_co_u32_e32 v8, vcc, s0, v6
	s_mov_b32 s0, 0x36000
	s_nop 0
	v_addc_co_u32_e32 v9, vcc, 0, v7, vcc
	v_add_co_u32_e32 v4, vcc, s0, v6
	v_lshl_add_u64 v[10:11], v[2:3], 1, s[44:45]
	s_nop 0
	v_addc_co_u32_e32 v5, vcc, 0, v7, vcc
	v_add_u32_e32 v6, 0x8040, v2
	v_mov_b32_e32 v7, v3
	v_lshl_add_u64 v[6:7], v[6:7], 1, s[44:45]
	v_add_u32_e32 v4, 0x10040, v2
	v_mov_b32_e32 v5, v3
	v_lshl_add_u64 v[4:5], v[4:5], 1, s[44:45]
	v_add_u32_e32 v6, 0x18040, v2
	v_mov_b32_e32 v7, v3
	v_lshl_add_u64 v[6:7], v[6:7], 1, s[44:45]
	v_and_b32_e32 v4, 1, v147
	v_cmp_eq_u32_e64 s[0:1], 0, v4
	v_bfe_i32 v4, v147, 2, 1
	v_and_b32_e32 v4, 0x2040, v4
	v_and_b32_e32 v5, 0xffffffc0, v12
	v_lshl_add_u32 v7, s60, 7, v18
	v_add_u32_e32 v4, v4, v5
	v_lshlrev_b32_e32 v5, 4, v147
	v_mul_lo_u32 v6, v15, s7
	v_or_b32_e32 v7, v7, v13
	s_mul_i32 s7, s28, 0x900
	v_lshlrev_b32_e32 v122, 4, v157
	v_and_b32_e32 v5, 48, v5
	v_lshlrev_b32_e32 v153, 4, v155
	v_subrev_u32_e32 v7, s7, v7
	v_mov_b32_e32 v20, 0
	v_lshrrev_b32_e32 v149, 4, v147
	s_mov_b32 s6, 0
	v_add_u32_e32 v116, 0x48000, v7
	v_add_u32_e32 v120, 0x10080, v2
	v_add_u32_e32 v123, v4, v5
	v_add_u32_e32 v124, v6, v153
	v_add_u32_e32 v125, v16, v122
	v_add_u32_e32 v126, v119, v17
	v_lshlrev_b32_e32 v206, 1, v2
	v_add_u32_e32 v207, 0x10000, v206
	v_add_u32_e32 v208, 0x20000, v206
	v_add_u32_e32 v209, 0x30000, v206
	v_lshlrev_b32_e32 v210, 1, v116
	v_add_u32_e32 v210, 0xfff70000, v210
	v_add_u32_e32 v211, 0x12000, v210
	v_add_u32_e32 v212, 0x24000, v210
	v_add_u32_e32 v213, 0x36000, v210
	v_bfe_u32 v120, v147, 5, 2
	v_sub_u32_e32 v120, 0, v120
	v_and_b32_e32 v120, 3, v120
	v_lshlrev_b32_e32 v120, 4, v120
	v_xor_b32_e32 v215, v123, v120
	v_bfe_u32 v120, v147, 2, 2
	v_sub_u32_e32 v120, 0, v120
	v_and_b32_e32 v120, 3, v120
	v_lshlrev_b32_e32 v120, 4, v120
	v_xor_b32_e32 v216, v125, v120
	v_and_b32_e32 v217, 15, v147
	v_lshlrev_b32_e32 v217, 4, v217
	v_bfe_u32 v120, v147, 7, 1
	v_lshlrev_b32_e32 v120, 7, v120
	v_xor_b32_e32 v217, v217, v120
	v_lshrrev_b32_e32 v120, 4, v147
	v_mul_u32_u24_e32 v120, 0x120, v120
	v_add_u32_e32 v217, v217, v120
	v_add_u32_e32 v214, 0x9000, v217
	v_bfe_u32 v218, v147, 4, 2
	v_lshlrev_b32_e32 v218, 3, v218
	v_bfe_u32 v120, v147, 2, 2
	v_add_u32_e32 v218, v218, v120
	v_mul_u32_u24_e32 v218, 0x120, v218
	v_lshrrev_b32_e32 v120, 6, v147
	v_lshrrev_b32_e32 v121, 4, v147
	v_xor_b32_e32 v120, v120, v121
	v_and_b32_e32 v120, 1, v120
	v_lshlrev_b32_e32 v120, 7, v120
	v_and_b32_e32 v121, 3, v147
	v_lshlrev_b32_e32 v121, 3, v121
	v_or3_b32 v218, v218, v120, v121
	global_load_dwordx4 v[80:83], v206, s[44:45]
	global_load_dwordx4 v[68:71], v207, s[44:45]
	global_load_dwordx4 v[72:75], v208, s[44:45]
	global_load_dwordx4 v[76:79], v209, s[44:45]
	global_load_dwordx4 v[88:91], v210, s[46:47]
	global_load_dwordx4 v[96:99], v211, s[46:47]
	global_load_dwordx4 v[108:111], v212, s[46:47]
	global_load_dwordx4 v[112:115], v213, s[46:47]
	s_add_u32 s46, s46, 0x48000
	s_addc_u32 s47, s47, 0
	global_load_dwordx4 v[84:87], v206, s[44:45] offset:128
	global_load_dwordx4 v[92:95], v207, s[44:45] offset:128
	global_load_dwordx4 v[100:103], v208, s[44:45] offset:128
	global_load_dwordx4 v[104:107], v209, s[44:45] offset:128
	global_load_dwordx4 v[190:193], v210, s[46:47]
	global_load_dwordx4 v[194:197], v211, s[46:47]
	global_load_dwordx4 v[198:201], v212, s[46:47]
	global_load_dwordx4 v[202:205], v213, s[46:47]
	s_add_u32 s46, s46, 0x48000
	s_addc_u32 s47, s47, 0
	v_mov_b32_e32 v21, v20
	v_mov_b32_e32 v22, v20
	v_mov_b32_e32 v23, v20
	v_mov_b32_e32 v32, v20
	v_mov_b32_e32 v33, v20
	v_mov_b32_e32 v34, v20
	v_mov_b32_e32 v35, v20
	v_mov_b32_e32 v4, v20
	v_mov_b32_e32 v5, v20
	v_mov_b32_e32 v6, v20
	v_mov_b32_e32 v7, v20
	v_mov_b32_e32 v8, v20
	v_mov_b32_e32 v9, v20
	v_mov_b32_e32 v10, v20
	v_mov_b32_e32 v11, v20
	v_mov_b32_e32 v12, v20
	v_mov_b32_e32 v13, v20
	v_mov_b32_e32 v14, v20
	v_mov_b32_e32 v15, v20
	v_mov_b32_e32 v16, v20
	v_mov_b32_e32 v17, v20
	v_mov_b32_e32 v18, v20
	v_mov_b32_e32 v19, v20
	v_mov_b32_e32 v24, v20
	v_mov_b32_e32 v25, v20
	v_mov_b32_e32 v26, v20
	v_mov_b32_e32 v27, v20
	v_mov_b32_e32 v28, v20
	v_mov_b32_e32 v29, v20
	v_mov_b32_e32 v30, v20
	v_mov_b32_e32 v31, v20
	v_mov_b32_e32 v36, v20
	v_mov_b32_e32 v37, v20
	v_mov_b32_e32 v38, v20
	v_mov_b32_e32 v39, v20
	v_mov_b32_e32 v40, v20
	v_mov_b32_e32 v41, v20
	v_mov_b32_e32 v42, v20
	v_mov_b32_e32 v43, v20
	v_mov_b32_e32 v44, v20
	v_mov_b32_e32 v45, v20
	v_mov_b32_e32 v46, v20
	v_mov_b32_e32 v47, v20
	v_mov_b32_e32 v48, v20
	v_mov_b32_e32 v49, v20
	v_mov_b32_e32 v50, v20
	v_mov_b32_e32 v51, v20
	v_mov_b32_e32 v52, v20
	v_mov_b32_e32 v53, v20
	v_mov_b32_e32 v54, v20
	v_mov_b32_e32 v55, v20
	v_mov_b32_e32 v56, v20
	v_mov_b32_e32 v57, v20
	v_mov_b32_e32 v58, v20
	v_mov_b32_e32 v59, v20
	v_mov_b32_e32 v60, v20
	v_mov_b32_e32 v61, v20
	v_mov_b32_e32 v62, v20
	v_mov_b32_e32 v63, v20
	v_mov_b32_e32 v64, v20
	v_mov_b32_e32 v65, v20
	v_mov_b32_e32 v66, v20
	v_mov_b32_e32 v67, v20
	s_waitcnt vmcnt(8)
	s_barrier
;     ...
;     auto lstore = [&](const u32x4 (&ra)[4], const u32x4 (&rb)[NRB]) __attribute__((always_inline)) {
; #pragma unroll
;         for (int i = 0; i < 4; ++i) { const int row = (tid >> 3) + 32 * i, kc = tid & 7;
;             const u32x4 v = (kc & 1) ? (u32x4){ra[i][2], ra[i][3], ra[i][0], ra[i][1]} : ra[i];
;             *(u32x4*)(lds + (kc >> 2) * GA_KH + row * 64 + (kc & 3) * 16) = v; }
; #pragma unroll
;         for (int i = 0; i < 4; ++i) { const int k = bk + 16 * i;
;             u32x4 v;
;             if (B_F32) { const f32x4 x = __builtin_bit_cast(f32x4, rb[2 * i]), y = __builtin_bit_cast(f32x4, rb[2 * i + 1]);
;                 v[0] = pk2bf(x[0], x[1]); v[1] = pk2bf(x[2], x[3]); v[2] = pk2bf(y[0], y[1]); v[3] = pk2bf(y[2], y[3]); }
;             else v = rb[i];
;             *(u32x4*)(lds + GB_OFF + k * GB_ST + bnc * 16) = v; }
;     };
;     const lds_cptr la = (lds_cptr)lds + (wr * 64 + fr) * 64 + fq * 16;
;     const lds_cptr lb = (lds_cptr)lds + GB_OFF + (8 * fq + (fr >> 2) + (fq & 1) * 4) * GB_ST + wc * 128 + (fr & 3) * 8;
;     const int bsw = (fq & 1) ? -4 * GB_ST : 4 * GB_ST;
;     auto compute = [&]() __attribute__((always_inline)) {
; #pragma unroll
;         for (int kh = 0; kh < 2; ++kh) {
;             bf16x8 af[4], bfr[4];
; #pragma unroll
;             for (int m = 0; m < 4; ++m) af[m] = *(const LAS bf16x8*)(la + kh * GA_KH + m * 1024);
; #pragma unroll
;             for (int n = 0; n < 4; ++n) {
;                 const s16x4 r0 = lds_tr(lb + kh * 32 * GB_ST + n * 32), r1 = lds_tr(lb + kh * 32 * GB_ST + n * 32 + bsw);
;                 bfr[n] = (bf16x8){r0[0], r0[1], r0[2], r0[3], r1[0], r1[1], r1[2], r1[3]};
;             }
; #pragma unroll
;             for (int m = 0; m < 4; ++m)
; #pragma unroll
;                 for (int n = 0; n < 4; ++n) acc[m][n] = __builtin_amdgcn_mfma_f32_16x16x32_bf16(bfr[n], af[m], acc[m][n], 0, 0, 0);
;         }
;     };
;     ...
;     gloadB(0, rb0); gloadA(0, ra0); gloadB(1, rb1);
;     for (int kt = 0; kt < nk; kt += 2) {
;         __syncthreads();
;         lstore(ra0, rb0);
;         __syncthreads();
;         gloadA(kt + 1, ra0);
;         if (kt + 2 < nk) gloadB(kt + 2, rb0);
;         compute();
;         __syncthreads();
;         lstore(ra0, rb1);
;         __syncthreads();
;         if (kt + 2 < nk) gloadA(kt + 2, ra0);
;         if (kt + 3 < nk) gloadB(kt + 3, rb1);
;         compute();
;     }
	ds_write_b128 v215, v[80:83]
	ds_write_b128 v215, v[68:71] offset:2048
	ds_write_b128 v215, v[72:75] offset:4096
	ds_write_b128 v215, v[76:79] offset:6144
	ds_write_b128 v217, v[88:91] offset:16512
	ds_write_b128 v217, v[96:99] offset:21120
	ds_write_b128 v217, v[108:111] offset:25728
	ds_write_b128 v217, v[112:115] offset:30336
	global_load_dwordx4 v[80:83], v206, s[44:45] offset:256
	global_load_dwordx4 v[68:71], v207, s[44:45] offset:256
	global_load_dwordx4 v[72:75], v208, s[44:45] offset:256
	global_load_dwordx4 v[76:79], v209, s[44:45] offset:256
	global_load_dwordx4 v[88:91], v210, s[46:47]
	global_load_dwordx4 v[96:99], v211, s[46:47]
	global_load_dwordx4 v[108:111], v212, s[46:47]
	global_load_dwordx4 v[112:115], v213, s[46:47]
	s_add_u32 s46, s46, 0x48000
	s_addc_u32 s47, s47, 0
	s_add_u32 s100, s46, 0x48000
	s_addc_u32 s101, s47, 0
	s_waitcnt lgkmcnt(0)
	s_barrier
.Lip_loop:
	ds_read_b64_tr_b16 v[158:159], v218 offset:16512
	ds_read_b64_tr_b16 v[160:161], v218 offset:17664
	ds_read_b128 v[128:131], v216
	ds_read_b64_tr_b16 v[162:163], v218 offset:16544
	ds_read_b64_tr_b16 v[164:165], v218 offset:17696
	s_waitcnt lgkmcnt(2)
	v_mfma_f32_16x16x32_bf16 v[64:67], v[158:161], v[128:131], v[64:67]
	ds_read_b64_tr_b16 v[166:167], v218 offset:16576
	ds_read_b64_tr_b16 v[168:169], v218 offset:17728
	s_waitcnt lgkmcnt(2)
	v_mfma_f32_16x16x32_bf16 v[60:63], v[162:165], v[128:131], v[60:63]
	ds_read_b64_tr_b16 v[170:171], v218 offset:16608
	ds_read_b64_tr_b16 v[172:173], v218 offset:17760
	s_waitcnt lgkmcnt(2)
	v_mfma_f32_16x16x32_bf16 v[56:59], v[166:169], v[128:131], v[56:59]
	ds_read_b128 v[132:135], v216 offset:1024
	s_waitcnt lgkmcnt(1)
	v_mfma_f32_16x16x32_bf16 v[52:55], v[170:173], v[128:131], v[52:55]
	ds_read_b128 v[136:139], v216 offset:2048
	s_waitcnt lgkmcnt(1)
	v_mfma_f32_16x16x32_bf16 v[48:51], v[158:161], v[132:135], v[48:51]
	ds_read_b128 v[140:143], v216 offset:3072
	v_mfma_f32_16x16x32_bf16 v[44:47], v[162:165], v[132:135], v[44:47]
	ds_read_b64_tr_b16 v[174:175], v218 offset:25728
	ds_read_b64_tr_b16 v[176:177], v218 offset:26880
	v_mfma_f32_16x16x32_bf16 v[40:43], v[166:169], v[132:135], v[40:43]
	ds_read_b64_tr_b16 v[178:179], v218 offset:25760
	ds_read_b64_tr_b16 v[180:181], v218 offset:26912
	v_mfma_f32_16x16x32_bf16 v[36:39], v[170:173], v[132:135], v[36:39]
	ds_read_b128 v[128:131], v216 offset:8256
	s_waitcnt lgkmcnt(6)
	v_mfma_f32_16x16x32_bf16 v[28:31], v[158:161], v[136:139], v[28:31]
	ds_read_b64_tr_b16 v[182:183], v218 offset:25792
	ds_read_b64_tr_b16 v[184:185], v218 offset:26944
	v_mfma_f32_16x16x32_bf16 v[24:27], v[162:165], v[136:139], v[24:27]
	ds_read_b64_tr_b16 v[186:187], v218 offset:25824
	ds_read_b64_tr_b16 v[188:189], v218 offset:26976
	v_mfma_f32_16x16x32_bf16 v[16:19], v[166:169], v[136:139], v[16:19]
	s_waitcnt vmcnt(8)
	ds_write_b128 v215, v[84:87] offset:36864
	v_mfma_f32_16x16x32_bf16 v[12:15], v[170:173], v[136:139], v[12:15]
	ds_read_b128 v[132:135], v216 offset:9280
	s_waitcnt lgkmcnt(11)
	v_mfma_f32_16x16x32_bf16 v[8:11], v[158:161], v[140:143], v[8:11]
	ds_write_b128 v215, v[92:95] offset:38912
	v_mfma_f32_16x16x32_bf16 v[4:7], v[162:165], v[140:143], v[4:7]
	ds_write_b128 v215, v[100:103] offset:40960
	v_mfma_f32_16x16x32_bf16 v[32:35], v[166:169], v[140:143], v[32:35]
	ds_write_b128 v215, v[104:107] offset:43008
	v_mfma_f32_16x16x32_bf16 v[20:23], v[170:173], v[140:143], v[20:23]
	s_waitcnt lgkmcnt(10)
	ds_read_b128 v[136:139], v216 offset:10304
	s_waitcnt lgkmcnt(10)
	v_mfma_f32_16x16x32_bf16 v[64:67], v[174:177], v[128:131], v[64:67]
	ds_write_b128 v214, v[190:193] offset:16512
	v_mfma_f32_16x16x32_bf16 v[60:63], v[178:181], v[128:131], v[60:63]
	ds_write_b128 v214, v[194:197] offset:21120
	s_waitcnt lgkmcnt(10)
	v_mfma_f32_16x16x32_bf16 v[56:59], v[182:185], v[128:131], v[56:59]
	ds_write_b128 v214, v[198:201] offset:25728
	s_waitcnt lgkmcnt(9)
	v_mfma_f32_16x16x32_bf16 v[52:55], v[186:189], v[128:131], v[52:55]
	ds_read_b128 v[140:143], v216 offset:11328
	s_waitcnt lgkmcnt(8)
	v_mfma_f32_16x16x32_bf16 v[48:51], v[174:177], v[132:135], v[48:51]
	ds_write_b128 v214, v[202:205] offset:30336
	v_mfma_f32_16x16x32_bf16 v[44:47], v[178:181], v[132:135], v[44:47]
	global_load_dwordx4 v[84:87], v206, s[44:45] offset:384
	v_mfma_f32_16x16x32_bf16 v[40:43], v[182:185], v[132:135], v[40:43]
	global_load_dwordx4 v[92:95], v207, s[44:45] offset:384
	v_mfma_f32_16x16x32_bf16 v[36:39], v[186:189], v[132:135], v[36:39]
	global_load_dwordx4 v[100:103], v208, s[44:45] offset:384
	s_waitcnt lgkmcnt(5)
	v_mfma_f32_16x16x32_bf16 v[28:31], v[174:177], v[136:139], v[28:31]
	global_load_dwordx4 v[104:107], v209, s[44:45] offset:384
	v_mfma_f32_16x16x32_bf16 v[24:27], v[178:181], v[136:139], v[24:27]
	global_load_dwordx4 v[190:193], v210, s[46:47]
	v_mfma_f32_16x16x32_bf16 v[16:19], v[182:185], v[136:139], v[16:19]
	global_load_dwordx4 v[194:197], v211, s[46:47]
	v_mfma_f32_16x16x32_bf16 v[12:15], v[186:189], v[136:139], v[12:15]
	global_load_dwordx4 v[198:201], v212, s[46:47]
	s_waitcnt lgkmcnt(1)
	v_mfma_f32_16x16x32_bf16 v[8:11], v[174:177], v[140:143], v[8:11]
	global_load_dwordx4 v[202:205], v213, s[46:47]
	v_mfma_f32_16x16x32_bf16 v[4:7], v[178:181], v[140:143], v[4:7]
	v_mfma_f32_16x16x32_bf16 v[32:35], v[182:185], v[140:143], v[32:35]
	v_mfma_f32_16x16x32_bf16 v[20:23], v[186:189], v[140:143], v[20:23]
	s_waitcnt lgkmcnt(0)
	s_barrier
	s_cmp_lt_u32 s6, 12
	s_cbranch_scc0 .Lip_h1_last
;     ...
;     auto lstore = [&](const u32x4 (&ra)[4], const u32x4 (&rb)[NRB]) __attribute__((always_inline)) {
; #pragma unroll
;         for (int i = 0; i < 4; ++i) { const int row = (tid >> 3) + 32 * i, kc = tid & 7;
;             const u32x4 v = (kc & 1) ? (u32x4){ra[i][2], ra[i][3], ra[i][0], ra[i][1]} : ra[i];
;             *(u32x4*)(lds + (kc >> 2) * GA_KH + row * 64 + (kc & 3) * 16) = v; }
; #pragma unroll
;         for (int i = 0; i < 4; ++i) { const int k = bk + 16 * i;
;             u32x4 v;
;             if (B_F32) { const f32x4 x = __builtin_bit_cast(f32x4, rb[2 * i]), y = __builtin_bit_cast(f32x4, rb[2 * i + 1]);
;                 v[0] = pk2bf(x[0], x[1]); v[1] = pk2bf(x[2], x[3]); v[2] = pk2bf(y[0], y[1]); v[3] = pk2bf(y[2], y[3]); }
;             else v = rb[i];
;             *(u32x4*)(lds + GB_OFF + k * GB_ST + bnc * 16) = v; }
;     };
;     const lds_cptr la = (lds_cptr)lds + (wr * 64 + fr) * 64 + fq * 16;
;     const lds_cptr lb = (lds_cptr)lds + GB_OFF + (8 * fq + (fr >> 2) + (fq & 1) * 4) * GB_ST + wc * 128 + (fr & 3) * 8;
;     const int bsw = (fq & 1) ? -4 * GB_ST : 4 * GB_ST;
;     auto compute = [&]() __attribute__((always_inline)) {
; #pragma unroll
;         for (int kh = 0; kh < 2; ++kh) {
;             bf16x8 af[4], bfr[4];
; #pragma unroll
;             for (int m = 0; m < 4; ++m) af[m] = *(const LAS bf16x8*)(la + kh * GA_KH + m * 1024);
; #pragma unroll
;             for (int n = 0; n < 4; ++n) {
;                 const s16x4 r0 = lds_tr(lb + kh * 32 * GB_ST + n * 32), r1 = lds_tr(lb + kh * 32 * GB_ST + n * 32 + bsw);
;                 bfr[n] = (bf16x8){r0[0], r0[1], r0[2], r0[3], r1[0], r1[1], r1[2], r1[3]};
;             }
; #pragma unroll
;             for (int m = 0; m < 4; ++m)
; #pragma unroll
;                 for (int n = 0; n < 4; ++n) acc[m][n] = __builtin_amdgcn_mfma_f32_16x16x32_bf16(bfr[n], af[m], acc[m][n], 0, 0, 0);
;         }
;     };
;     ...
;     gloadB(0, rb0); gloadA(0, ra0); gloadB(1, rb1);
;     for (int kt = 0; kt < nk; kt += 2) {
;         __syncthreads();
;         lstore(ra0, rb0);
;         __syncthreads();
;         gloadA(kt + 1, ra0);
;         if (kt + 2 < nk) gloadB(kt + 2, rb0);
;         compute();
;         __syncthreads();
;         lstore(ra0, rb1);
;         __syncthreads();
;         if (kt + 2 < nk) gloadA(kt + 2, ra0);
;         if (kt + 3 < nk) gloadB(kt + 3, rb1);
;         compute();
;     }
	ds_read_b64_tr_b16 v[158:159], v218 offset:53376
	ds_read_b64_tr_b16 v[160:161], v218 offset:54528
	ds_read_b128 v[128:131], v216 offset:36864
	ds_read_b64_tr_b16 v[162:163], v218 offset:53408
	ds_read_b64_tr_b16 v[164:165], v218 offset:54560
	s_waitcnt lgkmcnt(2)
	v_mfma_f32_16x16x32_bf16 v[64:67], v[158:161], v[128:131], v[64:67]
	ds_read_b64_tr_b16 v[166:167], v218 offset:53440
	ds_read_b64_tr_b16 v[168:169], v218 offset:54592
	s_waitcnt lgkmcnt(2)
	v_mfma_f32_16x16x32_bf16 v[60:63], v[162:165], v[128:131], v[60:63]
	ds_read_b64_tr_b16 v[170:171], v218 offset:53472
	ds_read_b64_tr_b16 v[172:173], v218 offset:54624
	s_waitcnt lgkmcnt(2)
	v_mfma_f32_16x16x32_bf16 v[56:59], v[166:169], v[128:131], v[56:59]
	ds_read_b128 v[132:135], v216 offset:37888
	s_waitcnt lgkmcnt(1)
	v_mfma_f32_16x16x32_bf16 v[52:55], v[170:173], v[128:131], v[52:55]
	ds_read_b128 v[136:139], v216 offset:38912
	s_waitcnt lgkmcnt(1)
	v_mfma_f32_16x16x32_bf16 v[48:51], v[158:161], v[132:135], v[48:51]
	ds_read_b128 v[140:143], v216 offset:39936
	v_mfma_f32_16x16x32_bf16 v[44:47], v[162:165], v[132:135], v[44:47]
	ds_read_b64_tr_b16 v[174:175], v218 offset:62592
	ds_read_b64_tr_b16 v[176:177], v218 offset:63744
	v_mfma_f32_16x16x32_bf16 v[40:43], v[166:169], v[132:135], v[40:43]
	ds_read_b64_tr_b16 v[178:179], v218 offset:62624
	ds_read_b64_tr_b16 v[180:181], v218 offset:63776
	v_mfma_f32_16x16x32_bf16 v[36:39], v[170:173], v[132:135], v[36:39]
	ds_read_b128 v[128:131], v216 offset:45120
	s_waitcnt lgkmcnt(6)
	v_mfma_f32_16x16x32_bf16 v[28:31], v[158:161], v[136:139], v[28:31]
	ds_read_b64_tr_b16 v[182:183], v218 offset:62656
	ds_read_b64_tr_b16 v[184:185], v218 offset:63808
	v_mfma_f32_16x16x32_bf16 v[24:27], v[162:165], v[136:139], v[24:27]
	ds_read_b64_tr_b16 v[186:187], v218 offset:62688
	ds_read_b64_tr_b16 v[188:189], v218 offset:63840
	v_mfma_f32_16x16x32_bf16 v[16:19], v[166:169], v[136:139], v[16:19]
	s_waitcnt vmcnt(8)
	ds_write_b128 v215, v[80:83]
	v_mfma_f32_16x16x32_bf16 v[12:15], v[170:173], v[136:139], v[12:15]
	ds_read_b128 v[132:135], v216 offset:46144
	s_waitcnt lgkmcnt(11)
	v_mfma_f32_16x16x32_bf16 v[8:11], v[158:161], v[140:143], v[8:11]
	ds_write_b128 v215, v[68:71] offset:2048
	v_mfma_f32_16x16x32_bf16 v[4:7], v[162:165], v[140:143], v[4:7]
	ds_write_b128 v215, v[72:75] offset:4096
	v_mfma_f32_16x16x32_bf16 v[32:35], v[166:169], v[140:143], v[32:35]
	ds_write_b128 v215, v[76:79] offset:6144
	v_mfma_f32_16x16x32_bf16 v[20:23], v[170:173], v[140:143], v[20:23]
	s_waitcnt lgkmcnt(10)
	ds_read_b128 v[136:139], v216 offset:47168
	s_waitcnt lgkmcnt(10)
	v_mfma_f32_16x16x32_bf16 v[64:67], v[174:177], v[128:131], v[64:67]
	ds_write_b128 v217, v[88:91] offset:16512
	v_mfma_f32_16x16x32_bf16 v[60:63], v[178:181], v[128:131], v[60:63]
	ds_write_b128 v217, v[96:99] offset:21120
	s_waitcnt lgkmcnt(10)
	v_mfma_f32_16x16x32_bf16 v[56:59], v[182:185], v[128:131], v[56:59]
	ds_write_b128 v217, v[108:111] offset:25728
	s_waitcnt lgkmcnt(9)
	v_mfma_f32_16x16x32_bf16 v[52:55], v[186:189], v[128:131], v[52:55]
	ds_read_b128 v[140:143], v216 offset:48192
	s_waitcnt lgkmcnt(8)
	v_mfma_f32_16x16x32_bf16 v[48:51], v[174:177], v[132:135], v[48:51]
	ds_write_b128 v217, v[112:115] offset:30336
	v_mfma_f32_16x16x32_bf16 v[44:47], v[178:181], v[132:135], v[44:47]
	global_load_dwordx4 v[80:83], v206, s[44:45] offset:512
	v_mfma_f32_16x16x32_bf16 v[40:43], v[182:185], v[132:135], v[40:43]
	global_load_dwordx4 v[68:71], v207, s[44:45] offset:512
	v_mfma_f32_16x16x32_bf16 v[36:39], v[186:189], v[132:135], v[36:39]
	global_load_dwordx4 v[72:75], v208, s[44:45] offset:512
	s_waitcnt lgkmcnt(5)
	v_mfma_f32_16x16x32_bf16 v[28:31], v[174:177], v[136:139], v[28:31]
	global_load_dwordx4 v[76:79], v209, s[44:45] offset:512
	v_mfma_f32_16x16x32_bf16 v[24:27], v[178:181], v[136:139], v[24:27]
	global_load_dwordx4 v[88:91], v210, s[100:101]
	v_mfma_f32_16x16x32_bf16 v[16:19], v[182:185], v[136:139], v[16:19]
	global_load_dwordx4 v[96:99], v211, s[100:101]
	v_mfma_f32_16x16x32_bf16 v[12:15], v[186:189], v[136:139], v[12:15]
	global_load_dwordx4 v[108:111], v212, s[100:101]
	s_waitcnt lgkmcnt(1)
	v_mfma_f32_16x16x32_bf16 v[8:11], v[174:177], v[140:143], v[8:11]
	global_load_dwordx4 v[112:115], v213, s[100:101]
	v_mfma_f32_16x16x32_bf16 v[4:7], v[178:181], v[140:143], v[4:7]
	v_mfma_f32_16x16x32_bf16 v[32:35], v[182:185], v[140:143], v[32:35]
	v_mfma_f32_16x16x32_bf16 v[20:23], v[186:189], v[140:143], v[20:23]
	s_waitcnt lgkmcnt(0)
	s_barrier
	s_add_u32 s44, s44, 0x100
	s_addc_u32 s45, s45, 0
	s_add_u32 s46, s46, 0x90000
	s_addc_u32 s47, s47, 0
	s_add_u32 s100, s100, 0x90000
	s_addc_u32 s101, s101, 0
	s_add_i32 s6, s6, 2
	s_branch .Lip_loop
;     ...
;     auto lstore = [&](const u32x4 (&ra)[4], const u32x4 (&rb)[NRB]) __attribute__((always_inline)) {
; #pragma unroll
;         for (int i = 0; i < 4; ++i) { const int row = (tid >> 3) + 32 * i, kc = tid & 7;
;             const u32x4 v = (kc & 1) ? (u32x4){ra[i][2], ra[i][3], ra[i][0], ra[i][1]} : ra[i];
;             *(u32x4*)(lds + (kc >> 2) * GA_KH + row * 64 + (kc & 3) * 16) = v; }
; #pragma unroll
;         for (int i = 0; i < 4; ++i) { const int k = bk + 16 * i;
;             u32x4 v;
;             if (B_F32) { const f32x4 x = __builtin_bit_cast(f32x4, rb[2 * i]), y = __builtin_bit_cast(f32x4, rb[2 * i + 1]);
;                 v[0] = pk2bf(x[0], x[1]); v[1] = pk2bf(x[2], x[3]); v[2] = pk2bf(y[0], y[1]); v[3] = pk2bf(y[2], y[3]); }
;             else v = rb[i];
;             *(u32x4*)(lds + GB_OFF + k * GB_ST + bnc * 16) = v; }
;     };
;     const lds_cptr la = (lds_cptr)lds + (wr * 64 + fr) * 64 + fq * 16;
;     const lds_cptr lb = (lds_cptr)lds + GB_OFF + (8 * fq + (fr >> 2) + (fq & 1) * 4) * GB_ST + wc * 128 + (fr & 3) * 8;
;     const int bsw = (fq & 1) ? -4 * GB_ST : 4 * GB_ST;
;     auto compute = [&]() __attribute__((always_inline)) {
; #pragma unroll
;         for (int kh = 0; kh < 2; ++kh) {
;             bf16x8 af[4], bfr[4];
; #pragma unroll
;             for (int m = 0; m < 4; ++m) af[m] = *(const LAS bf16x8*)(la + kh * GA_KH + m * 1024);
; #pragma unroll
;             for (int n = 0; n < 4; ++n) {
;                 const s16x4 r0 = lds_tr(lb + kh * 32 * GB_ST + n * 32), r1 = lds_tr(lb + kh * 32 * GB_ST + n * 32 + bsw);
;                 bfr[n] = (bf16x8){r0[0], r0[1], r0[2], r0[3], r1[0], r1[1], r1[2], r1[3]};
;             }
; #pragma unroll
;             for (int m = 0; m < 4; ++m)
; #pragma unroll
;                 for (int n = 0; n < 4; ++n) acc[m][n] = __builtin_amdgcn_mfma_f32_16x16x32_bf16(bfr[n], af[m], acc[m][n], 0, 0, 0);
;         }
;     };
;     ...
;     gloadB(0, rb0); gloadA(0, ra0); gloadB(1, rb1);
;     for (int kt = 0; kt < nk; kt += 2) {
;         __syncthreads();
;         lstore(ra0, rb0);
;         __syncthreads();
;         gloadA(kt + 1, ra0);
;         if (kt + 2 < nk) gloadB(kt + 2, rb0);
;         compute();
;         __syncthreads();
;         lstore(ra0, rb1);
;         __syncthreads();
;         if (kt + 2 < nk) gloadA(kt + 2, ra0);
;         if (kt + 3 < nk) gloadB(kt + 3, rb1);
;         compute();
;     }
.Lip_h1_last:
	ds_read_b64_tr_b16 v[158:159], v218 offset:53376
	ds_read_b64_tr_b16 v[160:161], v218 offset:54528
	ds_read_b128 v[128:131], v216 offset:36864
	ds_read_b64_tr_b16 v[162:163], v218 offset:53408
	ds_read_b64_tr_b16 v[164:165], v218 offset:54560
	s_waitcnt lgkmcnt(2)
	v_mfma_f32_16x16x32_bf16 v[64:67], v[158:161], v[128:131], v[64:67]
	ds_read_b64_tr_b16 v[166:167], v218 offset:53440
	ds_read_b64_tr_b16 v[168:169], v218 offset:54592
	s_waitcnt lgkmcnt(2)
	v_mfma_f32_16x16x32_bf16 v[60:63], v[162:165], v[128:131], v[60:63]
	ds_read_b64_tr_b16 v[170:171], v218 offset:53472
	ds_read_b64_tr_b16 v[172:173], v218 offset:54624
	s_waitcnt lgkmcnt(2)
	v_mfma_f32_16x16x32_bf16 v[56:59], v[166:169], v[128:131], v[56:59]
	ds_read_b128 v[132:135], v216 offset:37888
	s_waitcnt lgkmcnt(1)
	v_mfma_f32_16x16x32_bf16 v[52:55], v[170:173], v[128:131], v[52:55]
	ds_read_b128 v[136:139], v216 offset:38912
	s_waitcnt lgkmcnt(1)
	v_mfma_f32_16x16x32_bf16 v[48:51], v[158:161], v[132:135], v[48:51]
	ds_read_b128 v[140:143], v216 offset:39936
	v_mfma_f32_16x16x32_bf16 v[44:47], v[162:165], v[132:135], v[44:47]
	ds_read_b64_tr_b16 v[174:175], v218 offset:62592
	ds_read_b64_tr_b16 v[176:177], v218 offset:63744
	v_mfma_f32_16x16x32_bf16 v[40:43], v[166:169], v[132:135], v[40:43]
	ds_read_b64_tr_b16 v[178:179], v218 offset:62624
	ds_read_b64_tr_b16 v[180:181], v218 offset:63776
	v_mfma_f32_16x16x32_bf16 v[36:39], v[170:173], v[132:135], v[36:39]
	ds_read_b128 v[128:131], v216 offset:45120
	s_waitcnt lgkmcnt(6)
	v_mfma_f32_16x16x32_bf16 v[28:31], v[158:161], v[136:139], v[28:31]
	ds_read_b64_tr_b16 v[182:183], v218 offset:62656
	ds_read_b64_tr_b16 v[184:185], v218 offset:63808
	v_mfma_f32_16x16x32_bf16 v[24:27], v[162:165], v[136:139], v[24:27]
	ds_read_b64_tr_b16 v[186:187], v218 offset:62688
	ds_read_b64_tr_b16 v[188:189], v218 offset:63840
	v_mfma_f32_16x16x32_bf16 v[16:19], v[166:169], v[136:139], v[16:19]
	s_waitcnt vmcnt(8)
	ds_write_b128 v215, v[80:83]
	v_mfma_f32_16x16x32_bf16 v[12:15], v[170:173], v[136:139], v[12:15]
	ds_read_b128 v[132:135], v216 offset:46144
	s_waitcnt lgkmcnt(11)
	v_mfma_f32_16x16x32_bf16 v[8:11], v[158:161], v[140:143], v[8:11]
	ds_write_b128 v215, v[68:71] offset:2048
	v_mfma_f32_16x16x32_bf16 v[4:7], v[162:165], v[140:143], v[4:7]
	ds_write_b128 v215, v[72:75] offset:4096
	v_mfma_f32_16x16x32_bf16 v[32:35], v[166:169], v[140:143], v[32:35]
	ds_write_b128 v215, v[76:79] offset:6144
	v_mfma_f32_16x16x32_bf16 v[20:23], v[170:173], v[140:143], v[20:23]
	s_waitcnt lgkmcnt(10)
	ds_read_b128 v[136:139], v216 offset:47168
	s_waitcnt lgkmcnt(10)
	v_mfma_f32_16x16x32_bf16 v[64:67], v[174:177], v[128:131], v[64:67]
	ds_write_b128 v217, v[88:91] offset:16512
	v_mfma_f32_16x16x32_bf16 v[60:63], v[178:181], v[128:131], v[60:63]
	ds_write_b128 v217, v[96:99] offset:21120
	s_waitcnt lgkmcnt(10)
	v_mfma_f32_16x16x32_bf16 v[56:59], v[182:185], v[128:131], v[56:59]
	ds_write_b128 v217, v[108:111] offset:25728
	s_waitcnt lgkmcnt(9)
	v_mfma_f32_16x16x32_bf16 v[52:55], v[186:189], v[128:131], v[52:55]
	ds_read_b128 v[140:143], v216 offset:48192
	s_waitcnt lgkmcnt(8)
	v_mfma_f32_16x16x32_bf16 v[48:51], v[174:177], v[132:135], v[48:51]
	ds_write_b128 v217, v[112:115] offset:30336
	v_mfma_f32_16x16x32_bf16 v[44:47], v[178:181], v[132:135], v[44:47]
	v_mfma_f32_16x16x32_bf16 v[40:43], v[182:185], v[132:135], v[40:43]
	v_mfma_f32_16x16x32_bf16 v[36:39], v[186:189], v[132:135], v[36:39]
	s_waitcnt lgkmcnt(5)
	v_mfma_f32_16x16x32_bf16 v[28:31], v[174:177], v[136:139], v[28:31]
	v_mfma_f32_16x16x32_bf16 v[24:27], v[178:181], v[136:139], v[24:27]
	v_mfma_f32_16x16x32_bf16 v[16:19], v[182:185], v[136:139], v[16:19]
	v_mfma_f32_16x16x32_bf16 v[12:15], v[186:189], v[136:139], v[12:15]
	s_waitcnt lgkmcnt(1)
	v_mfma_f32_16x16x32_bf16 v[8:11], v[174:177], v[140:143], v[8:11]
	v_mfma_f32_16x16x32_bf16 v[4:7], v[178:181], v[140:143], v[4:7]
	v_mfma_f32_16x16x32_bf16 v[32:35], v[182:185], v[140:143], v[32:35]
	v_mfma_f32_16x16x32_bf16 v[20:23], v[186:189], v[140:143], v[20:23]
	s_waitcnt lgkmcnt(0)
	s_barrier
	ds_read_b64_tr_b16 v[158:159], v218 offset:16512
	ds_read_b64_tr_b16 v[160:161], v218 offset:17664
	ds_read_b128 v[128:131], v216
	ds_read_b64_tr_b16 v[162:163], v218 offset:16544
	ds_read_b64_tr_b16 v[164:165], v218 offset:17696
	s_waitcnt lgkmcnt(2)
	v_mfma_f32_16x16x32_bf16 v[64:67], v[158:161], v[128:131], v[64:67]
	ds_read_b64_tr_b16 v[166:167], v218 offset:16576
	ds_read_b64_tr_b16 v[168:169], v218 offset:17728
	s_waitcnt lgkmcnt(2)
	v_mfma_f32_16x16x32_bf16 v[60:63], v[162:165], v[128:131], v[60:63]
	ds_read_b64_tr_b16 v[170:171], v218 offset:16608
	ds_read_b64_tr_b16 v[172:173], v218 offset:17760
	s_waitcnt lgkmcnt(2)
	v_mfma_f32_16x16x32_bf16 v[56:59], v[166:169], v[128:131], v[56:59]
	ds_read_b128 v[132:135], v216 offset:1024
	s_waitcnt lgkmcnt(1)
	v_mfma_f32_16x16x32_bf16 v[52:55], v[170:173], v[128:131], v[52:55]
	ds_read_b128 v[136:139], v216 offset:2048
	s_waitcnt lgkmcnt(1)
	v_mfma_f32_16x16x32_bf16 v[48:51], v[158:161], v[132:135], v[48:51]
	ds_read_b128 v[140:143], v216 offset:3072
	v_mfma_f32_16x16x32_bf16 v[44:47], v[162:165], v[132:135], v[44:47]
	ds_read_b64_tr_b16 v[174:175], v218 offset:25728
	ds_read_b64_tr_b16 v[176:177], v218 offset:26880
	v_mfma_f32_16x16x32_bf16 v[40:43], v[166:169], v[132:135], v[40:43]
	ds_read_b64_tr_b16 v[178:179], v218 offset:25760
	ds_read_b64_tr_b16 v[180:181], v218 offset:26912
	v_mfma_f32_16x16x32_bf16 v[36:39], v[170:173], v[132:135], v[36:39]
	ds_read_b128 v[128:131], v216 offset:8256
	s_waitcnt lgkmcnt(6)
;     ...
;     auto lstore = [&](const u32x4 (&ra)[4], const u32x4 (&rb)[NRB]) __attribute__((always_inline)) {
; #pragma unroll
;         for (int i = 0; i < 4; ++i) { const int row = (tid >> 3) + 32 * i, kc = tid & 7;
;             const u32x4 v = (kc & 1) ? (u32x4){ra[i][2], ra[i][3], ra[i][0], ra[i][1]} : ra[i];
;             *(u32x4*)(lds + (kc >> 2) * GA_KH + row * 64 + (kc & 3) * 16) = v; }
; #pragma unroll
;         for (int i = 0; i < 4; ++i) { const int k = bk + 16 * i;
;             u32x4 v;
;             if (B_F32) { const f32x4 x = __builtin_bit_cast(f32x4, rb[2 * i]), y = __builtin_bit_cast(f32x4, rb[2 * i + 1]);
;                 v[0] = pk2bf(x[0], x[1]); v[1] = pk2bf(x[2], x[3]); v[2] = pk2bf(y[0], y[1]); v[3] = pk2bf(y[2], y[3]); }
;             else v = rb[i];
;             *(u32x4*)(lds + GB_OFF + k * GB_ST + bnc * 16) = v; }
;     };
;     const lds_cptr la = (lds_cptr)lds + (wr * 64 + fr) * 64 + fq * 16;
;     const lds_cptr lb = (lds_cptr)lds + GB_OFF + (8 * fq + (fr >> 2) + (fq & 1) * 4) * GB_ST + wc * 128 + (fr & 3) * 8;
;     const int bsw = (fq & 1) ? -4 * GB_ST : 4 * GB_ST;
;     auto compute = [&]() __attribute__((always_inline)) {
; #pragma unroll
;         for (int kh = 0; kh < 2; ++kh) {
;             bf16x8 af[4], bfr[4];
; #pragma unroll
;             for (int m = 0; m < 4; ++m) af[m] = *(const LAS bf16x8*)(la + kh * GA_KH + m * 1024);
; #pragma unroll
;             for (int n = 0; n < 4; ++n) {
;                 const s16x4 r0 = lds_tr(lb + kh * 32 * GB_ST + n * 32), r1 = lds_tr(lb + kh * 32 * GB_ST + n * 32 + bsw);
;                 bfr[n] = (bf16x8){r0[0], r0[1], r0[2], r0[3], r1[0], r1[1], r1[2], r1[3]};
;             }
; #pragma unroll
;             for (int m = 0; m < 4; ++m)
; #pragma unroll
;                 for (int n = 0; n < 4; ++n) acc[m][n] = __builtin_amdgcn_mfma_f32_16x16x32_bf16(bfr[n], af[m], acc[m][n], 0, 0, 0);
;         }
;     };
;     ...
;     gloadB(0, rb0); gloadA(0, ra0); gloadB(1, rb1);
;     for (int kt = 0; kt < nk; kt += 2) {
;         __syncthreads();
;         lstore(ra0, rb0);
;         __syncthreads();
;         gloadA(kt + 1, ra0);
;         if (kt + 2 < nk) gloadB(kt + 2, rb0);
;         compute();
;         __syncthreads();
;         lstore(ra0, rb1);
;         __syncthreads();
;         if (kt + 2 < nk) gloadA(kt + 2, ra0);
;         if (kt + 3 < nk) gloadB(kt + 3, rb1);
;         compute();
;     }
	v_mfma_f32_16x16x32_bf16 v[28:31], v[158:161], v[136:139], v[28:31]
	ds_read_b64_tr_b16 v[182:183], v218 offset:25792
	ds_read_b64_tr_b16 v[184:185], v218 offset:26944
	v_mfma_f32_16x16x32_bf16 v[24:27], v[162:165], v[136:139], v[24:27]
	ds_read_b64_tr_b16 v[186:187], v218 offset:25824
	ds_read_b64_tr_b16 v[188:189], v218 offset:26976
	v_mfma_f32_16x16x32_bf16 v[16:19], v[166:169], v[136:139], v[16:19]
	s_waitcnt vmcnt(0)
	ds_write_b128 v215, v[84:87] offset:36864
	v_mfma_f32_16x16x32_bf16 v[12:15], v[170:173], v[136:139], v[12:15]
	ds_read_b128 v[132:135], v216 offset:9280
	s_waitcnt lgkmcnt(11)
	v_mfma_f32_16x16x32_bf16 v[8:11], v[158:161], v[140:143], v[8:11]
	ds_write_b128 v215, v[92:95] offset:38912
	v_mfma_f32_16x16x32_bf16 v[4:7], v[162:165], v[140:143], v[4:7]
	ds_write_b128 v215, v[100:103] offset:40960
	v_mfma_f32_16x16x32_bf16 v[32:35], v[166:169], v[140:143], v[32:35]
	ds_write_b128 v215, v[104:107] offset:43008
	v_mfma_f32_16x16x32_bf16 v[20:23], v[170:173], v[140:143], v[20:23]
	s_waitcnt lgkmcnt(10)
	ds_read_b128 v[136:139], v216 offset:10304
	s_waitcnt lgkmcnt(10)
	v_mfma_f32_16x16x32_bf16 v[64:67], v[174:177], v[128:131], v[64:67]
	ds_write_b128 v214, v[190:193] offset:16512
	v_mfma_f32_16x16x32_bf16 v[60:63], v[178:181], v[128:131], v[60:63]
	ds_write_b128 v214, v[194:197] offset:21120
	s_waitcnt lgkmcnt(10)
	v_mfma_f32_16x16x32_bf16 v[56:59], v[182:185], v[128:131], v[56:59]
	ds_write_b128 v214, v[198:201] offset:25728
	s_waitcnt lgkmcnt(9)
	v_mfma_f32_16x16x32_bf16 v[52:55], v[186:189], v[128:131], v[52:55]
	ds_read_b128 v[140:143], v216 offset:11328
	s_waitcnt lgkmcnt(8)
	v_mfma_f32_16x16x32_bf16 v[48:51], v[174:177], v[132:135], v[48:51]
	ds_write_b128 v214, v[202:205] offset:30336
	v_mfma_f32_16x16x32_bf16 v[44:47], v[178:181], v[132:135], v[44:47]
	v_mfma_f32_16x16x32_bf16 v[40:43], v[182:185], v[132:135], v[40:43]
	v_mfma_f32_16x16x32_bf16 v[36:39], v[186:189], v[132:135], v[36:39]
	s_waitcnt lgkmcnt(5)
	v_mfma_f32_16x16x32_bf16 v[28:31], v[174:177], v[136:139], v[28:31]
	v_mfma_f32_16x16x32_bf16 v[24:27], v[178:181], v[136:139], v[24:27]
	v_mfma_f32_16x16x32_bf16 v[16:19], v[182:185], v[136:139], v[16:19]
	v_mfma_f32_16x16x32_bf16 v[12:15], v[186:189], v[136:139], v[12:15]
	s_waitcnt lgkmcnt(1)
	v_mfma_f32_16x16x32_bf16 v[8:11], v[174:177], v[140:143], v[8:11]
	v_mfma_f32_16x16x32_bf16 v[4:7], v[178:181], v[140:143], v[4:7]
	v_mfma_f32_16x16x32_bf16 v[32:35], v[182:185], v[140:143], v[32:35]
	v_mfma_f32_16x16x32_bf16 v[20:23], v[186:189], v[140:143], v[20:23]
	s_waitcnt lgkmcnt(0)
	s_barrier
	ds_read_b64_tr_b16 v[158:159], v218 offset:53376
	ds_read_b64_tr_b16 v[160:161], v218 offset:54528
	ds_read_b128 v[128:131], v216 offset:36864
	ds_read_b64_tr_b16 v[162:163], v218 offset:53408
	ds_read_b64_tr_b16 v[164:165], v218 offset:54560
	s_waitcnt lgkmcnt(2)
	v_mfma_f32_16x16x32_bf16 v[64:67], v[158:161], v[128:131], v[64:67]
	ds_read_b64_tr_b16 v[166:167], v218 offset:53440
	ds_read_b64_tr_b16 v[168:169], v218 offset:54592
	s_waitcnt lgkmcnt(2)
	v_mfma_f32_16x16x32_bf16 v[60:63], v[162:165], v[128:131], v[60:63]
	ds_read_b64_tr_b16 v[170:171], v218 offset:53472
	ds_read_b64_tr_b16 v[172:173], v218 offset:54624
	s_waitcnt lgkmcnt(2)
	v_mfma_f32_16x16x32_bf16 v[56:59], v[166:169], v[128:131], v[56:59]
	ds_read_b128 v[132:135], v216 offset:37888
	s_waitcnt lgkmcnt(1)
	v_mfma_f32_16x16x32_bf16 v[52:55], v[170:173], v[128:131], v[52:55]
	ds_read_b128 v[136:139], v216 offset:38912
	s_waitcnt lgkmcnt(1)
	v_mfma_f32_16x16x32_bf16 v[48:51], v[158:161], v[132:135], v[48:51]
	ds_read_b128 v[140:143], v216 offset:39936
	v_mfma_f32_16x16x32_bf16 v[44:47], v[162:165], v[132:135], v[44:47]
	ds_read_b64_tr_b16 v[174:175], v218 offset:62592
	ds_read_b64_tr_b16 v[176:177], v218 offset:63744
	v_mfma_f32_16x16x32_bf16 v[40:43], v[166:169], v[132:135], v[40:43]
	ds_read_b64_tr_b16 v[178:179], v218 offset:62624
	ds_read_b64_tr_b16 v[180:181], v218 offset:63776
	v_mfma_f32_16x16x32_bf16 v[36:39], v[170:173], v[132:135], v[36:39]
	ds_read_b128 v[128:131], v216 offset:45120
	s_waitcnt lgkmcnt(6)
	v_mfma_f32_16x16x32_bf16 v[28:31], v[158:161], v[136:139], v[28:31]
	ds_read_b64_tr_b16 v[182:183], v218 offset:62656
	ds_read_b64_tr_b16 v[184:185], v218 offset:63808
	v_mfma_f32_16x16x32_bf16 v[24:27], v[162:165], v[136:139], v[24:27]
	ds_read_b64_tr_b16 v[186:187], v218 offset:62688
	ds_read_b64_tr_b16 v[188:189], v218 offset:63840
	v_mfma_f32_16x16x32_bf16 v[16:19], v[166:169], v[136:139], v[16:19]
	v_mfma_f32_16x16x32_bf16 v[12:15], v[170:173], v[136:139], v[12:15]
	ds_read_b128 v[132:135], v216 offset:46144
	s_waitcnt lgkmcnt(10)
	v_mfma_f32_16x16x32_bf16 v[8:11], v[158:161], v[140:143], v[8:11]
	v_mfma_f32_16x16x32_bf16 v[4:7], v[162:165], v[140:143], v[4:7]
	v_mfma_f32_16x16x32_bf16 v[32:35], v[166:169], v[140:143], v[32:35]
	v_mfma_f32_16x16x32_bf16 v[20:23], v[170:173], v[140:143], v[20:23]
	ds_read_b128 v[136:139], v216 offset:47168
	s_waitcnt lgkmcnt(6)
	v_mfma_f32_16x16x32_bf16 v[64:67], v[174:177], v[128:131], v[64:67]
	v_mfma_f32_16x16x32_bf16 v[60:63], v[178:181], v[128:131], v[60:63]
	s_waitcnt lgkmcnt(4)
	v_mfma_f32_16x16x32_bf16 v[56:59], v[182:185], v[128:131], v[56:59]
	s_waitcnt lgkmcnt(2)
	v_mfma_f32_16x16x32_bf16 v[52:55], v[186:189], v[128:131], v[52:55]
	ds_read_b128 v[140:143], v216 offset:48192
	s_waitcnt lgkmcnt(2)
	v_mfma_f32_16x16x32_bf16 v[48:51], v[174:177], v[132:135], v[48:51]
	v_mfma_f32_16x16x32_bf16 v[44:47], v[178:181], v[132:135], v[44:47]
	v_mfma_f32_16x16x32_bf16 v[40:43], v[182:185], v[132:135], v[40:43]
	v_mfma_f32_16x16x32_bf16 v[36:39], v[186:189], v[132:135], v[36:39]
	s_waitcnt lgkmcnt(1)
	v_mfma_f32_16x16x32_bf16 v[28:31], v[174:177], v[136:139], v[28:31]
	v_mfma_f32_16x16x32_bf16 v[24:27], v[178:181], v[136:139], v[24:27]
	v_mfma_f32_16x16x32_bf16 v[16:19], v[182:185], v[136:139], v[16:19]
	v_mfma_f32_16x16x32_bf16 v[12:15], v[186:189], v[136:139], v[12:15]
	s_waitcnt lgkmcnt(0)
	v_mfma_f32_16x16x32_bf16 v[8:11], v[174:177], v[140:143], v[8:11]
	v_mfma_f32_16x16x32_bf16 v[4:7], v[178:181], v[140:143], v[4:7]
	v_mfma_f32_16x16x32_bf16 v[32:35], v[182:185], v[140:143], v[32:35]
	v_mfma_f32_16x16x32_bf16 v[20:23], v[186:189], v[140:143], v[20:23]
	s_waitcnt lgkmcnt(0)
	s_barrier
